# P0 weight transposes: global loads, hoisted mid-load wait removed (one round trip per 64x64 item), counted vmcnt
# speedup vs baseline: 1.0077x; 1.0025x over previous
; #define LAS __attribute__((address_space(3)))
; #define AIN(i) ((const float*)ldp(lds, (i)))
;     const int nblk = N / 64, kb = item / nblk, nb = item % nblk, k0 = 64 * kb, n0 = 64 * nb;
;     const int kr = lane >> 4, nc = (lane & 15) * 4;
;     const float* src = W + (size_t)(k0 + kr) * N + n0 + nc;
;     f32x4 v[16];
; #pragma unroll
;     for (int i = 0; i < 16; ++i) v[i] = __builtin_nontemporal_load((const f32x4*)(src + (size_t)(4 * i) * N));
; #pragma unroll
;     for (int i = 0; i < 16; ++i) { LAS float* d = scr + (4 * i + kr) * 65 + nc; d[0] = v[i].x * W8_SCALE; d[1] = v[i].y * W8_SCALE; d[2] = v[i].z * W8_SCALE; d[3] = v[i].w * W8_SCALE; }
; __device__ __forceinline__ void ph0(LAS unsigned char* lds, int tid, int lane, int wave, int G, int bid) {
;     ...
;             int r = NITEMS - 1 - it;
;             if (r < I_IN) { transpose_item_f8<0>(AIN(IWIN), D, INW, (unsigned char*)(ws + WS_WG8), scr, r, lane, -1); continue; } r -= I_IN;
;             if (r < I_IN2) { transpose_item<0>(AIN(IWIN), D, INW, (bf16*)(ws + WS_WINT), scr, (r >> 3) * 88 + 16 + (r & 7), lane); continue; } r -= I_IN2;
;             if (r < I_F) { transpose_item_f8<0>(AIN(IWF), FW, D, (unsigned char*)(ws + WS_WFT) + ((size_t)(SW / 128) << 15), scr, r, lane, -(SW + FW) / 128); continue; } r -= I_F;
;             if (r < I_S) { transpose_item_f8<0>(AIN(IWS), SW, D, (unsigned char*)(ws + WS_WFT), scr, r, lane, -(SW + FW) / 128); continue; } r -= I_S;
;             if (r < I_O) { transpose_item_f8<0>(AIN(IWOUT), D, D, (unsigned char*)(ws + WS_WOT), scr, r, lane, -1); continue; } r -= I_O;
;             if (r < I_G) { transpose_item<0>(AIN(IWGLU), SW, SW, (bf16*)(ws + WS_WGLUT), scr, r, lane); continue; } r -= I_G;
;             if (r < NE * I_E) { const int e = r >> 9; transpose_item_f8<1>(AIN(IW1) + (size_t)e * D * DE, D, DE, (unsigned char*)(ws + WS_W13T) + (size_t)e * 2048 * D, scr, r & 511, lane, -1); continue; } r -= NE * I_E;
;             if (r < NE * I_E) { const int e = r >> 9; transpose_item_f8<2>(AIN(IW3) + (size_t)e * D * DE, D, DE, (unsigned char*)(ws + WS_W13T) + (size_t)e * 2048 * D, scr, r & 511, lane, -1); continue; } r -= NE * I_E;
;             { const int e = r >> 9; transpose_item_f8<0>(AIN(IW2) + (size_t)e * DE * D, DE, D, (unsigned char*)(ws + WS_W2T) + (size_t)e * D * DE, scr, r & 511, lane, -1); }
.LBB0_114:
	s_cmp_lt_i32 s9, 0xc840
	s_mov_b64 s[10:11], -1
	s_cbranch_scc0 .LBB0_144
	s_cmpk_gt_i32 s23, 0xff
	s_cbranch_scc0 .LBB0_141
	s_add_i32 s92, s23, 0xffffff00
	s_cmpk_gt_i32 s92, 0x1ff
	s_cbranch_scc0 .LBB0_138
	s_add_i32 s93, s23, 0xfffffd00
	s_cmpk_gt_i32 s93, 0xff
	s_cbranch_scc0 .LBB0_135
	s_add_i32 s94, s23, 0xfffffc00
	s_cmpk_gt_i32 s94, 0x3ff
	s_cbranch_scc0 .LBB0_132
	s_add_i32 s95, s23, 0xfffff800
	s_cmp_gt_i32 s95, 63
	s_cbranch_scc0 .LBB0_129
	s_add_i32 s96, s23, 0xfffff7c0
	s_cmpk_gt_i32 s96, 0x3fff
	s_cbranch_scc0 .LBB0_126
	s_add_i32 s97, s23, 0xffffb7c0
	s_cmpk_gt_i32 s97, 0x3fff
	s_cbranch_scc0 .LBB0_123
	v_mov_b32_e32 v2, s26
	ds_read_b32 v2, v2
	v_mov_b32_e32 v9, s27
	ds_read_b32 v9, v9
	s_add_i32 s10, s23, 0xffff77c0
	s_lshr_b32 s0, s10, 9
	s_waitcnt lgkmcnt(0)
	v_readfirstlane_b32 s11, v2
	s_lshl_b64 vcc, s[0:1], 23
	v_readfirstlane_b32 s60, v9
	s_add_u32 vcc_lo, s11, vcc_lo
	s_addc_u32 vcc_hi, s60, vcc_hi
	s_lshl_b64 s[60:61], s[0:1], 21
	s_add_u32 s11, s17, s60
	s_addc_u32 s65, s18, s61
	s_bfe_u32 s0, s10, 0x40005
	s_lshl_b32 s60, s0, 6
	s_lshl_b32 s0, s10, 6
	v_or_b32_e32 v2, s60, v10
	s_and_b32 s63, s0, 0x7c0
	v_lshlrev_b32_e32 v2, 13, v2
	v_lshl_add_u64 v[62:63], vcc, 0, v[2:3]
	s_lshl_b32 s0, s63, 2
	v_lshl_add_u64 v[62:63], v[62:63], 0, s[0:1]
	v_mov_b32_e32 v9, v3
	v_lshl_add_u64 v[122:123], v[62:63], 0, v[8:9]
	v_add_co_u32_e32 v66, vcc, s28, v122
	s_lshr_b32 s0, s10, 5
	s_nop 0
	v_addc_co_u32_e32 v67, vcc, 0, v123, vcc
	global_load_dwordx4 v[62:65], v[122:123], off nt
	s_nop 0
	global_load_dwordx4 v[66:69], v[66:67], off nt
	v_add_co_u32_e32 v70, vcc, s29, v122
	s_lshl_b32 s10, s10, 1
	s_nop 0
	v_addc_co_u32_e32 v71, vcc, 0, v123, vcc
	v_add_co_u32_e32 v74, vcc, s30, v122
	s_bfe_u32 s0, s0, 0x30001
	s_nop 0
	v_addc_co_u32_e32 v75, vcc, 0, v123, vcc
	global_load_dwordx4 v[70:73], v[70:71], off nt
	s_nop 0
	global_load_dwordx4 v[74:77], v[74:75], off nt
	v_add_co_u32_e32 v78, vcc, s31, v122
	s_and_b32 s10, s10, 56
	s_nop 0
	v_addc_co_u32_e32 v79, vcc, 0, v123, vcc
	v_add_co_u32_e32 v82, vcc, s40, v122
	s_or_b32 s0, s10, s0
	s_nop 0
	v_addc_co_u32_e32 v83, vcc, 0, v123, vcc
	global_load_dwordx4 v[78:81], v[78:79], off nt
	s_nop 0
	global_load_dwordx4 v[82:85], v[82:83], off nt
	v_add_co_u32_e32 v86, vcc, s41, v122
	s_lshl_b32 s0, s0, 15
	s_nop 0
	v_addc_co_u32_e32 v87, vcc, 0, v123, vcc
	v_add_co_u32_e32 v90, vcc, s42, v122
	s_add_u32 s10, s11, s0
	s_nop 0
	v_addc_co_u32_e32 v91, vcc, 0, v123, vcc
	global_load_dwordx4 v[86:89], v[86:87], off nt
	s_nop 0
	global_load_dwordx4 v[90:93], v[90:91], off nt
	v_add_co_u32_e32 v94, vcc, s43, v122
	s_addc_u32 s11, s65, 0
	s_nop 0
	v_addc_co_u32_e32 v95, vcc, 0, v123, vcc
	v_add_co_u32_e32 v98, vcc, s44, v122
	v_and_or_b32 v2, s60, 64, v13
	s_nop 0
	v_addc_co_u32_e32 v99, vcc, 0, v123, vcc
	global_load_dwordx4 v[94:97], v[94:95], off nt
	s_nop 0
	global_load_dwordx4 v[98:101], v[98:99], off nt
	v_add_co_u32_e32 v102, vcc, s45, v122
	s_movk_i32 s65, 0x4000
	s_nop 0
	v_addc_co_u32_e32 v103, vcc, 0, v123, vcc
	v_add_co_u32_e32 v106, vcc, s46, v122
	s_nop 1
	v_addc_co_u32_e32 v107, vcc, 0, v123, vcc
	global_load_dwordx4 v[102:105], v[102:103], off nt
	s_nop 0
	global_load_dwordx4 v[106:109], v[106:107], off nt
	v_add_co_u32_e32 v110, vcc, s47, v122
	s_nop 1
	v_addc_co_u32_e32 v111, vcc, 0, v123, vcc
	global_load_dwordx4 v[110:113], v[110:111], off nt
	v_add_co_u32_e32 v114, vcc, s48, v122
	s_nop 1
	v_addc_co_u32_e32 v115, vcc, 0, v123, vcc
	global_load_dwordx4 v[114:117], v[114:115], off nt
	v_add_co_u32_e32 v118, vcc, s49, v122
	s_nop 1
	v_addc_co_u32_e32 v119, vcc, 0, v123, vcc
	global_load_dwordx4 v[118:121], v[118:119], off nt
	v_add_co_u32_e32 v122, vcc, s50, v122
	s_nop 1
	v_addc_co_u32_e32 v123, vcc, 0, v123, vcc
	global_load_dwordx4 v[122:125], v[122:123], off nt
	s_waitcnt vmcnt(15)
	v_pk_mul_f32 v[62:63], v[62:63], s[8:9] op_sel_hi:[1,0]
	ds_write2_b32 v11, v62, v63 offset1:1
	v_pk_mul_f32 v[62:63], v[64:65], s[8:9] op_sel_hi:[1,0]
	ds_write2_b32 v11, v62, v63 offset0:2 offset1:3
	s_waitcnt vmcnt(14)
	v_pk_mul_f32 v[62:63], v[66:67], s[8:9] op_sel_hi:[1,0]
	ds_write2_b32 v27, v62, v63 offset1:1
	v_pk_mul_f32 v[62:63], v[68:69], s[8:9] op_sel_hi:[1,0]
	ds_write2_b32 v28, v62, v63 offset1:1
	s_waitcnt vmcnt(13)
	v_pk_mul_f32 v[62:63], v[70:71], s[8:9] op_sel_hi:[1,0]
	ds_write2_b32 v29, v62, v63 offset1:1
	v_pk_mul_f32 v[62:63], v[72:73], s[8:9] op_sel_hi:[1,0]
	ds_write2_b32 v30, v62, v63 offset1:1
	s_waitcnt vmcnt(12)
	v_pk_mul_f32 v[62:63], v[74:75], s[8:9] op_sel_hi:[1,0]
	ds_write2_b32 v31, v62, v63 offset1:1
	v_pk_mul_f32 v[62:63], v[76:77], s[8:9] op_sel_hi:[1,0]
	ds_write2_b32 v32, v62, v63 offset1:1
	s_waitcnt vmcnt(11)
	v_pk_mul_f32 v[62:63], v[78:79], s[8:9] op_sel_hi:[1,0]
	ds_write2_b32 v33, v62, v63 offset1:1
	v_pk_mul_f32 v[62:63], v[80:81], s[8:9] op_sel_hi:[1,0]
	ds_write2_b32 v34, v62, v63 offset1:1
	s_waitcnt vmcnt(10)
	v_pk_mul_f32 v[62:63], v[82:83], s[8:9] op_sel_hi:[1,0]
	ds_write2_b32 v35, v62, v63 offset1:1
	v_pk_mul_f32 v[62:63], v[84:85], s[8:9] op_sel_hi:[1,0]
	ds_write2_b32 v36, v62, v63 offset1:1
	s_waitcnt vmcnt(9)
	v_pk_mul_f32 v[62:63], v[86:87], s[8:9] op_sel_hi:[1,0]
	ds_write2_b32 v37, v62, v63 offset1:1
	v_pk_mul_f32 v[62:63], v[88:89], s[8:9] op_sel_hi:[1,0]
	ds_write2_b32 v38, v62, v63 offset1:1
	s_waitcnt vmcnt(8)
	v_pk_mul_f32 v[62:63], v[90:91], s[8:9] op_sel_hi:[1,0]
	ds_write2_b32 v39, v62, v63 offset1:1
	v_pk_mul_f32 v[62:63], v[92:93], s[8:9] op_sel_hi:[1,0]
	ds_write2_b32 v40, v62, v63 offset1:1
	s_waitcnt vmcnt(7)
; #define LAS __attribute__((address_space(3)))
; __device__ __forceinline__ unsigned pk4_fp8(float a, float b, float c, float d) { int w = 0; w = __builtin_amdgcn_cvt_pk_fp8_f32(clamp8(a), clamp8(b), w, false); w = __builtin_amdgcn_cvt_pk_fp8_f32(clamp8(c), clamp8(d), w, true); return (unsigned)w; }
; #define LDS_WAIT() asm volatile("s_waitcnt lgkmcnt(0)" ::: "memory")
; __host__ __device__ __forceinline__ size_t tiled_off(size_t r, int kb, int ktiles) { return (((r >> 8) * ktiles + (kb >> 7)) << 15) + ((r & 255) << 7) + (kb & 127); }
;     ...
;     for (int i = 0; i < 16; ++i) v[i] = __builtin_nontemporal_load((const f32x4*)(src + (size_t)(4 * i) * N));
; #pragma unroll
;     for (int i = 0; i < 16; ++i) { LAS float* d = scr + (4 * i + kr) * 65 + nc; d[0] = v[i].x * W8_SCALE; d[1] = v[i].y * W8_SCALE; d[2] = v[i].z * W8_SCALE; d[3] = v[i].w * W8_SCALE; }
;     LDS_WAIT(); asm volatile("" ::: "memory");
;     const int c = lane & 3;
; #pragma unroll
;     for (int j = 0; j < 4; ++j) { const int n = (lane >> 2) + 16 * j; const LAS float* s = scr + (16 * c) * 65 + n;
;         u32x4 o; o.x = pk4_fp8(s[0 * 65], s[1 * 65], s[2 * 65], s[3 * 65]); o.y = pk4_fp8(s[4 * 65], s[5 * 65], s[6 * 65], s[7 * 65]);
;         o.z = pk4_fp8(s[8 * 65], s[9 * 65], s[10 * 65], s[11 * 65]); o.w = pk4_fp8(s[12 * 65], s[13 * 65], s[14 * 65], s[15 * 65]);
;         const int nn = n0 + n; const int row = MAP == 0 ? nn : ((nn >> 7) * 256 + (nn & 127) + (MAP == 2 ? 128 : 0));
;         __builtin_nontemporal_store(o, (u32x4*)(WT + (pitch < 0 ? tiled_off((size_t)row, k0 + 16 * c, pitch == -1 ? (K >> 7) : -pitch) : (size_t)row * (pitch ? pitch : K) + k0 + 16 * c))); }
;     LDS_WAIT(); asm volatile("" ::: "memory");
	v_pk_mul_f32 v[62:63], v[94:95], s[8:9] op_sel_hi:[1,0]
	ds_write2_b32 v41, v62, v63 offset1:1
	v_pk_mul_f32 v[62:63], v[96:97], s[8:9] op_sel_hi:[1,0]
	ds_write2_b32 v42, v62, v63 offset1:1
	s_waitcnt vmcnt(6)
	v_pk_mul_f32 v[62:63], v[98:99], s[8:9] op_sel_hi:[1,0]
	ds_write2_b32 v43, v62, v63 offset1:1
	v_pk_mul_f32 v[62:63], v[100:101], s[8:9] op_sel_hi:[1,0]
	ds_write2_b32 v44, v62, v63 offset1:1
	s_waitcnt vmcnt(0) lgkmcnt(0)
	v_pk_mul_f32 v[62:63], v[102:103], s[8:9] op_sel_hi:[1,0]
	ds_write2_b32 v45, v62, v63 offset1:1
	v_pk_mul_f32 v[62:63], v[104:105], s[8:9] op_sel_hi:[1,0]
	ds_write2_b32 v46, v62, v63 offset1:1
	v_pk_mul_f32 v[62:63], v[106:107], s[8:9] op_sel_hi:[1,0]
	ds_write2_b32 v47, v62, v63 offset1:1
	v_pk_mul_f32 v[62:63], v[108:109], s[8:9] op_sel_hi:[1,0]
	ds_write2_b32 v48, v62, v63 offset1:1
	v_pk_mul_f32 v[62:63], v[110:111], s[8:9] op_sel_hi:[1,0]
	ds_write2_b32 v49, v62, v63 offset1:1
	v_pk_mul_f32 v[62:63], v[112:113], s[8:9] op_sel_hi:[1,0]
	ds_write2_b32 v50, v62, v63 offset1:1
	v_pk_mul_f32 v[62:63], v[114:115], s[8:9] op_sel_hi:[1,0]
	ds_write2_b32 v51, v62, v63 offset1:1
	v_pk_mul_f32 v[62:63], v[116:117], s[8:9] op_sel_hi:[1,0]
	ds_write2_b32 v52, v62, v63 offset1:1
	v_pk_mul_f32 v[62:63], v[118:119], s[8:9] op_sel_hi:[1,0]
	ds_write2_b32 v53, v62, v63 offset1:1
	v_pk_mul_f32 v[62:63], v[120:121], s[8:9] op_sel_hi:[1,0]
	ds_write2_b32 v54, v62, v63 offset1:1
	v_pk_mul_f32 v[62:63], v[122:123], s[8:9] op_sel_hi:[1,0]
	ds_write2_b32 v55, v62, v63 offset1:1
	v_pk_mul_f32 v[62:63], v[124:125], s[8:9] op_sel_hi:[1,0]
	ds_write2_b32 v56, v62, v63 offset1:1
	s_waitcnt lgkmcnt(0)
	ds_read_b32 v9, v14
	ds_read_b32 v62, v14 offset:260
	ds_read_b32 v63, v14 offset:520
	ds_read_b32 v64, v14 offset:780
	ds_read_b32 v65, v14 offset:1040
	ds_read_b32 v66, v14 offset:1300
	ds_read_b32 v67, v14 offset:1560
	ds_read_b32 v68, v14 offset:1820
	s_waitcnt lgkmcnt(7)
	v_med3_f32 v9, v9, s51, v57
	s_waitcnt lgkmcnt(6)
	v_med3_f32 v69, v62, s51, v57
	v_mov_b32_e32 v62, v3
	v_cvt_pk_fp8_f32 v62, v9, v69
	s_waitcnt lgkmcnt(5)
	v_med3_f32 v9, v63, s51, v57
	s_waitcnt lgkmcnt(3)
	v_med3_f32 v65, v65, s51, v57
	s_waitcnt lgkmcnt(2)
	v_med3_f32 v66, v66, s51, v57
	v_mov_b32_e32 v63, v3
	v_cvt_pk_fp8_f32 v63, v65, v66
	v_med3_f32 v64, v64, s51, v57
	v_cvt_pk_fp8_f32 v62, v9, v64 op_sel:[0,0,1]
	s_waitcnt lgkmcnt(1)
	v_med3_f32 v9, v67, s51, v57
	s_waitcnt lgkmcnt(0)
	v_med3_f32 v64, v68, s51, v57
	v_cvt_pk_fp8_f32 v63, v9, v64 op_sel:[0,0,1]
	ds_read_b32 v9, v14 offset:2080
	ds_read_b32 v64, v14 offset:2340
	ds_read_b32 v65, v14 offset:2600
	ds_read_b32 v66, v14 offset:2860
	ds_read_b32 v67, v14 offset:3120
	ds_read_b32 v68, v14 offset:3380
	ds_read_b32 v69, v14 offset:3640
	ds_read_b32 v70, v14 offset:3900
	s_waitcnt lgkmcnt(7)
	v_med3_f32 v9, v9, s51, v57
	s_waitcnt lgkmcnt(6)
	v_med3_f32 v71, v64, s51, v57
	v_mov_b32_e32 v64, v3
	v_cvt_pk_fp8_f32 v64, v9, v71
	s_waitcnt lgkmcnt(5)
	v_med3_f32 v9, v65, s51, v57
	s_waitcnt lgkmcnt(3)
	v_med3_f32 v67, v67, s51, v57
	s_waitcnt lgkmcnt(2)
	v_med3_f32 v68, v68, s51, v57
	v_mov_b32_e32 v65, v3
	v_cvt_pk_fp8_f32 v65, v67, v68
	v_med3_f32 v66, v66, s51, v57
	v_cvt_pk_fp8_f32 v64, v9, v66 op_sel:[0,0,1]
	s_waitcnt lgkmcnt(1)
	v_med3_f32 v9, v69, s51, v57
	s_waitcnt lgkmcnt(0)
	v_med3_f32 v66, v70, s51, v57
	v_cvt_pk_fp8_f32 v65, v9, v66 op_sel:[0,0,1]
	v_or_b32_e32 v9, s63, v12
	v_lshlrev_b32_e32 v9, 7, v9
	v_and_b32_e32 v66, 0x6780, v9
	v_mov_b32_e32 v67, v3
	v_lshl_add_u64 v[66:67], s[10:11], 0, v[66:67]
	v_lshl_add_u64 v[66:67], v[66:67], 0, v[2:3]
	global_store_dwordx4 v[66:67], v[62:65], off nt
	ds_read_b32 v9, v14 offset:64
	ds_read_b32 v62, v14 offset:324
	ds_read_b32 v63, v14 offset:584
	ds_read_b32 v64, v14 offset:844
	ds_read_b32 v65, v14 offset:1104
	ds_read_b32 v66, v14 offset:1364
	ds_read_b32 v67, v14 offset:1624
	ds_read_b32 v68, v14 offset:1884
	s_waitcnt lgkmcnt(0)
	v_med3_f32 v9, v9, s51, v57
	v_med3_f32 v69, v62, s51, v57
	v_mov_b32_e32 v62, v3
	v_cvt_pk_fp8_f32 v62, v9, v69
	v_med3_f32 v9, v63, s51, v57
	v_med3_f32 v65, v65, s51, v57
	v_med3_f32 v66, v66, s51, v57
	v_mov_b32_e32 v63, v3
	v_cvt_pk_fp8_f32 v63, v65, v66
	v_med3_f32 v64, v64, s51, v57
	v_cvt_pk_fp8_f32 v62, v9, v64 op_sel:[0,0,1]
	v_med3_f32 v9, v67, s51, v57
	v_med3_f32 v64, v68, s51, v57
	v_cvt_pk_fp8_f32 v63, v9, v64 op_sel:[0,0,1]
	ds_read_b32 v9, v14 offset:2144
	ds_read_b32 v64, v14 offset:2404
	ds_read_b32 v65, v14 offset:2664
	ds_read_b32 v66, v14 offset:2924
	ds_read_b32 v67, v14 offset:3184
	ds_read_b32 v68, v14 offset:3444
	ds_read_b32 v69, v14 offset:3704
	ds_read_b32 v70, v14 offset:3964
	s_waitcnt lgkmcnt(0)
	v_med3_f32 v9, v9, s51, v57
	v_med3_f32 v71, v64, s51, v57
	v_mov_b32_e32 v64, v3
	v_cvt_pk_fp8_f32 v64, v9, v71
	v_med3_f32 v9, v65, s51, v57
	v_med3_f32 v67, v67, s51, v57
	v_med3_f32 v68, v68, s51, v57
	v_mov_b32_e32 v65, v3
	v_cvt_pk_fp8_f32 v65, v67, v68
	v_med3_f32 v66, v66, s51, v57
	v_cvt_pk_fp8_f32 v64, v9, v66 op_sel:[0,0,1]
	v_med3_f32 v9, v69, s51, v57
	v_med3_f32 v66, v70, s51, v57
	v_cvt_pk_fp8_f32 v65, v9, v66 op_sel:[0,0,1]
	v_or_b32_e32 v9, s63, v15
	v_lshlrev_b32_e32 v9, 7, v9
	v_and_b32_e32 v66, 0x6f80, v9
	v_mov_b32_e32 v67, v3
	v_lshl_add_u64 v[66:67], s[10:11], 0, v[66:67]
	v_lshl_add_u64 v[66:67], v[66:67], 0, v[2:3]
	global_store_dwordx4 v[66:67], v[62:65], off nt
	ds_read_b32 v9, v14 offset:128
	ds_read_b32 v62, v14 offset:388
	ds_read_b32 v63, v14 offset:648
	ds_read_b32 v64, v14 offset:908
	ds_read_b32 v65, v14 offset:1168
	ds_read_b32 v66, v14 offset:1428
	ds_read_b32 v67, v14 offset:1688
	ds_read_b32 v68, v14 offset:1948
	s_waitcnt lgkmcnt(0)
; #define LAS __attribute__((address_space(3)))
; __device__ __forceinline__ unsigned pk4_fp8(float a, float b, float c, float d) { int w = 0; w = __builtin_amdgcn_cvt_pk_fp8_f32(clamp8(a), clamp8(b), w, false); w = __builtin_amdgcn_cvt_pk_fp8_f32(clamp8(c), clamp8(d), w, true); return (unsigned)w; }
; #define LDS_WAIT() asm volatile("s_waitcnt lgkmcnt(0)" ::: "memory")
; __host__ __device__ __forceinline__ size_t tiled_off(size_t r, int kb, int ktiles) { return (((r >> 8) * ktiles + (kb >> 7)) << 15) + ((r & 255) << 7) + (kb & 127); }
;     const int nblk = N / 64, kb = item / nblk, nb = item % nblk, k0 = 64 * kb, n0 = 64 * nb;
;     const int kr = lane >> 4, nc = (lane & 15) * 4;
;     const float* src = W + (size_t)(k0 + kr) * N + n0 + nc;
;     f32x4 v[16];
; #pragma unroll
;     for (int i = 0; i < 16; ++i) v[i] = __builtin_nontemporal_load((const f32x4*)(src + (size_t)(4 * i) * N));
; #pragma unroll
;     for (int i = 0; i < 16; ++i) { LAS float* d = scr + (4 * i + kr) * 65 + nc; d[0] = v[i].x * W8_SCALE; d[1] = v[i].y * W8_SCALE; d[2] = v[i].z * W8_SCALE; d[3] = v[i].w * W8_SCALE; }
;     LDS_WAIT(); asm volatile("" ::: "memory");
;     const int c = lane & 3;
; #pragma unroll
;     for (int j = 0; j < 4; ++j) { const int n = (lane >> 2) + 16 * j; const LAS float* s = scr + (16 * c) * 65 + n;
;         u32x4 o; o.x = pk4_fp8(s[0 * 65], s[1 * 65], s[2 * 65], s[3 * 65]); o.y = pk4_fp8(s[4 * 65], s[5 * 65], s[6 * 65], s[7 * 65]);
;         o.z = pk4_fp8(s[8 * 65], s[9 * 65], s[10 * 65], s[11 * 65]); o.w = pk4_fp8(s[12 * 65], s[13 * 65], s[14 * 65], s[15 * 65]);
;         const int nn = n0 + n; const int row = MAP == 0 ? nn : ((nn >> 7) * 256 + (nn & 127) + (MAP == 2 ? 128 : 0));
;         __builtin_nontemporal_store(o, (u32x4*)(WT + (pitch < 0 ? tiled_off((size_t)row, k0 + 16 * c, pitch == -1 ? (K >> 7) : -pitch) : (size_t)row * (pitch ? pitch : K) + k0 + 16 * c))); }
;     LDS_WAIT(); asm volatile("" ::: "memory");
	v_med3_f32 v9, v9, s51, v57
	v_med3_f32 v69, v62, s51, v57
	v_mov_b32_e32 v62, v3
	v_cvt_pk_fp8_f32 v62, v9, v69
	v_med3_f32 v9, v63, s51, v57
	v_med3_f32 v65, v65, s51, v57
	v_med3_f32 v66, v66, s51, v57
	v_mov_b32_e32 v63, v3
	v_cvt_pk_fp8_f32 v63, v65, v66
	v_med3_f32 v64, v64, s51, v57
	v_cvt_pk_fp8_f32 v62, v9, v64 op_sel:[0,0,1]
	v_med3_f32 v9, v67, s51, v57
	v_med3_f32 v64, v68, s51, v57
	v_cvt_pk_fp8_f32 v63, v9, v64 op_sel:[0,0,1]
	ds_read_b32 v9, v14 offset:2208
	ds_read_b32 v64, v14 offset:2468
	ds_read_b32 v65, v14 offset:2728
	ds_read_b32 v66, v14 offset:2988
	ds_read_b32 v67, v14 offset:3248
	ds_read_b32 v68, v14 offset:3508
	ds_read_b32 v69, v14 offset:3768
	ds_read_b32 v70, v14 offset:4028
	s_waitcnt lgkmcnt(0)
	v_med3_f32 v9, v9, s51, v57
	v_med3_f32 v71, v64, s51, v57
	v_mov_b32_e32 v64, v3
	v_cvt_pk_fp8_f32 v64, v9, v71
	v_med3_f32 v9, v65, s51, v57
	v_med3_f32 v67, v67, s51, v57
	v_med3_f32 v68, v68, s51, v57
	v_mov_b32_e32 v65, v3
	v_cvt_pk_fp8_f32 v65, v67, v68
	v_med3_f32 v66, v66, s51, v57
	v_cvt_pk_fp8_f32 v64, v9, v66 op_sel:[0,0,1]
	v_med3_f32 v9, v69, s51, v57
	v_med3_f32 v66, v70, s51, v57
	v_cvt_pk_fp8_f32 v65, v9, v66 op_sel:[0,0,1]
	v_or_b32_e32 v9, s63, v16
	v_lshlrev_b32_e32 v9, 7, v9
	v_and_b32_e32 v66, 0x7780, v9
	v_mov_b32_e32 v67, v3
	v_lshl_add_u64 v[66:67], s[10:11], 0, v[66:67]
	v_lshl_add_u64 v[66:67], v[66:67], 0, v[2:3]
	global_store_dwordx4 v[66:67], v[62:65], off nt
	ds_read_b32 v9, v14 offset:192
	ds_read_b32 v62, v14 offset:452
	ds_read_b32 v63, v14 offset:712
	ds_read_b32 v64, v14 offset:972
	ds_read_b32 v65, v14 offset:1232
	ds_read_b32 v66, v14 offset:1492
	ds_read_b32 v67, v14 offset:1752
	ds_read_b32 v68, v14 offset:2012
	s_waitcnt lgkmcnt(0)
	v_med3_f32 v9, v9, s51, v57
	v_med3_f32 v69, v62, s51, v57
	v_mov_b32_e32 v62, v3
	v_cvt_pk_fp8_f32 v62, v9, v69
	v_med3_f32 v9, v63, s51, v57
	v_med3_f32 v65, v65, s51, v57
	v_med3_f32 v66, v66, s51, v57
	v_mov_b32_e32 v63, v3
	v_cvt_pk_fp8_f32 v63, v65, v66
	v_med3_f32 v64, v64, s51, v57
	v_cvt_pk_fp8_f32 v62, v9, v64 op_sel:[0,0,1]
	v_med3_f32 v9, v67, s51, v57
	v_med3_f32 v64, v68, s51, v57
	v_cvt_pk_fp8_f32 v63, v9, v64 op_sel:[0,0,1]
	ds_read_b32 v9, v14 offset:2272
	ds_read_b32 v64, v14 offset:2532
	ds_read_b32 v65, v14 offset:2792
	ds_read_b32 v66, v14 offset:3052
	ds_read_b32 v67, v14 offset:3312
	ds_read_b32 v68, v14 offset:3572
	ds_read_b32 v69, v14 offset:3832
	ds_read_b32 v70, v14 offset:4092
	s_waitcnt lgkmcnt(0)
	v_med3_f32 v9, v9, s51, v57
	v_med3_f32 v71, v64, s51, v57
	v_mov_b32_e32 v64, v3
	v_cvt_pk_fp8_f32 v64, v9, v71
	v_med3_f32 v9, v65, s51, v57
	v_med3_f32 v67, v67, s51, v57
	v_med3_f32 v68, v68, s51, v57
	v_mov_b32_e32 v65, v3
	v_cvt_pk_fp8_f32 v65, v67, v68
	v_med3_f32 v66, v66, s51, v57
	v_cvt_pk_fp8_f32 v64, v9, v66 op_sel:[0,0,1]
	v_med3_f32 v9, v69, s51, v57
	v_med3_f32 v66, v70, s51, v57
	v_cvt_pk_fp8_f32 v65, v9, v66 op_sel:[0,0,1]
	v_or_b32_e32 v9, s63, v17
	v_lshlrev_b32_e32 v9, 7, v9
	v_and_b32_e32 v66, 0x7f80, v9
	v_mov_b32_e32 v67, v3
	v_lshl_add_u64 v[66:67], s[10:11], 0, v[66:67]
	v_lshl_add_u64 v[66:67], v[66:67], 0, v[2:3]
	global_store_dwordx4 v[66:67], v[62:65], off nt
	s_waitcnt lgkmcnt(0)
	s_mov_b64 s[10:11], 0
.LBB0_123:
	s_andn2_b64 vcc, exec, s[10:11]
	s_cbranch_vccnz .LBB0_125
	v_mov_b32_e32 v2, s52
	ds_read_b32 v2, v2
	v_mov_b32_e32 v9, s53
	ds_read_b32 v9, v9
	s_lshr_b32 s0, s97, 9
	s_lshl_b64 s[10:11], s[0:1], 23
	s_waitcnt lgkmcnt(0)
	v_readfirstlane_b32 s60, v2
	s_add_u32 vcc_lo, s60, s10
	v_readfirstlane_b32 s61, v9
	s_addc_u32 vcc_hi, s61, s11
	s_lshl_b64 s[10:11], s[0:1], 22
	s_add_u32 s10, s19, s10
	s_addc_u32 s11, s20, s11
	s_and_b32 s0, s97, 0x1ff
	s_lshl_b32 s63, s0, 2
	s_and_b32 s0, s63, 0x7c0
	v_or_b32_e32 v2, s0, v10
	v_lshlrev_b32_e32 v2, 12, v2
	s_lshl_b32 s0, s97, 8
	v_lshl_add_u64 v[62:63], vcc, 0, v[2:3]
	s_and_b32 s0, s0, 0xf00
	v_lshl_add_u64 v[62:63], v[62:63], 0, s[0:1]
	v_mov_b32_e32 v9, v3
	v_lshl_add_u64 v[122:123], v[62:63], 0, v[8:9]
	v_add_co_u32_e32 v66, vcc, s65, v122
	s_mov_b32 s0, 0x24000
	s_nop 0
	v_addc_co_u32_e32 v67, vcc, 0, v123, vcc
	global_load_dwordx4 v[62:65], v[122:123], off nt
	s_nop 0
	global_load_dwordx4 v[66:69], v[66:67], off nt
	v_add_co_u32_e32 v70, vcc, s28, v122
	s_lshl_b32 s60, s97, 7
	s_nop 0
	v_addc_co_u32_e32 v71, vcc, 0, v123, vcc
	v_add_co_u32_e32 v74, vcc, s66, v122
	s_and_b32 s60, s60, 0x700
	s_nop 0
	v_addc_co_u32_e32 v75, vcc, 0, v123, vcc
	global_load_dwordx4 v[70:73], v[70:71], off nt
	s_nop 0
	global_load_dwordx4 v[74:77], v[74:75], off nt
	v_add_co_u32_e32 v78, vcc, s29, v122
	s_bfe_u32 s61, s97, 0x40005
	s_nop 0
	v_addc_co_u32_e32 v79, vcc, 0, v123, vcc
	v_add_co_u32_e32 v82, vcc, s59, v122
	v_and_or_b32 v2, s63, 64, v13
	s_nop 0
	v_addc_co_u32_e32 v83, vcc, 0, v123, vcc
	global_load_dwordx4 v[78:81], v[78:79], off nt
	s_nop 0
	global_load_dwordx4 v[82:85], v[82:83], off nt
	v_add_co_u32_e32 v86, vcc, s30, v122
	s_nop 1
	v_addc_co_u32_e32 v87, vcc, 0, v123, vcc
	v_add_co_u32_e32 v90, vcc, s62, v122
	s_nop 1
	v_addc_co_u32_e32 v91, vcc, 0, v123, vcc
	global_load_dwordx4 v[86:89], v[86:87], off nt
	s_nop 0
	global_load_dwordx4 v[90:93], v[90:91], off nt
	v_add_co_u32_e32 v94, vcc, s31, v122
	s_nop 1
	v_addc_co_u32_e32 v95, vcc, 0, v123, vcc
	v_add_co_u32_e32 v98, vcc, s0, v122
	s_mov_b32 s0, 0x34000
	s_nop 0
	v_addc_co_u32_e32 v99, vcc, 0, v123, vcc
	global_load_dwordx4 v[94:97], v[94:95], off nt
	s_nop 0
	global_load_dwordx4 v[98:101], v[98:99], off nt
	v_add_co_u32_e32 v102, vcc, s40, v122
	s_nop 1
	v_addc_co_u32_e32 v103, vcc, 0, v123, vcc
	v_add_co_u32_e32 v106, vcc, s64, v122
	s_nop 1
	v_addc_co_u32_e32 v107, vcc, 0, v123, vcc
	global_load_dwordx4 v[102:105], v[102:103], off nt
	s_nop 0
	global_load_dwordx4 v[106:109], v[106:107], off nt
	v_add_co_u32_e32 v110, vcc, s41, v122
	s_nop 1
	v_addc_co_u32_e32 v111, vcc, 0, v123, vcc
	global_load_dwordx4 v[110:113], v[110:111], off nt
	v_add_co_u32_e32 v114, vcc, s0, v122
	s_mov_b32 s0, 0x3c000
	s_nop 0
	v_addc_co_u32_e32 v115, vcc, 0, v123, vcc
	global_load_dwordx4 v[114:117], v[114:115], off nt
	v_add_co_u32_e32 v118, vcc, s42, v122
	s_nop 1
	v_addc_co_u32_e32 v119, vcc, 0, v123, vcc
	global_load_dwordx4 v[118:121], v[118:119], off nt
	v_add_co_u32_e32 v122, vcc, s0, v122
	s_lshl_b32 s0, s97, 6
	s_nop 0
	v_addc_co_u32_e32 v123, vcc, 0, v123, vcc
	global_load_dwordx4 v[122:125], v[122:123], off nt
	s_waitcnt vmcnt(15)
; #define LAS __attribute__((address_space(3)))
; __device__ __forceinline__ unsigned pk4_fp8(float a, float b, float c, float d) { int w = 0; w = __builtin_amdgcn_cvt_pk_fp8_f32(clamp8(a), clamp8(b), w, false); w = __builtin_amdgcn_cvt_pk_fp8_f32(clamp8(c), clamp8(d), w, true); return (unsigned)w; }
; #define LDS_WAIT() asm volatile("s_waitcnt lgkmcnt(0)" ::: "memory")
; __host__ __device__ __forceinline__ size_t tiled_off(size_t r, int kb, int ktiles) { return (((r >> 8) * ktiles + (kb >> 7)) << 15) + ((r & 255) << 7) + (kb & 127); }
;     ...
;     for (int i = 0; i < 16; ++i) v[i] = __builtin_nontemporal_load((const f32x4*)(src + (size_t)(4 * i) * N));
; #pragma unroll
;     for (int i = 0; i < 16; ++i) { LAS float* d = scr + (4 * i + kr) * 65 + nc; d[0] = v[i].x * W8_SCALE; d[1] = v[i].y * W8_SCALE; d[2] = v[i].z * W8_SCALE; d[3] = v[i].w * W8_SCALE; }
;     LDS_WAIT(); asm volatile("" ::: "memory");
;     const int c = lane & 3;
; #pragma unroll
;     for (int j = 0; j < 4; ++j) { const int n = (lane >> 2) + 16 * j; const LAS float* s = scr + (16 * c) * 65 + n;
;         u32x4 o; o.x = pk4_fp8(s[0 * 65], s[1 * 65], s[2 * 65], s[3 * 65]); o.y = pk4_fp8(s[4 * 65], s[5 * 65], s[6 * 65], s[7 * 65]);
;         o.z = pk4_fp8(s[8 * 65], s[9 * 65], s[10 * 65], s[11 * 65]); o.w = pk4_fp8(s[12 * 65], s[13 * 65], s[14 * 65], s[15 * 65]);
;         const int nn = n0 + n; const int row = MAP == 0 ? nn : ((nn >> 7) * 256 + (nn & 127) + (MAP == 2 ? 128 : 0));
;         __builtin_nontemporal_store(o, (u32x4*)(WT + (pitch < 0 ? tiled_off((size_t)row, k0 + 16 * c, pitch == -1 ? (K >> 7) : -pitch) : (size_t)row * (pitch ? pitch : K) + k0 + 16 * c))); }
;     LDS_WAIT(); asm volatile("" ::: "memory");
	v_pk_mul_f32 v[62:63], v[62:63], s[8:9] op_sel_hi:[1,0]
	ds_write2_b32 v11, v62, v63 offset1:1
	v_pk_mul_f32 v[62:63], v[64:65], s[8:9] op_sel_hi:[1,0]
	ds_write2_b32 v11, v62, v63 offset0:2 offset1:3
	s_waitcnt vmcnt(14)
	v_pk_mul_f32 v[62:63], v[66:67], s[8:9] op_sel_hi:[1,0]
	ds_write2_b32 v27, v62, v63 offset1:1
	v_pk_mul_f32 v[62:63], v[68:69], s[8:9] op_sel_hi:[1,0]
	ds_write2_b32 v28, v62, v63 offset1:1
	s_waitcnt vmcnt(13)
	v_pk_mul_f32 v[62:63], v[70:71], s[8:9] op_sel_hi:[1,0]
	ds_write2_b32 v29, v62, v63 offset1:1
	v_pk_mul_f32 v[62:63], v[72:73], s[8:9] op_sel_hi:[1,0]
	ds_write2_b32 v30, v62, v63 offset1:1
	s_waitcnt vmcnt(12)
	v_pk_mul_f32 v[62:63], v[74:75], s[8:9] op_sel_hi:[1,0]
	ds_write2_b32 v31, v62, v63 offset1:1
	v_pk_mul_f32 v[62:63], v[76:77], s[8:9] op_sel_hi:[1,0]
	ds_write2_b32 v32, v62, v63 offset1:1
	s_waitcnt vmcnt(11)
	v_pk_mul_f32 v[62:63], v[78:79], s[8:9] op_sel_hi:[1,0]
	ds_write2_b32 v33, v62, v63 offset1:1
	v_pk_mul_f32 v[62:63], v[80:81], s[8:9] op_sel_hi:[1,0]
	ds_write2_b32 v34, v62, v63 offset1:1
	s_waitcnt vmcnt(10)
	v_pk_mul_f32 v[62:63], v[82:83], s[8:9] op_sel_hi:[1,0]
	ds_write2_b32 v35, v62, v63 offset1:1
	v_pk_mul_f32 v[62:63], v[84:85], s[8:9] op_sel_hi:[1,0]
	ds_write2_b32 v36, v62, v63 offset1:1
	s_and_b32 s0, s0, 64
	s_or_b32 s0, s60, s0
	s_waitcnt vmcnt(0) lgkmcnt(0)
	v_pk_mul_f32 v[62:63], v[86:87], s[8:9] op_sel_hi:[1,0]
	ds_write2_b32 v37, v62, v63 offset1:1
	v_pk_mul_f32 v[62:63], v[88:89], s[8:9] op_sel_hi:[1,0]
	ds_write2_b32 v38, v62, v63 offset1:1
	v_pk_mul_f32 v[62:63], v[90:91], s[8:9] op_sel_hi:[1,0]
	ds_write2_b32 v39, v62, v63 offset1:1
	v_pk_mul_f32 v[62:63], v[92:93], s[8:9] op_sel_hi:[1,0]
	ds_write2_b32 v40, v62, v63 offset1:1
	v_pk_mul_f32 v[62:63], v[94:95], s[8:9] op_sel_hi:[1,0]
	ds_write2_b32 v41, v62, v63 offset1:1
	v_pk_mul_f32 v[62:63], v[96:97], s[8:9] op_sel_hi:[1,0]
	ds_write2_b32 v42, v62, v63 offset1:1
	v_pk_mul_f32 v[62:63], v[98:99], s[8:9] op_sel_hi:[1,0]
	ds_write2_b32 v43, v62, v63 offset1:1
	v_pk_mul_f32 v[62:63], v[100:101], s[8:9] op_sel_hi:[1,0]
	ds_write2_b32 v44, v62, v63 offset1:1
	v_pk_mul_f32 v[62:63], v[102:103], s[8:9] op_sel_hi:[1,0]
	ds_write2_b32 v45, v62, v63 offset1:1
	v_pk_mul_f32 v[62:63], v[104:105], s[8:9] op_sel_hi:[1,0]
	ds_write2_b32 v46, v62, v63 offset1:1
	v_pk_mul_f32 v[62:63], v[106:107], s[8:9] op_sel_hi:[1,0]
	ds_write2_b32 v47, v62, v63 offset1:1
	v_pk_mul_f32 v[62:63], v[108:109], s[8:9] op_sel_hi:[1,0]
	ds_write2_b32 v48, v62, v63 offset1:1
	v_pk_mul_f32 v[62:63], v[110:111], s[8:9] op_sel_hi:[1,0]
	ds_write2_b32 v49, v62, v63 offset1:1
	v_pk_mul_f32 v[62:63], v[112:113], s[8:9] op_sel_hi:[1,0]
	ds_write2_b32 v50, v62, v63 offset1:1
	v_pk_mul_f32 v[62:63], v[114:115], s[8:9] op_sel_hi:[1,0]
	ds_write2_b32 v51, v62, v63 offset1:1
	v_pk_mul_f32 v[62:63], v[116:117], s[8:9] op_sel_hi:[1,0]
	ds_write2_b32 v52, v62, v63 offset1:1
	v_pk_mul_f32 v[62:63], v[118:119], s[8:9] op_sel_hi:[1,0]
	ds_write2_b32 v53, v62, v63 offset1:1
	v_pk_mul_f32 v[62:63], v[120:121], s[8:9] op_sel_hi:[1,0]
	ds_write2_b32 v54, v62, v63 offset1:1
	v_pk_mul_f32 v[62:63], v[122:123], s[8:9] op_sel_hi:[1,0]
	ds_write2_b32 v55, v62, v63 offset1:1
	v_pk_mul_f32 v[62:63], v[124:125], s[8:9] op_sel_hi:[1,0]
	ds_write2_b32 v56, v62, v63 offset1:1
	s_waitcnt lgkmcnt(0)
	ds_read_b32 v9, v14
	ds_read_b32 v62, v14 offset:260
	ds_read_b32 v63, v14 offset:520
	ds_read_b32 v64, v14 offset:780
	ds_read_b32 v65, v14 offset:1040
	ds_read_b32 v66, v14 offset:1300
	ds_read_b32 v67, v14 offset:1560
	ds_read_b32 v68, v14 offset:1820
	s_waitcnt lgkmcnt(7)
	v_med3_f32 v9, v9, s51, v57
	s_waitcnt lgkmcnt(6)
	v_med3_f32 v69, v62, s51, v57
	v_mov_b32_e32 v62, v3
	v_cvt_pk_fp8_f32 v62, v9, v69
	s_waitcnt lgkmcnt(5)
	v_med3_f32 v9, v63, s51, v57
	s_waitcnt lgkmcnt(3)
	v_med3_f32 v65, v65, s51, v57
	s_waitcnt lgkmcnt(2)
	v_med3_f32 v66, v66, s51, v57
	v_mov_b32_e32 v63, v3
	v_cvt_pk_fp8_f32 v63, v65, v66
	v_med3_f32 v64, v64, s51, v57
	v_cvt_pk_fp8_f32 v62, v9, v64 op_sel:[0,0,1]
	s_waitcnt lgkmcnt(1)
	v_med3_f32 v9, v67, s51, v57
	s_waitcnt lgkmcnt(0)
	v_med3_f32 v64, v68, s51, v57
	v_cvt_pk_fp8_f32 v63, v9, v64 op_sel:[0,0,1]
	ds_read_b32 v9, v14 offset:2080
	ds_read_b32 v64, v14 offset:2340
	ds_read_b32 v65, v14 offset:2600
	ds_read_b32 v66, v14 offset:2860
	ds_read_b32 v67, v14 offset:3120
	ds_read_b32 v68, v14 offset:3380
	ds_read_b32 v69, v14 offset:3640
	ds_read_b32 v70, v14 offset:3900
	s_waitcnt lgkmcnt(7)
	v_med3_f32 v9, v9, s51, v57
	s_waitcnt lgkmcnt(6)
	v_med3_f32 v71, v64, s51, v57
	v_mov_b32_e32 v64, v3
	v_cvt_pk_fp8_f32 v64, v9, v71
	s_waitcnt lgkmcnt(5)
	v_med3_f32 v9, v65, s51, v57
	s_waitcnt lgkmcnt(3)
	v_med3_f32 v67, v67, s51, v57
	s_waitcnt lgkmcnt(2)
	v_med3_f32 v68, v68, s51, v57
	v_mov_b32_e32 v65, v3
	v_cvt_pk_fp8_f32 v65, v67, v68
	v_med3_f32 v66, v66, s51, v57
	v_cvt_pk_fp8_f32 v64, v9, v66 op_sel:[0,0,1]
	s_waitcnt lgkmcnt(1)
	v_med3_f32 v9, v69, s51, v57
	s_waitcnt lgkmcnt(0)
; #define LAS __attribute__((address_space(3)))
; __device__ __forceinline__ unsigned pk4_fp8(float a, float b, float c, float d) { int w = 0; w = __builtin_amdgcn_cvt_pk_fp8_f32(clamp8(a), clamp8(b), w, false); w = __builtin_amdgcn_cvt_pk_fp8_f32(clamp8(c), clamp8(d), w, true); return (unsigned)w; }
; #define LDS_WAIT() asm volatile("s_waitcnt lgkmcnt(0)" ::: "memory")
; __host__ __device__ __forceinline__ size_t tiled_off(size_t r, int kb, int ktiles) { return (((r >> 8) * ktiles + (kb >> 7)) << 15) + ((r & 255) << 7) + (kb & 127); }
;     ...
;     const int c = lane & 3;
; #pragma unroll
;     for (int j = 0; j < 4; ++j) { const int n = (lane >> 2) + 16 * j; const LAS float* s = scr + (16 * c) * 65 + n;
;         u32x4 o; o.x = pk4_fp8(s[0 * 65], s[1 * 65], s[2 * 65], s[3 * 65]); o.y = pk4_fp8(s[4 * 65], s[5 * 65], s[6 * 65], s[7 * 65]);
;         o.z = pk4_fp8(s[8 * 65], s[9 * 65], s[10 * 65], s[11 * 65]); o.w = pk4_fp8(s[12 * 65], s[13 * 65], s[14 * 65], s[15 * 65]);
;         const int nn = n0 + n; const int row = MAP == 0 ? nn : ((nn >> 7) * 256 + (nn & 127) + (MAP == 2 ? 128 : 0));
;         __builtin_nontemporal_store(o, (u32x4*)(WT + (pitch < 0 ? tiled_off((size_t)row, k0 + 16 * c, pitch == -1 ? (K >> 7) : -pitch) : (size_t)row * (pitch ? pitch : K) + k0 + 16 * c))); }
;     LDS_WAIT(); asm volatile("" ::: "memory");
	v_med3_f32 v66, v70, s51, v57
	v_cvt_pk_fp8_f32 v65, v9, v66 op_sel:[0,0,1]
	v_or_b32_e32 v9, s0, v12
	v_lshlrev_b32_e32 v9, 7, v9
	s_movk_i32 s0, 0x6780
	v_bitop3_b32 v66, v9, s0, v58 bitop3:0xc8
	s_lshr_b32 s0, s60, 4
	s_or_b32 s0, s0, s61
	s_lshl_b32 s0, s0, 15
	s_add_u32 s10, s10, s0
	v_mov_b32_e32 v67, v3
	s_addc_u32 s11, s11, 0
	v_lshl_add_u64 v[66:67], s[10:11], 0, v[66:67]
	v_lshl_add_u64 v[66:67], v[66:67], 0, v[2:3]
	global_store_dwordx4 v[66:67], v[62:65], off nt
	ds_read_b32 v62, v14 offset:64
	ds_read_b32 v63, v14 offset:324
	ds_read_b32 v64, v14 offset:584
	ds_read_b32 v65, v14 offset:844
	ds_read_b32 v66, v14 offset:1104
	ds_read_b32 v67, v14 offset:1364
	ds_read_b32 v68, v14 offset:1624
	ds_read_b32 v69, v14 offset:1884
	s_waitcnt lgkmcnt(0)
	v_med3_f32 v70, v62, s51, v57
	v_med3_f32 v63, v63, s51, v57
	v_mov_b32_e32 v62, v3
	v_cvt_pk_fp8_f32 v62, v70, v63
	v_med3_f32 v66, v66, s51, v57
	v_med3_f32 v67, v67, s51, v57
	v_mov_b32_e32 v63, v3
	v_cvt_pk_fp8_f32 v63, v66, v67
	v_med3_f32 v64, v64, s51, v57
	v_med3_f32 v65, v65, s51, v57
	v_cvt_pk_fp8_f32 v62, v64, v65 op_sel:[0,0,1]
	v_med3_f32 v64, v68, s51, v57
	v_med3_f32 v65, v69, s51, v57
	v_cvt_pk_fp8_f32 v63, v64, v65 op_sel:[0,0,1]
	ds_read_b32 v64, v14 offset:2144
	ds_read_b32 v65, v14 offset:2404
	ds_read_b32 v66, v14 offset:2664
	ds_read_b32 v67, v14 offset:2924
	ds_read_b32 v68, v14 offset:3184
	ds_read_b32 v69, v14 offset:3444
	ds_read_b32 v70, v14 offset:3704
	ds_read_b32 v71, v14 offset:3964
	s_waitcnt lgkmcnt(0)
	v_med3_f32 v72, v64, s51, v57
	v_med3_f32 v65, v65, s51, v57
	v_mov_b32_e32 v64, v3
	v_cvt_pk_fp8_f32 v64, v72, v65
	v_med3_f32 v68, v68, s51, v57
	v_med3_f32 v69, v69, s51, v57
	v_mov_b32_e32 v65, v3
	v_cvt_pk_fp8_f32 v65, v68, v69
	v_med3_f32 v66, v66, s51, v57
	v_med3_f32 v67, v67, s51, v57
	v_cvt_pk_fp8_f32 v64, v66, v67 op_sel:[0,0,1]
	v_med3_f32 v66, v70, s51, v57
	v_med3_f32 v67, v71, s51, v57
	v_cvt_pk_fp8_f32 v65, v66, v67 op_sel:[0,0,1]
	s_movk_i32 s0, 0x6f80
	v_bitop3_b32 v66, v9, s0, v59 bitop3:0xc8
	v_mov_b32_e32 v67, v3
	v_lshl_add_u64 v[66:67], s[10:11], 0, v[66:67]
	v_lshl_add_u64 v[66:67], v[66:67], 0, v[2:3]
	global_store_dwordx4 v[66:67], v[62:65], off nt
	ds_read_b32 v62, v14 offset:128
	ds_read_b32 v63, v14 offset:388
	ds_read_b32 v64, v14 offset:648
	ds_read_b32 v65, v14 offset:908
	ds_read_b32 v66, v14 offset:1168
	ds_read_b32 v67, v14 offset:1428
	ds_read_b32 v68, v14 offset:1688
	ds_read_b32 v69, v14 offset:1948
	s_waitcnt lgkmcnt(0)
	v_med3_f32 v70, v62, s51, v57
	v_med3_f32 v63, v63, s51, v57
	v_mov_b32_e32 v62, v3
	v_cvt_pk_fp8_f32 v62, v70, v63
	v_med3_f32 v66, v66, s51, v57
	v_med3_f32 v67, v67, s51, v57
	v_mov_b32_e32 v63, v3
	v_cvt_pk_fp8_f32 v63, v66, v67
	v_med3_f32 v64, v64, s51, v57
	v_med3_f32 v65, v65, s51, v57
	v_cvt_pk_fp8_f32 v62, v64, v65 op_sel:[0,0,1]
	v_med3_f32 v64, v68, s51, v57
	v_med3_f32 v65, v69, s51, v57
	v_cvt_pk_fp8_f32 v63, v64, v65 op_sel:[0,0,1]
	ds_read_b32 v64, v14 offset:2208
	ds_read_b32 v65, v14 offset:2468
	ds_read_b32 v66, v14 offset:2728
	ds_read_b32 v67, v14 offset:2988
	ds_read_b32 v68, v14 offset:3248
	ds_read_b32 v69, v14 offset:3508
	ds_read_b32 v70, v14 offset:3768
	ds_read_b32 v71, v14 offset:4028
	s_waitcnt lgkmcnt(0)
	v_med3_f32 v72, v64, s51, v57
	v_med3_f32 v65, v65, s51, v57
	v_mov_b32_e32 v64, v3
	v_cvt_pk_fp8_f32 v64, v72, v65
	v_med3_f32 v68, v68, s51, v57
	v_med3_f32 v69, v69, s51, v57
	v_mov_b32_e32 v65, v3
	v_cvt_pk_fp8_f32 v65, v68, v69
	v_med3_f32 v66, v66, s51, v57
	v_med3_f32 v67, v67, s51, v57
	v_cvt_pk_fp8_f32 v64, v66, v67 op_sel:[0,0,1]
	v_med3_f32 v66, v70, s51, v57
	v_med3_f32 v67, v71, s51, v57
	v_cvt_pk_fp8_f32 v65, v66, v67 op_sel:[0,0,1]
	s_movk_i32 s0, 0x7780
	v_bitop3_b32 v66, v9, s0, v60 bitop3:0xc8
	v_mov_b32_e32 v67, v3
	v_lshl_add_u64 v[66:67], s[10:11], 0, v[66:67]
	v_lshl_add_u64 v[66:67], v[66:67], 0, v[2:3]
	global_store_dwordx4 v[66:67], v[62:65], off nt
	ds_read_b32 v62, v14 offset:192
	ds_read_b32 v63, v14 offset:452
	ds_read_b32 v64, v14 offset:712
	ds_read_b32 v65, v14 offset:972
	ds_read_b32 v66, v14 offset:1232
	ds_read_b32 v67, v14 offset:1492
	ds_read_b32 v68, v14 offset:1752
	ds_read_b32 v69, v14 offset:2012
	s_waitcnt lgkmcnt(0)
	v_med3_f32 v70, v62, s51, v57
	v_med3_f32 v63, v63, s51, v57
	v_mov_b32_e32 v62, v3
	v_cvt_pk_fp8_f32 v62, v70, v63
	v_med3_f32 v66, v66, s51, v57
	v_med3_f32 v67, v67, s51, v57
	v_mov_b32_e32 v63, v3
	v_cvt_pk_fp8_f32 v63, v66, v67
	v_med3_f32 v64, v64, s51, v57
	v_med3_f32 v65, v65, s51, v57
	v_cvt_pk_fp8_f32 v62, v64, v65 op_sel:[0,0,1]
	v_med3_f32 v64, v68, s51, v57
	v_med3_f32 v65, v69, s51, v57
	v_cvt_pk_fp8_f32 v63, v64, v65 op_sel:[0,0,1]
	ds_read_b32 v64, v14 offset:2272
	ds_read_b32 v65, v14 offset:2532
	ds_read_b32 v66, v14 offset:2792
	ds_read_b32 v67, v14 offset:3052
	ds_read_b32 v68, v14 offset:3312
	ds_read_b32 v69, v14 offset:3572
	ds_read_b32 v70, v14 offset:3832
	ds_read_b32 v71, v14 offset:4092
	s_waitcnt lgkmcnt(0)
	v_med3_f32 v72, v64, s51, v57
	v_med3_f32 v65, v65, s51, v57
	v_mov_b32_e32 v64, v3
	v_cvt_pk_fp8_f32 v64, v72, v65
	v_med3_f32 v68, v68, s51, v57
	v_med3_f32 v69, v69, s51, v57
	v_mov_b32_e32 v65, v3
	v_cvt_pk_fp8_f32 v65, v68, v69
	v_med3_f32 v66, v66, s51, v57
	v_med3_f32 v67, v67, s51, v57
	v_cvt_pk_fp8_f32 v64, v66, v67 op_sel:[0,0,1]
	v_med3_f32 v66, v70, s51, v57
	v_med3_f32 v67, v71, s51, v57
	v_cvt_pk_fp8_f32 v65, v66, v67 op_sel:[0,0,1]
	s_movk_i32 s0, 0x7f80
	v_bitop3_b32 v66, v9, s0, v61 bitop3:0xc8
	v_mov_b32_e32 v67, v3
	v_lshl_add_u64 v[66:67], s[10:11], 0, v[66:67]
	v_lshl_add_u64 v[66:67], v[66:67], 0, v[2:3]
	global_store_dwordx4 v[66:67], v[62:65], off nt
	s_waitcnt lgkmcnt(0)

; #define LAS __attribute__((address_space(3)))
; __device__ __forceinline__ unsigned pk4_fp8(float a, float b, float c, float d) { int w = 0; w = __builtin_amdgcn_cvt_pk_fp8_f32(clamp8(a), clamp8(b), w, false); w = __builtin_amdgcn_cvt_pk_fp8_f32(clamp8(c), clamp8(d), w, true); return (unsigned)w; }
; #define LDS_WAIT() asm volatile("s_waitcnt lgkmcnt(0)" ::: "memory")
; __host__ __device__ __forceinline__ size_t tiled_off(size_t r, int kb, int ktiles) { return (((r >> 8) * ktiles + (kb >> 7)) << 15) + ((r & 255) << 7) + (kb & 127); }
;     const int nblk = N / 64, kb = item / nblk, nb = item % nblk, k0 = 64 * kb, n0 = 64 * nb;
;     const int kr = lane >> 4, nc = (lane & 15) * 4;
;     const float* src = W + (size_t)(k0 + kr) * N + n0 + nc;
;     f32x4 v[16];
; #pragma unroll
;     for (int i = 0; i < 16; ++i) v[i] = __builtin_nontemporal_load((const f32x4*)(src + (size_t)(4 * i) * N));
; #pragma unroll
;     for (int i = 0; i < 16; ++i) { LAS float* d = scr + (4 * i + kr) * 65 + nc; d[0] = v[i].x * W8_SCALE; d[1] = v[i].y * W8_SCALE; d[2] = v[i].z * W8_SCALE; d[3] = v[i].w * W8_SCALE; }
;     LDS_WAIT(); asm volatile("" ::: "memory");
;     const int c = lane & 3;
; #pragma unroll
;     for (int j = 0; j < 4; ++j) { const int n = (lane >> 2) + 16 * j; const LAS float* s = scr + (16 * c) * 65 + n;
;         u32x4 o; o.x = pk4_fp8(s[0 * 65], s[1 * 65], s[2 * 65], s[3 * 65]); o.y = pk4_fp8(s[4 * 65], s[5 * 65], s[6 * 65], s[7 * 65]);
;         o.z = pk4_fp8(s[8 * 65], s[9 * 65], s[10 * 65], s[11 * 65]); o.w = pk4_fp8(s[12 * 65], s[13 * 65], s[14 * 65], s[15 * 65]);
;         const int nn = n0 + n; const int row = MAP == 0 ? nn : ((nn >> 7) * 256 + (nn & 127) + (MAP == 2 ? 128 : 0));
;         __builtin_nontemporal_store(o, (u32x4*)(WT + (pitch < 0 ? tiled_off((size_t)row, k0 + 16 * c, pitch == -1 ? (K >> 7) : -pitch) : (size_t)row * (pitch ? pitch : K) + k0 + 16 * c))); }
;     LDS_WAIT(); asm volatile("" ::: "memory");
.LBB0_126:
	s_andn2_b64 vcc, exec, s[10:11]
	s_cbranch_vccnz .LBB0_128
	v_mov_b32_e32 v2, s67
	ds_read_b32 v2, v2
	v_mov_b32_e32 v9, s68
	ds_read_b32 v9, v9
	s_lshr_b32 s0, s96, 9
	s_lshl_b64 s[10:11], s[0:1], 23
	s_waitcnt lgkmcnt(0)
	v_readfirstlane_b32 s60, v2
	s_add_u32 vcc_lo, s60, s10
	v_readfirstlane_b32 s61, v9
	s_addc_u32 vcc_hi, s61, s11
	s_lshl_b64 s[10:11], s[0:1], 22
	s_add_u32 s10, s19, s10
	s_addc_u32 s11, s20, s11
	s_and_b32 s0, s96, 0x1ff
	s_lshl_b32 s65, s0, 2
	s_and_b32 s0, s65, 0x7c0
	v_or_b32_e32 v2, s0, v10
	v_lshlrev_b32_e32 v2, 12, v2
	s_lshl_b32 s0, s96, 8
	v_lshl_add_u64 v[62:63], vcc, 0, v[2:3]
	s_and_b32 s0, s0, 0xf00
	v_lshl_add_u64 v[62:63], v[62:63], 0, s[0:1]
	v_mov_b32_e32 v9, v3
	s_movk_i32 s60, 0x4000
	v_lshl_add_u64 v[122:123], v[62:63], 0, v[8:9]
	v_add_co_u32_e32 v66, vcc, s60, v122
	s_mov_b32 s0, 0x24000
	s_nop 0
	v_addc_co_u32_e32 v67, vcc, 0, v123, vcc
	global_load_dwordx4 v[62:65], v[122:123], off nt
	s_nop 0
	global_load_dwordx4 v[66:69], v[66:67], off nt
	v_add_co_u32_e32 v70, vcc, s28, v122
	s_lshl_b32 s61, s96, 3
	s_nop 0
	v_addc_co_u32_e32 v71, vcc, 0, v123, vcc
	v_add_co_u32_e32 v74, vcc, s66, v122
	s_bfe_u32 s60, s96, 0x40005
	s_nop 0
	v_addc_co_u32_e32 v75, vcc, 0, v123, vcc
	global_load_dwordx4 v[70:73], v[70:71], off nt
	s_nop 0
	global_load_dwordx4 v[74:77], v[74:75], off nt
	v_add_co_u32_e32 v78, vcc, s29, v122
	s_and_b32 s61, s61, 0x70
	s_nop 0
	v_addc_co_u32_e32 v79, vcc, 0, v123, vcc
	v_add_co_u32_e32 v82, vcc, s59, v122
	s_or_b32 s60, s61, s60
	s_nop 0
	v_addc_co_u32_e32 v83, vcc, 0, v123, vcc
	global_load_dwordx4 v[78:81], v[78:79], off nt
	s_nop 0
	global_load_dwordx4 v[82:85], v[82:83], off nt
	v_add_co_u32_e32 v86, vcc, s30, v122
	s_lshl_b32 s60, s60, 15
	s_nop 0
	v_addc_co_u32_e32 v87, vcc, 0, v123, vcc
	v_add_co_u32_e32 v90, vcc, s62, v122
	v_and_or_b32 v2, s65, 64, v13
	s_nop 0
	v_addc_co_u32_e32 v91, vcc, 0, v123, vcc
	global_load_dwordx4 v[86:89], v[86:87], off nt
	s_nop 0
	global_load_dwordx4 v[90:93], v[90:91], off nt
	v_add_co_u32_e32 v94, vcc, s31, v122
	s_movk_i32 s65, 0x4000
	s_nop 0
	v_addc_co_u32_e32 v95, vcc, 0, v123, vcc
	v_add_co_u32_e32 v98, vcc, s0, v122
	s_mov_b32 s0, 0x34000
	s_nop 0
	v_addc_co_u32_e32 v99, vcc, 0, v123, vcc
	global_load_dwordx4 v[94:97], v[94:95], off nt
	s_nop 0
	global_load_dwordx4 v[98:101], v[98:99], off nt
	v_add_co_u32_e32 v102, vcc, s40, v122
	s_nop 1
	v_addc_co_u32_e32 v103, vcc, 0, v123, vcc
	v_add_co_u32_e32 v106, vcc, s64, v122
	s_nop 1
	v_addc_co_u32_e32 v107, vcc, 0, v123, vcc
	global_load_dwordx4 v[102:105], v[102:103], off nt
	s_nop 0
	global_load_dwordx4 v[106:109], v[106:107], off nt
	v_add_co_u32_e32 v110, vcc, s41, v122
	s_nop 1
	v_addc_co_u32_e32 v111, vcc, 0, v123, vcc
	global_load_dwordx4 v[110:113], v[110:111], off nt
	v_add_co_u32_e32 v114, vcc, s0, v122
	s_mov_b32 s0, 0x3c000
	s_nop 0
	v_addc_co_u32_e32 v115, vcc, 0, v123, vcc
	global_load_dwordx4 v[114:117], v[114:115], off nt
	v_add_co_u32_e32 v118, vcc, s42, v122
	s_nop 1
	v_addc_co_u32_e32 v119, vcc, 0, v123, vcc
	global_load_dwordx4 v[118:121], v[118:119], off nt
	v_add_co_u32_e32 v122, vcc, s0, v122
	s_lshl_b32 s0, s96, 6
	s_nop 0
	v_addc_co_u32_e32 v123, vcc, 0, v123, vcc
	global_load_dwordx4 v[122:125], v[122:123], off nt
	s_waitcnt vmcnt(15)
	v_pk_mul_f32 v[62:63], v[62:63], s[8:9] op_sel_hi:[1,0]
	ds_write2_b32 v11, v62, v63 offset1:1
	v_pk_mul_f32 v[62:63], v[64:65], s[8:9] op_sel_hi:[1,0]
	ds_write2_b32 v11, v62, v63 offset0:2 offset1:3
	s_waitcnt vmcnt(14)
	v_pk_mul_f32 v[62:63], v[66:67], s[8:9] op_sel_hi:[1,0]
	ds_write2_b32 v27, v62, v63 offset1:1
	v_pk_mul_f32 v[62:63], v[68:69], s[8:9] op_sel_hi:[1,0]
	ds_write2_b32 v28, v62, v63 offset1:1
	s_waitcnt vmcnt(13)
	v_pk_mul_f32 v[62:63], v[70:71], s[8:9] op_sel_hi:[1,0]
	ds_write2_b32 v29, v62, v63 offset1:1
	v_pk_mul_f32 v[62:63], v[72:73], s[8:9] op_sel_hi:[1,0]
	ds_write2_b32 v30, v62, v63 offset1:1
	s_waitcnt vmcnt(12)
	v_pk_mul_f32 v[62:63], v[74:75], s[8:9] op_sel_hi:[1,0]
	ds_write2_b32 v31, v62, v63 offset1:1
	v_pk_mul_f32 v[62:63], v[76:77], s[8:9] op_sel_hi:[1,0]
	ds_write2_b32 v32, v62, v63 offset1:1
	s_waitcnt vmcnt(11)
	v_pk_mul_f32 v[62:63], v[78:79], s[8:9] op_sel_hi:[1,0]
	ds_write2_b32 v33, v62, v63 offset1:1
	v_pk_mul_f32 v[62:63], v[80:81], s[8:9] op_sel_hi:[1,0]
	ds_write2_b32 v34, v62, v63 offset1:1
	s_waitcnt vmcnt(10)
	v_pk_mul_f32 v[62:63], v[82:83], s[8:9] op_sel_hi:[1,0]
	ds_write2_b32 v35, v62, v63 offset1:1
	v_pk_mul_f32 v[62:63], v[84:85], s[8:9] op_sel_hi:[1,0]
	ds_write2_b32 v36, v62, v63 offset1:1
	s_waitcnt vmcnt(9)
	v_pk_mul_f32 v[62:63], v[86:87], s[8:9] op_sel_hi:[1,0]
	ds_write2_b32 v37, v62, v63 offset1:1
	v_pk_mul_f32 v[62:63], v[88:89], s[8:9] op_sel_hi:[1,0]
	ds_write2_b32 v38, v62, v63 offset1:1
	s_waitcnt vmcnt(8)
	v_pk_mul_f32 v[62:63], v[90:91], s[8:9] op_sel_hi:[1,0]
	ds_write2_b32 v39, v62, v63 offset1:1
	v_pk_mul_f32 v[62:63], v[92:93], s[8:9] op_sel_hi:[1,0]
	ds_write2_b32 v40, v62, v63 offset1:1
	s_waitcnt vmcnt(7)
	v_pk_mul_f32 v[62:63], v[94:95], s[8:9] op_sel_hi:[1,0]
	ds_write2_b32 v41, v62, v63 offset1:1
	v_pk_mul_f32 v[62:63], v[96:97], s[8:9] op_sel_hi:[1,0]
	ds_write2_b32 v42, v62, v63 offset1:1
	s_waitcnt vmcnt(6)
	v_pk_mul_f32 v[62:63], v[98:99], s[8:9] op_sel_hi:[1,0]
	ds_write2_b32 v43, v62, v63 offset1:1
	v_pk_mul_f32 v[62:63], v[100:101], s[8:9] op_sel_hi:[1,0]
	ds_write2_b32 v44, v62, v63 offset1:1
	s_and_b32 s63, s0, 64
	s_add_u32 s10, s10, s60
	s_addc_u32 s11, s11, 0
	s_waitcnt vmcnt(0) lgkmcnt(0)
; #define LAS __attribute__((address_space(3)))
; __device__ __forceinline__ unsigned pk4_fp8(float a, float b, float c, float d) { int w = 0; w = __builtin_amdgcn_cvt_pk_fp8_f32(clamp8(a), clamp8(b), w, false); w = __builtin_amdgcn_cvt_pk_fp8_f32(clamp8(c), clamp8(d), w, true); return (unsigned)w; }
; #define LDS_WAIT() asm volatile("s_waitcnt lgkmcnt(0)" ::: "memory")
; __host__ __device__ __forceinline__ size_t tiled_off(size_t r, int kb, int ktiles) { return (((r >> 8) * ktiles + (kb >> 7)) << 15) + ((r & 255) << 7) + (kb & 127); }
;     ...
;     for (int i = 0; i < 16; ++i) { LAS float* d = scr + (4 * i + kr) * 65 + nc; d[0] = v[i].x * W8_SCALE; d[1] = v[i].y * W8_SCALE; d[2] = v[i].z * W8_SCALE; d[3] = v[i].w * W8_SCALE; }
;     LDS_WAIT(); asm volatile("" ::: "memory");
;     const int c = lane & 3;
; #pragma unroll
;     for (int j = 0; j < 4; ++j) { const int n = (lane >> 2) + 16 * j; const LAS float* s = scr + (16 * c) * 65 + n;
;         u32x4 o; o.x = pk4_fp8(s[0 * 65], s[1 * 65], s[2 * 65], s[3 * 65]); o.y = pk4_fp8(s[4 * 65], s[5 * 65], s[6 * 65], s[7 * 65]);
;         o.z = pk4_fp8(s[8 * 65], s[9 * 65], s[10 * 65], s[11 * 65]); o.w = pk4_fp8(s[12 * 65], s[13 * 65], s[14 * 65], s[15 * 65]);
;         const int nn = n0 + n; const int row = MAP == 0 ? nn : ((nn >> 7) * 256 + (nn & 127) + (MAP == 2 ? 128 : 0));
;         __builtin_nontemporal_store(o, (u32x4*)(WT + (pitch < 0 ? tiled_off((size_t)row, k0 + 16 * c, pitch == -1 ? (K >> 7) : -pitch) : (size_t)row * (pitch ? pitch : K) + k0 + 16 * c))); }
;     LDS_WAIT(); asm volatile("" ::: "memory");
	v_pk_mul_f32 v[62:63], v[102:103], s[8:9] op_sel_hi:[1,0]
	ds_write2_b32 v45, v62, v63 offset1:1
	v_pk_mul_f32 v[62:63], v[104:105], s[8:9] op_sel_hi:[1,0]
	ds_write2_b32 v46, v62, v63 offset1:1
	v_pk_mul_f32 v[62:63], v[106:107], s[8:9] op_sel_hi:[1,0]
	ds_write2_b32 v47, v62, v63 offset1:1
	v_pk_mul_f32 v[62:63], v[108:109], s[8:9] op_sel_hi:[1,0]
	ds_write2_b32 v48, v62, v63 offset1:1
	v_pk_mul_f32 v[62:63], v[110:111], s[8:9] op_sel_hi:[1,0]
	ds_write2_b32 v49, v62, v63 offset1:1
	v_pk_mul_f32 v[62:63], v[112:113], s[8:9] op_sel_hi:[1,0]
	ds_write2_b32 v50, v62, v63 offset1:1
	v_pk_mul_f32 v[62:63], v[114:115], s[8:9] op_sel_hi:[1,0]
	ds_write2_b32 v51, v62, v63 offset1:1
	v_pk_mul_f32 v[62:63], v[116:117], s[8:9] op_sel_hi:[1,0]
	ds_write2_b32 v52, v62, v63 offset1:1
	v_pk_mul_f32 v[62:63], v[118:119], s[8:9] op_sel_hi:[1,0]
	ds_write2_b32 v53, v62, v63 offset1:1
	v_pk_mul_f32 v[62:63], v[120:121], s[8:9] op_sel_hi:[1,0]
	ds_write2_b32 v54, v62, v63 offset1:1
	v_pk_mul_f32 v[62:63], v[122:123], s[8:9] op_sel_hi:[1,0]
	ds_write2_b32 v55, v62, v63 offset1:1
	v_pk_mul_f32 v[62:63], v[124:125], s[8:9] op_sel_hi:[1,0]
	ds_write2_b32 v56, v62, v63 offset1:1
	s_waitcnt lgkmcnt(0)
	ds_read_b32 v9, v14
	ds_read_b32 v62, v14 offset:260
	ds_read_b32 v63, v14 offset:520
	ds_read_b32 v64, v14 offset:780
	ds_read_b32 v65, v14 offset:1040
	ds_read_b32 v66, v14 offset:1300
	ds_read_b32 v67, v14 offset:1560
	ds_read_b32 v68, v14 offset:1820
	s_waitcnt lgkmcnt(7)
	v_med3_f32 v9, v9, s51, v57
	s_waitcnt lgkmcnt(6)
	v_med3_f32 v69, v62, s51, v57
	v_mov_b32_e32 v62, v3
	v_cvt_pk_fp8_f32 v62, v9, v69
	s_waitcnt lgkmcnt(5)
	v_med3_f32 v9, v63, s51, v57
	s_waitcnt lgkmcnt(3)
	v_med3_f32 v65, v65, s51, v57
	s_waitcnt lgkmcnt(2)
	v_med3_f32 v66, v66, s51, v57
	v_mov_b32_e32 v63, v3
	v_cvt_pk_fp8_f32 v63, v65, v66
	v_med3_f32 v64, v64, s51, v57
	v_cvt_pk_fp8_f32 v62, v9, v64 op_sel:[0,0,1]
	s_waitcnt lgkmcnt(1)
	v_med3_f32 v9, v67, s51, v57
	s_waitcnt lgkmcnt(0)
	v_med3_f32 v64, v68, s51, v57
	v_cvt_pk_fp8_f32 v63, v9, v64 op_sel:[0,0,1]
	ds_read_b32 v9, v14 offset:2080
	ds_read_b32 v64, v14 offset:2340
	ds_read_b32 v65, v14 offset:2600
	ds_read_b32 v66, v14 offset:2860
	ds_read_b32 v67, v14 offset:3120
	ds_read_b32 v68, v14 offset:3380
	ds_read_b32 v69, v14 offset:3640
	ds_read_b32 v70, v14 offset:3900
	s_waitcnt lgkmcnt(7)
	v_med3_f32 v9, v9, s51, v57
	s_waitcnt lgkmcnt(6)
	v_med3_f32 v71, v64, s51, v57
	v_mov_b32_e32 v64, v3
	v_cvt_pk_fp8_f32 v64, v9, v71
	s_waitcnt lgkmcnt(5)
	v_med3_f32 v9, v65, s51, v57
	s_waitcnt lgkmcnt(3)
	v_med3_f32 v67, v67, s51, v57
	s_waitcnt lgkmcnt(2)
	v_med3_f32 v68, v68, s51, v57
	v_mov_b32_e32 v65, v3
	v_cvt_pk_fp8_f32 v65, v67, v68
	v_med3_f32 v66, v66, s51, v57
	v_cvt_pk_fp8_f32 v64, v9, v66 op_sel:[0,0,1]
	s_waitcnt lgkmcnt(1)
	v_med3_f32 v9, v69, s51, v57
	s_waitcnt lgkmcnt(0)
	v_med3_f32 v66, v70, s51, v57
	v_cvt_pk_fp8_f32 v65, v9, v66 op_sel:[0,0,1]
	v_or_b32_e32 v9, s63, v12
	v_lshlrev_b32_e32 v66, 7, v9
	v_mov_b32_e32 v67, v3
	v_lshl_add_u64 v[66:67], s[10:11], 0, v[66:67]
	v_lshl_add_u64 v[66:67], v[66:67], 0, v[2:3]
	global_store_dwordx4 v[66:67], v[62:65], off nt
	ds_read_b32 v9, v14 offset:64
	ds_read_b32 v62, v14 offset:324
	ds_read_b32 v63, v14 offset:584
	ds_read_b32 v64, v14 offset:844
	ds_read_b32 v65, v14 offset:1104
	ds_read_b32 v66, v14 offset:1364
	ds_read_b32 v67, v14 offset:1624
	ds_read_b32 v68, v14 offset:1884
	s_waitcnt lgkmcnt(0)
	v_med3_f32 v9, v9, s51, v57
	v_med3_f32 v69, v62, s51, v57
	v_mov_b32_e32 v62, v3
	v_cvt_pk_fp8_f32 v62, v9, v69
	v_med3_f32 v9, v63, s51, v57
	v_med3_f32 v65, v65, s51, v57
	v_med3_f32 v66, v66, s51, v57
	v_mov_b32_e32 v63, v3
	v_cvt_pk_fp8_f32 v63, v65, v66
	v_med3_f32 v64, v64, s51, v57
	v_cvt_pk_fp8_f32 v62, v9, v64 op_sel:[0,0,1]
	v_med3_f32 v9, v67, s51, v57
	v_med3_f32 v64, v68, s51, v57
	v_cvt_pk_fp8_f32 v63, v9, v64 op_sel:[0,0,1]
	ds_read_b32 v9, v14 offset:2144
	ds_read_b32 v64, v14 offset:2404
	ds_read_b32 v65, v14 offset:2664
	ds_read_b32 v66, v14 offset:2924
	ds_read_b32 v67, v14 offset:3184
	ds_read_b32 v68, v14 offset:3444
	ds_read_b32 v69, v14 offset:3704
	ds_read_b32 v70, v14 offset:3964
	s_waitcnt lgkmcnt(0)
; #define LAS __attribute__((address_space(3)))
; __device__ __forceinline__ unsigned pk4_fp8(float a, float b, float c, float d) { int w = 0; w = __builtin_amdgcn_cvt_pk_fp8_f32(clamp8(a), clamp8(b), w, false); w = __builtin_amdgcn_cvt_pk_fp8_f32(clamp8(c), clamp8(d), w, true); return (unsigned)w; }
; #define LDS_WAIT() asm volatile("s_waitcnt lgkmcnt(0)" ::: "memory")
; __host__ __device__ __forceinline__ size_t tiled_off(size_t r, int kb, int ktiles) { return (((r >> 8) * ktiles + (kb >> 7)) << 15) + ((r & 255) << 7) + (kb & 127); }
;     ...
;     const int c = lane & 3;
; #pragma unroll
;     for (int j = 0; j < 4; ++j) { const int n = (lane >> 2) + 16 * j; const LAS float* s = scr + (16 * c) * 65 + n;
;         u32x4 o; o.x = pk4_fp8(s[0 * 65], s[1 * 65], s[2 * 65], s[3 * 65]); o.y = pk4_fp8(s[4 * 65], s[5 * 65], s[6 * 65], s[7 * 65]);
;         o.z = pk4_fp8(s[8 * 65], s[9 * 65], s[10 * 65], s[11 * 65]); o.w = pk4_fp8(s[12 * 65], s[13 * 65], s[14 * 65], s[15 * 65]);
;         const int nn = n0 + n; const int row = MAP == 0 ? nn : ((nn >> 7) * 256 + (nn & 127) + (MAP == 2 ? 128 : 0));
;         __builtin_nontemporal_store(o, (u32x4*)(WT + (pitch < 0 ? tiled_off((size_t)row, k0 + 16 * c, pitch == -1 ? (K >> 7) : -pitch) : (size_t)row * (pitch ? pitch : K) + k0 + 16 * c))); }
;     LDS_WAIT(); asm volatile("" ::: "memory");
	v_med3_f32 v9, v9, s51, v57
	v_med3_f32 v71, v64, s51, v57
	v_mov_b32_e32 v64, v3
	v_cvt_pk_fp8_f32 v64, v9, v71
	v_med3_f32 v9, v65, s51, v57
	v_med3_f32 v67, v67, s51, v57
	v_med3_f32 v68, v68, s51, v57
	v_mov_b32_e32 v65, v3
	v_cvt_pk_fp8_f32 v65, v67, v68
	v_med3_f32 v66, v66, s51, v57
	v_cvt_pk_fp8_f32 v64, v9, v66 op_sel:[0,0,1]
	v_med3_f32 v9, v69, s51, v57
	v_med3_f32 v66, v70, s51, v57
	v_cvt_pk_fp8_f32 v65, v9, v66 op_sel:[0,0,1]
	v_or_b32_e32 v9, s63, v15
	v_lshlrev_b32_e32 v66, 7, v9
	v_mov_b32_e32 v67, v3
	v_lshl_add_u64 v[66:67], s[10:11], 0, v[66:67]
	v_lshl_add_u64 v[66:67], v[66:67], 0, v[2:3]
	global_store_dwordx4 v[66:67], v[62:65], off nt
	ds_read_b32 v9, v14 offset:128
	ds_read_b32 v62, v14 offset:388
	ds_read_b32 v63, v14 offset:648
	ds_read_b32 v64, v14 offset:908
	ds_read_b32 v65, v14 offset:1168
	ds_read_b32 v66, v14 offset:1428
	ds_read_b32 v67, v14 offset:1688
	ds_read_b32 v68, v14 offset:1948
	s_waitcnt lgkmcnt(0)
	v_med3_f32 v9, v9, s51, v57
	v_med3_f32 v69, v62, s51, v57
	v_mov_b32_e32 v62, v3
	v_cvt_pk_fp8_f32 v62, v9, v69
	v_med3_f32 v9, v63, s51, v57
	v_med3_f32 v65, v65, s51, v57
	v_med3_f32 v66, v66, s51, v57
	v_mov_b32_e32 v63, v3
	v_cvt_pk_fp8_f32 v63, v65, v66
	v_med3_f32 v64, v64, s51, v57
	v_cvt_pk_fp8_f32 v62, v9, v64 op_sel:[0,0,1]
	v_med3_f32 v9, v67, s51, v57
	v_med3_f32 v64, v68, s51, v57
	v_cvt_pk_fp8_f32 v63, v9, v64 op_sel:[0,0,1]
	ds_read_b32 v9, v14 offset:2208
	ds_read_b32 v64, v14 offset:2468
	ds_read_b32 v65, v14 offset:2728
	ds_read_b32 v66, v14 offset:2988
	ds_read_b32 v67, v14 offset:3248
	ds_read_b32 v68, v14 offset:3508
	ds_read_b32 v69, v14 offset:3768
	ds_read_b32 v70, v14 offset:4028
	s_waitcnt lgkmcnt(0)
	v_med3_f32 v9, v9, s51, v57
	v_med3_f32 v71, v64, s51, v57
	v_mov_b32_e32 v64, v3
	v_cvt_pk_fp8_f32 v64, v9, v71
	v_med3_f32 v9, v65, s51, v57
	v_med3_f32 v67, v67, s51, v57
	v_med3_f32 v68, v68, s51, v57
	v_mov_b32_e32 v65, v3
	v_cvt_pk_fp8_f32 v65, v67, v68
	v_med3_f32 v66, v66, s51, v57
	v_cvt_pk_fp8_f32 v64, v9, v66 op_sel:[0,0,1]
	v_med3_f32 v9, v69, s51, v57
	v_med3_f32 v66, v70, s51, v57
	v_cvt_pk_fp8_f32 v65, v9, v66 op_sel:[0,0,1]
	v_or_b32_e32 v9, s0, v16
	v_lshlrev_b32_e32 v9, 7, v9
	v_and_b32_e32 v66, 0x3780, v9
	v_mov_b32_e32 v67, v3
	v_lshl_add_u64 v[66:67], s[10:11], 0, v[66:67]
	v_lshl_add_u64 v[66:67], v[66:67], 0, v[2:3]
	global_store_dwordx4 v[66:67], v[62:65], off nt
	ds_read_b32 v9, v14 offset:192
	ds_read_b32 v62, v14 offset:452
	ds_read_b32 v63, v14 offset:712
	ds_read_b32 v64, v14 offset:972
	ds_read_b32 v65, v14 offset:1232
	ds_read_b32 v66, v14 offset:1492
	ds_read_b32 v67, v14 offset:1752
	ds_read_b32 v68, v14 offset:2012
	s_waitcnt lgkmcnt(0)
	v_med3_f32 v9, v9, s51, v57
	v_med3_f32 v69, v62, s51, v57
	v_mov_b32_e32 v62, v3
	v_cvt_pk_fp8_f32 v62, v9, v69
	v_med3_f32 v9, v63, s51, v57
	v_med3_f32 v65, v65, s51, v57
	v_med3_f32 v66, v66, s51, v57
	v_mov_b32_e32 v63, v3
	v_cvt_pk_fp8_f32 v63, v65, v66
	v_med3_f32 v64, v64, s51, v57
	v_cvt_pk_fp8_f32 v62, v9, v64 op_sel:[0,0,1]
	v_med3_f32 v9, v67, s51, v57
	v_med3_f32 v64, v68, s51, v57
	v_cvt_pk_fp8_f32 v63, v9, v64 op_sel:[0,0,1]
	ds_read_b32 v9, v14 offset:2272
	ds_read_b32 v64, v14 offset:2532
	ds_read_b32 v65, v14 offset:2792
	ds_read_b32 v66, v14 offset:3052
	ds_read_b32 v67, v14 offset:3312
	ds_read_b32 v68, v14 offset:3572
	ds_read_b32 v69, v14 offset:3832
	ds_read_b32 v70, v14 offset:4092
	s_waitcnt lgkmcnt(0)
	v_med3_f32 v9, v9, s51, v57
	v_med3_f32 v71, v64, s51, v57
	v_mov_b32_e32 v64, v3
	v_cvt_pk_fp8_f32 v64, v9, v71
	v_med3_f32 v9, v65, s51, v57
	v_med3_f32 v67, v67, s51, v57
	v_med3_f32 v68, v68, s51, v57
	v_mov_b32_e32 v65, v3
	v_cvt_pk_fp8_f32 v65, v67, v68
	v_med3_f32 v66, v66, s51, v57
	v_cvt_pk_fp8_f32 v64, v9, v66 op_sel:[0,0,1]
	v_med3_f32 v9, v69, s51, v57
	v_med3_f32 v66, v70, s51, v57
	v_cvt_pk_fp8_f32 v65, v9, v66 op_sel:[0,0,1]
	v_or_b32_e32 v9, s63, v17
	v_lshlrev_b32_e32 v66, 7, v9
	v_mov_b32_e32 v67, v3
	v_lshl_add_u64 v[66:67], s[10:11], 0, v[66:67]
	v_lshl_add_u64 v[66:67], v[66:67], 0, v[2:3]
	global_store_dwordx4 v[66:67], v[62:65], off nt
	s_waitcnt lgkmcnt(0)

; #define LAS __attribute__((address_space(3)))
; #define LDS_WAIT() asm volatile("s_waitcnt lgkmcnt(0)" ::: "memory")
; template <int MAP>
; __device__ __forceinline__ void transpose_item(const float* W, int K, int N, bf16* WT, LAS float* scr, int item, int lane) {
;     const int nblk = N / 64, kb = item / nblk, nb = item % nblk, k0 = 64 * kb, n0 = 64 * nb;
;     const int kr = lane >> 4, nc = (lane & 15) * 4;
;     const float* src = W + (size_t)(k0 + kr) * N + n0 + nc;
;     f32x4 v[16];
; #pragma unroll
;     for (int i = 0; i < 16; ++i) v[i] = __builtin_nontemporal_load((const f32x4*)(src + (size_t)(4 * i) * N));
; #pragma unroll
;     for (int i = 0; i < 16; ++i) { LAS float* d = scr + (4 * i + kr) * 65 + nc; d[0] = v[i].x; d[1] = v[i].y; d[2] = v[i].z; d[3] = v[i].w; }
;     LDS_WAIT(); asm volatile("" ::: "memory");
.LBB0_129:
	s_andn2_b64 vcc, exec, s[10:11]
	s_cbranch_vccnz .LBB0_131
	v_mov_b32_e32 v2, s69
	ds_read_b32 v2, v2
	v_mov_b32_e32 v9, s70
	ds_read_b32 v9, v9
	s_and_b32 s11, s24, 0x7c0
	s_lshl_b32 s0, s95, 6
	s_waitcnt lgkmcnt(0)
	v_readfirstlane_b32 s96, v2
	v_or_b32_e32 v2, s11, v10
	v_readfirstlane_b32 s97, v9
	s_and_b32 s10, s0, 0x1c0
	v_lshlrev_b32_e32 v2, 11, v2
	v_lshl_add_u64 v[62:63], s[96:97], 0, v[2:3]
	s_lshl_b32 s0, s10, 2
	v_lshl_add_u64 v[62:63], v[62:63], 0, s[0:1]
	v_mov_b32_e32 v9, v3
	v_lshl_add_u64 v[122:123], v[62:63], 0, v[8:9]
	s_movk_i32 s0, 0x2000
	v_add_co_u32_e32 v66, vcc, s0, v122
	s_movk_i32 s0, 0x6000
	s_nop 0
	v_addc_co_u32_e32 v67, vcc, 0, v123, vcc
	v_add_co_u32_e32 v70, vcc, s65, v122
	global_load_dwordx4 v[62:65], v[122:123], off nt
	s_nop 0
	global_load_dwordx4 v[66:69], v[66:67], off nt
	v_addc_co_u32_e32 v71, vcc, 0, v123, vcc
	v_add_co_u32_e32 v74, vcc, s0, v122
	s_mov_b32 s0, 0xa000
	s_nop 0
	v_addc_co_u32_e32 v75, vcc, 0, v123, vcc
	v_add_co_u32_e32 v78, vcc, s28, v122
	global_load_dwordx4 v[70:73], v[70:71], off nt
	s_nop 0
	global_load_dwordx4 v[74:77], v[74:75], off nt
	v_addc_co_u32_e32 v79, vcc, 0, v123, vcc
	v_add_co_u32_e32 v82, vcc, s0, v122
	s_mov_b32 s0, 0xe000
	s_nop 0
	v_addc_co_u32_e32 v83, vcc, 0, v123, vcc
	v_add_co_u32_e32 v86, vcc, s66, v122
	global_load_dwordx4 v[78:81], v[78:79], off nt
	s_nop 0
	global_load_dwordx4 v[82:85], v[82:83], off nt
	v_addc_co_u32_e32 v87, vcc, 0, v123, vcc
	v_add_co_u32_e32 v90, vcc, s0, v122
	s_mov_b32 s0, 0x12000
	s_nop 0
	v_addc_co_u32_e32 v91, vcc, 0, v123, vcc
	v_add_co_u32_e32 v94, vcc, s29, v122
	global_load_dwordx4 v[86:89], v[86:87], off nt
	s_nop 0
	global_load_dwordx4 v[90:93], v[90:91], off nt
	v_addc_co_u32_e32 v95, vcc, 0, v123, vcc
	v_add_co_u32_e32 v98, vcc, s0, v122
	s_mov_b32 s0, 0x1a000
	s_nop 0
	v_addc_co_u32_e32 v99, vcc, 0, v123, vcc
	v_add_co_u32_e32 v102, vcc, s59, v122
	global_load_dwordx4 v[94:97], v[94:95], off nt
	s_nop 0
	global_load_dwordx4 v[98:101], v[98:99], off nt
	v_addc_co_u32_e32 v103, vcc, 0, v123, vcc
	v_add_co_u32_e32 v106, vcc, s71, v122
	s_nop 1
	v_addc_co_u32_e32 v107, vcc, 0, v123, vcc
	v_add_co_u32_e32 v110, vcc, s30, v122
	global_load_dwordx4 v[102:105], v[102:103], off nt
	s_nop 0
	global_load_dwordx4 v[106:109], v[106:107], off nt
	v_addc_co_u32_e32 v111, vcc, 0, v123, vcc
	v_add_co_u32_e32 v114, vcc, s0, v122
	s_mov_b32 s0, 0x1e000
	s_nop 0
	v_addc_co_u32_e32 v115, vcc, 0, v123, vcc
	global_load_dwordx4 v[110:113], v[110:111], off nt
	s_nop 0
	global_load_dwordx4 v[114:117], v[114:115], off nt
	v_add_co_u32_e32 v118, vcc, s62, v122
	s_nop 1
	v_addc_co_u32_e32 v119, vcc, 0, v123, vcc
	global_load_dwordx4 v[118:121], v[118:119], off nt
	v_add_co_u32_e32 v122, vcc, s0, v122
	s_lshl_b32 s0, s11, 1
	s_nop 0
	v_addc_co_u32_e32 v123, vcc, 0, v123, vcc
	global_load_dwordx4 v[122:125], v[122:123], off nt
	s_waitcnt vmcnt(0) lgkmcnt(0)
	ds_write2_b32 v11, v62, v63 offset1:1
	ds_write2_b32 v11, v64, v65 offset0:2 offset1:3
	ds_write2_b32 v27, v66, v67 offset1:1
	ds_write2_b32 v28, v68, v69 offset1:1
	ds_write2_b32 v29, v70, v71 offset1:1
	ds_write2_b32 v30, v72, v73 offset1:1
	ds_write2_b32 v31, v74, v75 offset1:1
	ds_write2_b32 v32, v76, v77 offset1:1
	ds_write2_b32 v33, v78, v79 offset1:1
	ds_write2_b32 v34, v80, v81 offset1:1
	ds_write2_b32 v35, v82, v83 offset1:1
	ds_write2_b32 v36, v84, v85 offset1:1
	ds_write2_b32 v37, v86, v87 offset1:1
	ds_write2_b32 v38, v88, v89 offset1:1
	ds_write2_b32 v39, v90, v91 offset1:1
	ds_write2_b32 v40, v92, v93 offset1:1
	ds_write2_b32 v41, v94, v95 offset1:1
	ds_write2_b32 v42, v96, v97 offset1:1
	ds_write2_b32 v43, v98, v99 offset1:1
	ds_write2_b32 v44, v100, v101 offset1:1
	ds_write2_b32 v45, v102, v103 offset1:1
	ds_write2_b32 v46, v104, v105 offset1:1
	ds_write2_b32 v47, v106, v107 offset1:1
	ds_write2_b32 v48, v108, v109 offset1:1
	ds_write2_b32 v49, v110, v111 offset1:1
	ds_write2_b32 v50, v112, v113 offset1:1
	ds_write2_b32 v51, v114, v115 offset1:1
	ds_write2_b32 v52, v116, v117 offset1:1
	ds_write2_b32 v53, v118, v119 offset1:1
	ds_write2_b32 v54, v120, v121 offset1:1
	ds_write2_b32 v55, v122, v123 offset1:1
	ds_write2_b32 v56, v124, v125 offset1:1
	s_waitcnt lgkmcnt(0)
	ds_read_b32 v2, v19
	ds_read_b32 v9, v19 offset:260
	ds_read_b32 v63, v19 offset:520
	ds_read_b32 v64, v19 offset:780
	ds_read_b32 v65, v19 offset:1040
	ds_read_b32 v68, v19 offset:1300
	ds_read_b32 v69, v19 offset:1560
	ds_read_b32 v70, v19 offset:1820
	s_waitcnt lgkmcnt(6)
; #define LAS __attribute__((address_space(3)))
; __device__ __forceinline__ unsigned pk_bf16(float lo, float hi) { const bf16x2_t r = __builtin_convertvector((f32x2){lo, hi}, bf16x2_t); return __builtin_bit_cast(unsigned, r); }
; #define LDS_WAIT() asm volatile("s_waitcnt lgkmcnt(0)" ::: "memory")
; template <int MAP>
; __device__ __forceinline__ void transpose_item(const float* W, int K, int N, bf16* WT, LAS float* scr, int item, int lane) {
;     ...
;     const int c = lane & 7;
; #pragma unroll
;     for (int j = 0; j < 8; ++j) { const int n = (lane >> 3) + 8 * j; const LAS float* s = scr + (8 * c) * 65 + n;
;         u32x4 o; o.x = pk_bf16(s[0 * 65], s[1 * 65]); o.y = pk_bf16(s[2 * 65], s[3 * 65]); o.z = pk_bf16(s[4 * 65], s[5 * 65]); o.w = pk_bf16(s[6 * 65], s[7 * 65]);
;         const int nn = n0 + n; const int row = MAP == 0 ? nn : ((nn >> 7) * 256 + (nn & 127) + (MAP == 2 ? 128 : 0));
;         __builtin_nontemporal_store(o, (u32x4*)(WT + (size_t)row * K + k0 + 8 * c)); }
;     LDS_WAIT(); asm volatile("" ::: "memory");
	v_cvt_pk_bf16_f32 v62, v2, v9
	v_or_b32_e32 v2, s10, v18
	v_lshl_add_u64 v[66:67], v[4:5], 0, s[0:1]
	v_lshlrev_b32_e32 v2, 10, v2
	s_waitcnt lgkmcnt(4)
	v_cvt_pk_bf16_f32 v63, v63, v64
	s_waitcnt lgkmcnt(2)
	v_cvt_pk_bf16_f32 v64, v65, v68
	s_waitcnt lgkmcnt(0)
	v_cvt_pk_bf16_f32 v65, v69, v70
	v_lshl_add_u64 v[68:69], v[66:67], 0, v[2:3]
	global_store_dwordx4 v[68:69], v[62:65], off nt
	ds_read_b32 v2, v19 offset:32
	ds_read_b32 v9, v19 offset:292
	ds_read_b32 v63, v19 offset:552
	ds_read_b32 v64, v19 offset:812
	ds_read_b32 v65, v19 offset:1072
	ds_read_b32 v68, v19 offset:1332
	ds_read_b32 v69, v19 offset:1592
	ds_read_b32 v70, v19 offset:1852
	s_waitcnt lgkmcnt(0)
	v_cvt_pk_bf16_f32 v62, v2, v9
	v_or_b32_e32 v2, s10, v20
	v_lshlrev_b32_e32 v2, 10, v2
	v_cvt_pk_bf16_f32 v63, v63, v64
	v_cvt_pk_bf16_f32 v64, v65, v68
	v_cvt_pk_bf16_f32 v65, v69, v70
	v_lshl_add_u64 v[68:69], v[66:67], 0, v[2:3]
	global_store_dwordx4 v[68:69], v[62:65], off nt
	ds_read_b32 v2, v19 offset:64
	ds_read_b32 v9, v19 offset:324
	ds_read_b32 v63, v19 offset:584
	ds_read_b32 v64, v19 offset:844
	ds_read_b32 v65, v19 offset:1104
	ds_read_b32 v68, v19 offset:1364
	ds_read_b32 v69, v19 offset:1624
	ds_read_b32 v70, v19 offset:1884
	s_waitcnt lgkmcnt(0)
	v_cvt_pk_bf16_f32 v62, v2, v9
	v_or_b32_e32 v2, s10, v21
	v_lshlrev_b32_e32 v2, 10, v2
	v_cvt_pk_bf16_f32 v63, v63, v64
	v_cvt_pk_bf16_f32 v64, v65, v68
	v_cvt_pk_bf16_f32 v65, v69, v70
	v_lshl_add_u64 v[68:69], v[66:67], 0, v[2:3]
	global_store_dwordx4 v[68:69], v[62:65], off nt
	ds_read_b32 v2, v19 offset:96
	ds_read_b32 v9, v19 offset:356
	ds_read_b32 v63, v19 offset:616
	ds_read_b32 v64, v19 offset:876
	ds_read_b32 v65, v19 offset:1136
	ds_read_b32 v68, v19 offset:1396
	ds_read_b32 v69, v19 offset:1656
	ds_read_b32 v70, v19 offset:1916
	s_waitcnt lgkmcnt(0)
	v_cvt_pk_bf16_f32 v62, v2, v9
	v_or_b32_e32 v2, s10, v22
	v_lshlrev_b32_e32 v2, 10, v2
	v_cvt_pk_bf16_f32 v63, v63, v64
	v_cvt_pk_bf16_f32 v64, v65, v68
	v_cvt_pk_bf16_f32 v65, v69, v70
	v_lshl_add_u64 v[68:69], v[66:67], 0, v[2:3]
	global_store_dwordx4 v[68:69], v[62:65], off nt
	ds_read_b32 v2, v19 offset:128
	ds_read_b32 v9, v19 offset:388
	ds_read_b32 v63, v19 offset:648
	ds_read_b32 v64, v19 offset:908
	ds_read_b32 v65, v19 offset:1168
	ds_read_b32 v68, v19 offset:1428
	ds_read_b32 v69, v19 offset:1688
	ds_read_b32 v70, v19 offset:1948
	s_waitcnt lgkmcnt(0)
	v_cvt_pk_bf16_f32 v62, v2, v9
	v_or_b32_e32 v2, s10, v23
	v_lshlrev_b32_e32 v2, 10, v2
	v_cvt_pk_bf16_f32 v63, v63, v64
	v_cvt_pk_bf16_f32 v64, v65, v68
	v_cvt_pk_bf16_f32 v65, v69, v70
	v_lshl_add_u64 v[68:69], v[66:67], 0, v[2:3]
	global_store_dwordx4 v[68:69], v[62:65], off nt
	ds_read_b32 v2, v19 offset:160
	ds_read_b32 v9, v19 offset:420
	ds_read_b32 v63, v19 offset:680
	ds_read_b32 v64, v19 offset:940
	ds_read_b32 v65, v19 offset:1200
	ds_read_b32 v68, v19 offset:1460
	ds_read_b32 v69, v19 offset:1720
	ds_read_b32 v70, v19 offset:1980
	s_waitcnt lgkmcnt(0)
	v_cvt_pk_bf16_f32 v62, v2, v9
	v_or_b32_e32 v2, s10, v24
	v_lshlrev_b32_e32 v2, 10, v2
	v_cvt_pk_bf16_f32 v63, v63, v64
	v_cvt_pk_bf16_f32 v64, v65, v68
	v_cvt_pk_bf16_f32 v65, v69, v70
	v_lshl_add_u64 v[68:69], v[66:67], 0, v[2:3]
	global_store_dwordx4 v[68:69], v[62:65], off nt
	ds_read_b32 v2, v19 offset:192
	ds_read_b32 v9, v19 offset:452
	ds_read_b32 v63, v19 offset:712
	ds_read_b32 v64, v19 offset:972
	ds_read_b32 v65, v19 offset:1232
	ds_read_b32 v68, v19 offset:1492
	ds_read_b32 v69, v19 offset:1752
	ds_read_b32 v70, v19 offset:2012
	s_waitcnt lgkmcnt(0)
	v_cvt_pk_bf16_f32 v62, v2, v9
	v_or_b32_e32 v2, s10, v25
	v_lshlrev_b32_e32 v2, 10, v2
	v_cvt_pk_bf16_f32 v63, v63, v64
	v_cvt_pk_bf16_f32 v64, v65, v68
	v_cvt_pk_bf16_f32 v65, v69, v70
	v_lshl_add_u64 v[68:69], v[66:67], 0, v[2:3]
	global_store_dwordx4 v[68:69], v[62:65], off nt
	ds_read_b32 v2, v19 offset:224
	ds_read_b32 v9, v19 offset:484
	ds_read_b32 v63, v19 offset:744
	ds_read_b32 v64, v19 offset:1004
	ds_read_b32 v65, v19 offset:1264
	ds_read_b32 v68, v19 offset:1524
	ds_read_b32 v69, v19 offset:1784
	ds_read_b32 v70, v19 offset:2044
	s_waitcnt lgkmcnt(0)
	v_cvt_pk_bf16_f32 v62, v2, v9
	v_or_b32_e32 v2, s10, v26
	v_lshlrev_b32_e32 v2, 10, v2
	v_cvt_pk_bf16_f32 v63, v63, v64
	v_cvt_pk_bf16_f32 v64, v65, v68
	v_cvt_pk_bf16_f32 v65, v69, v70
	v_lshl_add_u64 v[66:67], v[66:67], 0, v[2:3]
	global_store_dwordx4 v[66:67], v[62:65], off nt
	s_waitcnt lgkmcnt(0)

; #define LAS __attribute__((address_space(3)))
; __device__ __forceinline__ unsigned pk4_fp8(float a, float b, float c, float d) { int w = 0; w = __builtin_amdgcn_cvt_pk_fp8_f32(clamp8(a), clamp8(b), w, false); w = __builtin_amdgcn_cvt_pk_fp8_f32(clamp8(c), clamp8(d), w, true); return (unsigned)w; }
; #define LDS_WAIT() asm volatile("s_waitcnt lgkmcnt(0)" ::: "memory")
; __host__ __device__ __forceinline__ size_t tiled_off(size_t r, int kb, int ktiles) { return (((r >> 8) * ktiles + (kb >> 7)) << 15) + ((r & 255) << 7) + (kb & 127); }
; #define AIN(i) ((const float*)ldp(lds, (i)))
;     const int nblk = N / 64, kb = item / nblk, nb = item % nblk, k0 = 64 * kb, n0 = 64 * nb;
;     const int kr = lane >> 4, nc = (lane & 15) * 4;
;     const float* src = W + (size_t)(k0 + kr) * N + n0 + nc;
;     f32x4 v[16];
; #pragma unroll
;     for (int i = 0; i < 16; ++i) v[i] = __builtin_nontemporal_load((const f32x4*)(src + (size_t)(4 * i) * N));
; #pragma unroll
;     for (int i = 0; i < 16; ++i) { LAS float* d = scr + (4 * i + kr) * 65 + nc; d[0] = v[i].x * W8_SCALE; d[1] = v[i].y * W8_SCALE; d[2] = v[i].z * W8_SCALE; d[3] = v[i].w * W8_SCALE; }
;     LDS_WAIT(); asm volatile("" ::: "memory");
;     const int c = lane & 3;
; #pragma unroll
;     for (int j = 0; j < 4; ++j) { const int n = (lane >> 2) + 16 * j; const LAS float* s = scr + (16 * c) * 65 + n;
;         u32x4 o; o.x = pk4_fp8(s[0 * 65], s[1 * 65], s[2 * 65], s[3 * 65]); o.y = pk4_fp8(s[4 * 65], s[5 * 65], s[6 * 65], s[7 * 65]);
;         o.z = pk4_fp8(s[8 * 65], s[9 * 65], s[10 * 65], s[11 * 65]); o.w = pk4_fp8(s[12 * 65], s[13 * 65], s[14 * 65], s[15 * 65]);
;         const int nn = n0 + n; const int row = MAP == 0 ? nn : ((nn >> 7) * 256 + (nn & 127) + (MAP == 2 ? 128 : 0));
;         __builtin_nontemporal_store(o, (u32x4*)(WT + (pitch < 0 ? tiled_off((size_t)row, k0 + 16 * c, pitch == -1 ? (K >> 7) : -pitch) : (size_t)row * (pitch ? pitch : K) + k0 + 16 * c))); }
;     LDS_WAIT(); asm volatile("" ::: "memory");
; __device__ __forceinline__ void ph0(LAS unsigned char* lds, int tid, int lane, int wave, int G, int bid) {
;     ...
;             if (r < I_O) { transpose_item_f8<0>(AIN(IWOUT), D, D, (unsigned char*)(ws + WS_WOT), scr, r, lane, -1); continue; } r -= I_O;
.LBB0_132:
	s_andn2_b64 vcc, exec, s[10:11]
	s_cbranch_vccnz .LBB0_134
	v_mov_b32_e32 v2, s72
	ds_read_b32 v2, v2
	v_mov_b32_e32 v9, s73
	ds_read_b32 v9, v9
	s_bfe_u32 s0, s94, 0xb0005
	s_lshl_b32 s60, s0, 6
	s_waitcnt lgkmcnt(0)
	v_readfirstlane_b32 s10, v2
	s_lshl_b32 s0, s94, 6
	v_or_b32_e32 v2, s60, v10
	v_readfirstlane_b32 s11, v9
	s_and_b32 s63, s0, 0x7c0
	v_lshlrev_b32_e32 v2, 13, v2
	v_lshl_add_u64 v[62:63], s[10:11], 0, v[2:3]
	s_lshl_b32 s0, s63, 2
	v_lshl_add_u64 v[62:63], v[62:63], 0, s[0:1]
	v_mov_b32_e32 v9, v3
	v_lshl_add_u64 v[122:123], v[62:63], 0, v[8:9]
	v_add_co_u32_e32 v66, vcc, s28, v122
	s_lshr_b32 s0, s94, 5
	s_nop 0
	v_addc_co_u32_e32 v67, vcc, 0, v123, vcc
	global_load_dwordx4 v[62:65], v[122:123], off nt
	s_nop 0
	global_load_dwordx4 v[66:69], v[66:67], off nt
	v_add_co_u32_e32 v70, vcc, s29, v122
	s_lshl_b32 s10, s94, 2
	s_nop 0
	v_addc_co_u32_e32 v71, vcc, 0, v123, vcc
	v_add_co_u32_e32 v74, vcc, s30, v122
	s_bfe_u32 s0, s0, 0xa0001
	s_nop 0
	v_addc_co_u32_e32 v75, vcc, 0, v123, vcc
	global_load_dwordx4 v[70:73], v[70:71], off nt
	s_nop 0
	global_load_dwordx4 v[74:77], v[74:75], off nt
	v_add_co_u32_e32 v78, vcc, s31, v122
	s_and_b32 s10, s10, 0x70
	s_nop 0
	v_addc_co_u32_e32 v79, vcc, 0, v123, vcc
	v_add_co_u32_e32 v82, vcc, s40, v122
	s_add_i32 s10, s10, s0
	s_nop 0
	v_addc_co_u32_e32 v83, vcc, 0, v123, vcc
	global_load_dwordx4 v[78:81], v[78:79], off nt
	s_nop 0
	global_load_dwordx4 v[82:85], v[82:83], off nt
	v_add_co_u32_e32 v86, vcc, s41, v122
	s_lshl_b32 s0, s10, 15
	s_nop 0
	v_addc_co_u32_e32 v87, vcc, 0, v123, vcc
	v_add_co_u32_e32 v90, vcc, s42, v122
	s_add_u32 s10, s21, s0
	s_nop 0
	v_addc_co_u32_e32 v91, vcc, 0, v123, vcc
	global_load_dwordx4 v[86:89], v[86:87], off nt
	s_nop 0
	global_load_dwordx4 v[90:93], v[90:91], off nt
	v_add_co_u32_e32 v94, vcc, s43, v122
	s_addc_u32 s11, s22, 0
	s_nop 0
	v_addc_co_u32_e32 v95, vcc, 0, v123, vcc
	v_add_co_u32_e32 v98, vcc, s44, v122
	v_and_or_b32 v2, s60, 64, v13
	s_nop 0
	v_addc_co_u32_e32 v99, vcc, 0, v123, vcc
	global_load_dwordx4 v[94:97], v[94:95], off nt
	s_nop 0
	global_load_dwordx4 v[98:101], v[98:99], off nt
	v_add_co_u32_e32 v102, vcc, s45, v122
	s_nop 1
	v_addc_co_u32_e32 v103, vcc, 0, v123, vcc
	v_add_co_u32_e32 v106, vcc, s46, v122
	s_nop 1
	v_addc_co_u32_e32 v107, vcc, 0, v123, vcc
	global_load_dwordx4 v[102:105], v[102:103], off nt
	s_nop 0
	global_load_dwordx4 v[106:109], v[106:107], off nt
	v_add_co_u32_e32 v110, vcc, s47, v122
	s_nop 1
	v_addc_co_u32_e32 v111, vcc, 0, v123, vcc
	global_load_dwordx4 v[110:113], v[110:111], off nt
	v_add_co_u32_e32 v114, vcc, s48, v122
	s_nop 1
	v_addc_co_u32_e32 v115, vcc, 0, v123, vcc
	global_load_dwordx4 v[114:117], v[114:115], off nt
	v_add_co_u32_e32 v118, vcc, s49, v122
	s_nop 1
	v_addc_co_u32_e32 v119, vcc, 0, v123, vcc
	global_load_dwordx4 v[118:121], v[118:119], off nt
	v_add_co_u32_e32 v122, vcc, s50, v122
	s_nop 1
	v_addc_co_u32_e32 v123, vcc, 0, v123, vcc
	global_load_dwordx4 v[122:125], v[122:123], off nt
	s_waitcnt vmcnt(15)
	v_pk_mul_f32 v[62:63], v[62:63], s[8:9] op_sel_hi:[1,0]
	ds_write2_b32 v11, v62, v63 offset1:1
	v_pk_mul_f32 v[62:63], v[64:65], s[8:9] op_sel_hi:[1,0]
	ds_write2_b32 v11, v62, v63 offset0:2 offset1:3
	s_waitcnt vmcnt(14)
	v_pk_mul_f32 v[62:63], v[66:67], s[8:9] op_sel_hi:[1,0]
	ds_write2_b32 v27, v62, v63 offset1:1
	v_pk_mul_f32 v[62:63], v[68:69], s[8:9] op_sel_hi:[1,0]
	ds_write2_b32 v28, v62, v63 offset1:1
	s_waitcnt vmcnt(13)
	v_pk_mul_f32 v[62:63], v[70:71], s[8:9] op_sel_hi:[1,0]
	ds_write2_b32 v29, v62, v63 offset1:1
	v_pk_mul_f32 v[62:63], v[72:73], s[8:9] op_sel_hi:[1,0]
	ds_write2_b32 v30, v62, v63 offset1:1
	s_waitcnt vmcnt(12)
	v_pk_mul_f32 v[62:63], v[74:75], s[8:9] op_sel_hi:[1,0]
	ds_write2_b32 v31, v62, v63 offset1:1
	v_pk_mul_f32 v[62:63], v[76:77], s[8:9] op_sel_hi:[1,0]
	ds_write2_b32 v32, v62, v63 offset1:1
	s_waitcnt vmcnt(11)
	v_pk_mul_f32 v[62:63], v[78:79], s[8:9] op_sel_hi:[1,0]
	ds_write2_b32 v33, v62, v63 offset1:1
	v_pk_mul_f32 v[62:63], v[80:81], s[8:9] op_sel_hi:[1,0]
	ds_write2_b32 v34, v62, v63 offset1:1
	s_waitcnt vmcnt(10)
	v_pk_mul_f32 v[62:63], v[82:83], s[8:9] op_sel_hi:[1,0]
	ds_write2_b32 v35, v62, v63 offset1:1
	v_pk_mul_f32 v[62:63], v[84:85], s[8:9] op_sel_hi:[1,0]
	ds_write2_b32 v36, v62, v63 offset1:1
	s_waitcnt vmcnt(9)
	v_pk_mul_f32 v[62:63], v[86:87], s[8:9] op_sel_hi:[1,0]
	ds_write2_b32 v37, v62, v63 offset1:1
	v_pk_mul_f32 v[62:63], v[88:89], s[8:9] op_sel_hi:[1,0]
	ds_write2_b32 v38, v62, v63 offset1:1
	s_waitcnt vmcnt(8)
	v_pk_mul_f32 v[62:63], v[90:91], s[8:9] op_sel_hi:[1,0]
	ds_write2_b32 v39, v62, v63 offset1:1
	v_pk_mul_f32 v[62:63], v[92:93], s[8:9] op_sel_hi:[1,0]
	ds_write2_b32 v40, v62, v63 offset1:1
	s_waitcnt vmcnt(7)
	v_pk_mul_f32 v[62:63], v[94:95], s[8:9] op_sel_hi:[1,0]
	ds_write2_b32 v41, v62, v63 offset1:1
	v_pk_mul_f32 v[62:63], v[96:97], s[8:9] op_sel_hi:[1,0]
	ds_write2_b32 v42, v62, v63 offset1:1
	s_waitcnt vmcnt(6)
	v_pk_mul_f32 v[62:63], v[98:99], s[8:9] op_sel_hi:[1,0]
	ds_write2_b32 v43, v62, v63 offset1:1
	v_pk_mul_f32 v[62:63], v[100:101], s[8:9] op_sel_hi:[1,0]
	ds_write2_b32 v44, v62, v63 offset1:1
	s_waitcnt vmcnt(0) lgkmcnt(0)
; #define LAS __attribute__((address_space(3)))
; __device__ __forceinline__ unsigned pk4_fp8(float a, float b, float c, float d) { int w = 0; w = __builtin_amdgcn_cvt_pk_fp8_f32(clamp8(a), clamp8(b), w, false); w = __builtin_amdgcn_cvt_pk_fp8_f32(clamp8(c), clamp8(d), w, true); return (unsigned)w; }
; #define LDS_WAIT() asm volatile("s_waitcnt lgkmcnt(0)" ::: "memory")
; __host__ __device__ __forceinline__ size_t tiled_off(size_t r, int kb, int ktiles) { return (((r >> 8) * ktiles + (kb >> 7)) << 15) + ((r & 255) << 7) + (kb & 127); }
;     ...
;     for (int i = 0; i < 16; ++i) { LAS float* d = scr + (4 * i + kr) * 65 + nc; d[0] = v[i].x * W8_SCALE; d[1] = v[i].y * W8_SCALE; d[2] = v[i].z * W8_SCALE; d[3] = v[i].w * W8_SCALE; }
;     LDS_WAIT(); asm volatile("" ::: "memory");
;     const int c = lane & 3;
; #pragma unroll
;     for (int j = 0; j < 4; ++j) { const int n = (lane >> 2) + 16 * j; const LAS float* s = scr + (16 * c) * 65 + n;
;         u32x4 o; o.x = pk4_fp8(s[0 * 65], s[1 * 65], s[2 * 65], s[3 * 65]); o.y = pk4_fp8(s[4 * 65], s[5 * 65], s[6 * 65], s[7 * 65]);
;         o.z = pk4_fp8(s[8 * 65], s[9 * 65], s[10 * 65], s[11 * 65]); o.w = pk4_fp8(s[12 * 65], s[13 * 65], s[14 * 65], s[15 * 65]);
;         const int nn = n0 + n; const int row = MAP == 0 ? nn : ((nn >> 7) * 256 + (nn & 127) + (MAP == 2 ? 128 : 0));
;         __builtin_nontemporal_store(o, (u32x4*)(WT + (pitch < 0 ? tiled_off((size_t)row, k0 + 16 * c, pitch == -1 ? (K >> 7) : -pitch) : (size_t)row * (pitch ? pitch : K) + k0 + 16 * c))); }
;     LDS_WAIT(); asm volatile("" ::: "memory");
	v_pk_mul_f32 v[62:63], v[102:103], s[8:9] op_sel_hi:[1,0]
	ds_write2_b32 v45, v62, v63 offset1:1
	v_pk_mul_f32 v[62:63], v[104:105], s[8:9] op_sel_hi:[1,0]
	ds_write2_b32 v46, v62, v63 offset1:1
	v_pk_mul_f32 v[62:63], v[106:107], s[8:9] op_sel_hi:[1,0]
	ds_write2_b32 v47, v62, v63 offset1:1
	v_pk_mul_f32 v[62:63], v[108:109], s[8:9] op_sel_hi:[1,0]
	ds_write2_b32 v48, v62, v63 offset1:1
	v_pk_mul_f32 v[62:63], v[110:111], s[8:9] op_sel_hi:[1,0]
	ds_write2_b32 v49, v62, v63 offset1:1
	v_pk_mul_f32 v[62:63], v[112:113], s[8:9] op_sel_hi:[1,0]
	ds_write2_b32 v50, v62, v63 offset1:1
	v_pk_mul_f32 v[62:63], v[114:115], s[8:9] op_sel_hi:[1,0]
	ds_write2_b32 v51, v62, v63 offset1:1
	v_pk_mul_f32 v[62:63], v[116:117], s[8:9] op_sel_hi:[1,0]
	ds_write2_b32 v52, v62, v63 offset1:1
	v_pk_mul_f32 v[62:63], v[118:119], s[8:9] op_sel_hi:[1,0]
	ds_write2_b32 v53, v62, v63 offset1:1
	v_pk_mul_f32 v[62:63], v[120:121], s[8:9] op_sel_hi:[1,0]
	ds_write2_b32 v54, v62, v63 offset1:1
	v_pk_mul_f32 v[62:63], v[122:123], s[8:9] op_sel_hi:[1,0]
	ds_write2_b32 v55, v62, v63 offset1:1
	v_pk_mul_f32 v[62:63], v[124:125], s[8:9] op_sel_hi:[1,0]
	ds_write2_b32 v56, v62, v63 offset1:1
	s_waitcnt lgkmcnt(0)
	ds_read_b32 v9, v14
	ds_read_b32 v62, v14 offset:260
	ds_read_b32 v63, v14 offset:520
	ds_read_b32 v64, v14 offset:780
	ds_read_b32 v65, v14 offset:1040
	ds_read_b32 v66, v14 offset:1300
	ds_read_b32 v67, v14 offset:1560
	ds_read_b32 v68, v14 offset:1820
	s_waitcnt lgkmcnt(7)
	v_med3_f32 v9, v9, s51, v57
	s_waitcnt lgkmcnt(6)
	v_med3_f32 v69, v62, s51, v57
	v_mov_b32_e32 v62, v3
	v_cvt_pk_fp8_f32 v62, v9, v69
	s_waitcnt lgkmcnt(5)
	v_med3_f32 v9, v63, s51, v57
	s_waitcnt lgkmcnt(3)
	v_med3_f32 v65, v65, s51, v57
	s_waitcnt lgkmcnt(2)
	v_med3_f32 v66, v66, s51, v57
	v_mov_b32_e32 v63, v3
	v_cvt_pk_fp8_f32 v63, v65, v66
	v_med3_f32 v64, v64, s51, v57
	v_cvt_pk_fp8_f32 v62, v9, v64 op_sel:[0,0,1]
	s_waitcnt lgkmcnt(1)
	v_med3_f32 v9, v67, s51, v57
	s_waitcnt lgkmcnt(0)
	v_med3_f32 v64, v68, s51, v57
	v_cvt_pk_fp8_f32 v63, v9, v64 op_sel:[0,0,1]
	ds_read_b32 v9, v14 offset:2080
	ds_read_b32 v64, v14 offset:2340
	ds_read_b32 v65, v14 offset:2600
	ds_read_b32 v66, v14 offset:2860
	ds_read_b32 v67, v14 offset:3120
	ds_read_b32 v68, v14 offset:3380
	ds_read_b32 v69, v14 offset:3640
	ds_read_b32 v70, v14 offset:3900
	s_waitcnt lgkmcnt(7)
	v_med3_f32 v9, v9, s51, v57
	s_waitcnt lgkmcnt(6)
	v_med3_f32 v71, v64, s51, v57
	v_mov_b32_e32 v64, v3
	v_cvt_pk_fp8_f32 v64, v9, v71
	s_waitcnt lgkmcnt(5)
	v_med3_f32 v9, v65, s51, v57
	s_waitcnt lgkmcnt(3)
	v_med3_f32 v67, v67, s51, v57
	s_waitcnt lgkmcnt(2)
	v_med3_f32 v68, v68, s51, v57
	v_mov_b32_e32 v65, v3
	v_cvt_pk_fp8_f32 v65, v67, v68
	v_med3_f32 v66, v66, s51, v57
	v_cvt_pk_fp8_f32 v64, v9, v66 op_sel:[0,0,1]
	s_waitcnt lgkmcnt(1)
	v_med3_f32 v9, v69, s51, v57
	s_waitcnt lgkmcnt(0)
	v_med3_f32 v66, v70, s51, v57
	v_cvt_pk_fp8_f32 v65, v9, v66 op_sel:[0,0,1]
	v_or_b32_e32 v9, s63, v12
	v_lshlrev_b32_e32 v9, 7, v9
	v_and_b32_e32 v66, 0x6780, v9
	v_mov_b32_e32 v67, v3
	v_lshl_add_u64 v[66:67], s[10:11], 0, v[66:67]
	v_lshl_add_u64 v[66:67], v[66:67], 0, v[2:3]
	global_store_dwordx4 v[66:67], v[62:65], off nt
	ds_read_b32 v9, v14 offset:64
	ds_read_b32 v62, v14 offset:324
	ds_read_b32 v63, v14 offset:584
	ds_read_b32 v64, v14 offset:844
	ds_read_b32 v65, v14 offset:1104
	ds_read_b32 v66, v14 offset:1364
	ds_read_b32 v67, v14 offset:1624
	ds_read_b32 v68, v14 offset:1884
	s_waitcnt lgkmcnt(0)
	v_med3_f32 v9, v9, s51, v57
	v_med3_f32 v69, v62, s51, v57
	v_mov_b32_e32 v62, v3
	v_cvt_pk_fp8_f32 v62, v9, v69
	v_med3_f32 v9, v63, s51, v57
	v_med3_f32 v65, v65, s51, v57
	v_med3_f32 v66, v66, s51, v57
	v_mov_b32_e32 v63, v3
	v_cvt_pk_fp8_f32 v63, v65, v66
	v_med3_f32 v64, v64, s51, v57
	v_cvt_pk_fp8_f32 v62, v9, v64 op_sel:[0,0,1]
	v_med3_f32 v9, v67, s51, v57
	v_med3_f32 v64, v68, s51, v57
	v_cvt_pk_fp8_f32 v63, v9, v64 op_sel:[0,0,1]
	ds_read_b32 v9, v14 offset:2144
	ds_read_b32 v64, v14 offset:2404
	ds_read_b32 v65, v14 offset:2664
	ds_read_b32 v66, v14 offset:2924
	ds_read_b32 v67, v14 offset:3184
	ds_read_b32 v68, v14 offset:3444
	ds_read_b32 v69, v14 offset:3704
	ds_read_b32 v70, v14 offset:3964
	s_waitcnt lgkmcnt(0)
; #define LAS __attribute__((address_space(3)))
; __device__ __forceinline__ unsigned pk4_fp8(float a, float b, float c, float d) { int w = 0; w = __builtin_amdgcn_cvt_pk_fp8_f32(clamp8(a), clamp8(b), w, false); w = __builtin_amdgcn_cvt_pk_fp8_f32(clamp8(c), clamp8(d), w, true); return (unsigned)w; }
; #define LDS_WAIT() asm volatile("s_waitcnt lgkmcnt(0)" ::: "memory")
; __host__ __device__ __forceinline__ size_t tiled_off(size_t r, int kb, int ktiles) { return (((r >> 8) * ktiles + (kb >> 7)) << 15) + ((r & 255) << 7) + (kb & 127); }
;     ...
;     const int c = lane & 3;
; #pragma unroll
;     for (int j = 0; j < 4; ++j) { const int n = (lane >> 2) + 16 * j; const LAS float* s = scr + (16 * c) * 65 + n;
;         u32x4 o; o.x = pk4_fp8(s[0 * 65], s[1 * 65], s[2 * 65], s[3 * 65]); o.y = pk4_fp8(s[4 * 65], s[5 * 65], s[6 * 65], s[7 * 65]);
;         o.z = pk4_fp8(s[8 * 65], s[9 * 65], s[10 * 65], s[11 * 65]); o.w = pk4_fp8(s[12 * 65], s[13 * 65], s[14 * 65], s[15 * 65]);
;         const int nn = n0 + n; const int row = MAP == 0 ? nn : ((nn >> 7) * 256 + (nn & 127) + (MAP == 2 ? 128 : 0));
;         __builtin_nontemporal_store(o, (u32x4*)(WT + (pitch < 0 ? tiled_off((size_t)row, k0 + 16 * c, pitch == -1 ? (K >> 7) : -pitch) : (size_t)row * (pitch ? pitch : K) + k0 + 16 * c))); }
;     LDS_WAIT(); asm volatile("" ::: "memory");
	v_med3_f32 v9, v9, s51, v57
	v_med3_f32 v71, v64, s51, v57
	v_mov_b32_e32 v64, v3
	v_cvt_pk_fp8_f32 v64, v9, v71
	v_med3_f32 v9, v65, s51, v57
	v_med3_f32 v67, v67, s51, v57
	v_med3_f32 v68, v68, s51, v57
	v_mov_b32_e32 v65, v3
	v_cvt_pk_fp8_f32 v65, v67, v68
	v_med3_f32 v66, v66, s51, v57
	v_cvt_pk_fp8_f32 v64, v9, v66 op_sel:[0,0,1]
	v_med3_f32 v9, v69, s51, v57
	v_med3_f32 v66, v70, s51, v57
	v_cvt_pk_fp8_f32 v65, v9, v66 op_sel:[0,0,1]
	v_or_b32_e32 v9, s63, v15
	v_lshlrev_b32_e32 v9, 7, v9
	v_and_b32_e32 v66, 0x6f80, v9
	v_mov_b32_e32 v67, v3
	v_lshl_add_u64 v[66:67], s[10:11], 0, v[66:67]
	v_lshl_add_u64 v[66:67], v[66:67], 0, v[2:3]
	global_store_dwordx4 v[66:67], v[62:65], off nt
	ds_read_b32 v9, v14 offset:128
	ds_read_b32 v62, v14 offset:388
	ds_read_b32 v63, v14 offset:648
	ds_read_b32 v64, v14 offset:908
	ds_read_b32 v65, v14 offset:1168
	ds_read_b32 v66, v14 offset:1428
	ds_read_b32 v67, v14 offset:1688
	ds_read_b32 v68, v14 offset:1948
	s_waitcnt lgkmcnt(0)
	v_med3_f32 v9, v9, s51, v57
	v_med3_f32 v69, v62, s51, v57
	v_mov_b32_e32 v62, v3
	v_cvt_pk_fp8_f32 v62, v9, v69
	v_med3_f32 v9, v63, s51, v57
	v_med3_f32 v65, v65, s51, v57
	v_med3_f32 v66, v66, s51, v57
	v_mov_b32_e32 v63, v3
	v_cvt_pk_fp8_f32 v63, v65, v66
	v_med3_f32 v64, v64, s51, v57
	v_cvt_pk_fp8_f32 v62, v9, v64 op_sel:[0,0,1]
	v_med3_f32 v9, v67, s51, v57
	v_med3_f32 v64, v68, s51, v57
	v_cvt_pk_fp8_f32 v63, v9, v64 op_sel:[0,0,1]
	ds_read_b32 v9, v14 offset:2208
	ds_read_b32 v64, v14 offset:2468
	ds_read_b32 v65, v14 offset:2728
	ds_read_b32 v66, v14 offset:2988
	ds_read_b32 v67, v14 offset:3248
	ds_read_b32 v68, v14 offset:3508
	ds_read_b32 v69, v14 offset:3768
	ds_read_b32 v70, v14 offset:4028
	s_waitcnt lgkmcnt(0)
	v_med3_f32 v9, v9, s51, v57
	v_med3_f32 v71, v64, s51, v57
	v_mov_b32_e32 v64, v3
	v_cvt_pk_fp8_f32 v64, v9, v71
	v_med3_f32 v9, v65, s51, v57
	v_med3_f32 v67, v67, s51, v57
	v_med3_f32 v68, v68, s51, v57
	v_mov_b32_e32 v65, v3
	v_cvt_pk_fp8_f32 v65, v67, v68
	v_med3_f32 v66, v66, s51, v57
	v_cvt_pk_fp8_f32 v64, v9, v66 op_sel:[0,0,1]
	v_med3_f32 v9, v69, s51, v57
	v_med3_f32 v66, v70, s51, v57
	v_cvt_pk_fp8_f32 v65, v9, v66 op_sel:[0,0,1]
	v_or_b32_e32 v9, s63, v16
	v_lshlrev_b32_e32 v9, 7, v9
	v_and_b32_e32 v66, 0x7780, v9
	v_mov_b32_e32 v67, v3
	v_lshl_add_u64 v[66:67], s[10:11], 0, v[66:67]
	v_lshl_add_u64 v[66:67], v[66:67], 0, v[2:3]
	global_store_dwordx4 v[66:67], v[62:65], off nt
	ds_read_b32 v9, v14 offset:192
	ds_read_b32 v62, v14 offset:452
	ds_read_b32 v63, v14 offset:712
	ds_read_b32 v64, v14 offset:972
	ds_read_b32 v65, v14 offset:1232
	ds_read_b32 v66, v14 offset:1492
	ds_read_b32 v67, v14 offset:1752
	ds_read_b32 v68, v14 offset:2012
	s_waitcnt lgkmcnt(0)
	v_med3_f32 v9, v9, s51, v57
	v_med3_f32 v69, v62, s51, v57
	v_mov_b32_e32 v62, v3
	v_cvt_pk_fp8_f32 v62, v9, v69
	v_med3_f32 v9, v63, s51, v57
	v_med3_f32 v65, v65, s51, v57
	v_med3_f32 v66, v66, s51, v57
	v_mov_b32_e32 v63, v3
	v_cvt_pk_fp8_f32 v63, v65, v66
	v_med3_f32 v64, v64, s51, v57
	v_cvt_pk_fp8_f32 v62, v9, v64 op_sel:[0,0,1]
	v_med3_f32 v9, v67, s51, v57
	v_med3_f32 v64, v68, s51, v57
	v_cvt_pk_fp8_f32 v63, v9, v64 op_sel:[0,0,1]
	ds_read_b32 v9, v14 offset:2272
	ds_read_b32 v64, v14 offset:2532
	ds_read_b32 v65, v14 offset:2792
	ds_read_b32 v66, v14 offset:3052
	ds_read_b32 v67, v14 offset:3312
	ds_read_b32 v68, v14 offset:3572
	ds_read_b32 v69, v14 offset:3832
	ds_read_b32 v70, v14 offset:4092
	s_waitcnt lgkmcnt(0)
	v_med3_f32 v9, v9, s51, v57
	v_med3_f32 v71, v64, s51, v57
	v_mov_b32_e32 v64, v3
	v_cvt_pk_fp8_f32 v64, v9, v71
	v_med3_f32 v9, v65, s51, v57
	v_med3_f32 v67, v67, s51, v57
	v_med3_f32 v68, v68, s51, v57
	v_mov_b32_e32 v65, v3
	v_cvt_pk_fp8_f32 v65, v67, v68
	v_med3_f32 v66, v66, s51, v57
	v_cvt_pk_fp8_f32 v64, v9, v66 op_sel:[0,0,1]
	v_med3_f32 v9, v69, s51, v57
	v_med3_f32 v66, v70, s51, v57
	v_cvt_pk_fp8_f32 v65, v9, v66 op_sel:[0,0,1]
	v_or_b32_e32 v9, s63, v17
	v_lshlrev_b32_e32 v9, 7, v9
	v_and_b32_e32 v66, 0x7f80, v9
	v_mov_b32_e32 v67, v3
	v_lshl_add_u64 v[66:67], s[10:11], 0, v[66:67]
	v_lshl_add_u64 v[66:67], v[66:67], 0, v[2:3]
	global_store_dwordx4 v[66:67], v[62:65], off nt
	s_waitcnt lgkmcnt(0)

; #define LAS __attribute__((address_space(3)))
; __device__ __forceinline__ unsigned pk4_fp8(float a, float b, float c, float d) { int w = 0; w = __builtin_amdgcn_cvt_pk_fp8_f32(clamp8(a), clamp8(b), w, false); w = __builtin_amdgcn_cvt_pk_fp8_f32(clamp8(c), clamp8(d), w, true); return (unsigned)w; }
; #define LDS_WAIT() asm volatile("s_waitcnt lgkmcnt(0)" ::: "memory")
; __host__ __device__ __forceinline__ size_t tiled_off(size_t r, int kb, int ktiles) { return (((r >> 8) * ktiles + (kb >> 7)) << 15) + ((r & 255) << 7) + (kb & 127); }
; #define AIN(i) ((const float*)ldp(lds, (i)))
;     const int nblk = N / 64, kb = item / nblk, nb = item % nblk, k0 = 64 * kb, n0 = 64 * nb;
;     const int kr = lane >> 4, nc = (lane & 15) * 4;
;     const float* src = W + (size_t)(k0 + kr) * N + n0 + nc;
;     f32x4 v[16];
; #pragma unroll
;     for (int i = 0; i < 16; ++i) v[i] = __builtin_nontemporal_load((const f32x4*)(src + (size_t)(4 * i) * N));
; #pragma unroll
;     for (int i = 0; i < 16; ++i) { LAS float* d = scr + (4 * i + kr) * 65 + nc; d[0] = v[i].x * W8_SCALE; d[1] = v[i].y * W8_SCALE; d[2] = v[i].z * W8_SCALE; d[3] = v[i].w * W8_SCALE; }
;     LDS_WAIT(); asm volatile("" ::: "memory");
;     const int c = lane & 3;
; #pragma unroll
;     for (int j = 0; j < 4; ++j) { const int n = (lane >> 2) + 16 * j; const LAS float* s = scr + (16 * c) * 65 + n;
;         u32x4 o; o.x = pk4_fp8(s[0 * 65], s[1 * 65], s[2 * 65], s[3 * 65]); o.y = pk4_fp8(s[4 * 65], s[5 * 65], s[6 * 65], s[7 * 65]);
;         o.z = pk4_fp8(s[8 * 65], s[9 * 65], s[10 * 65], s[11 * 65]); o.w = pk4_fp8(s[12 * 65], s[13 * 65], s[14 * 65], s[15 * 65]);
;         const int nn = n0 + n; const int row = MAP == 0 ? nn : ((nn >> 7) * 256 + (nn & 127) + (MAP == 2 ? 128 : 0));
;         __builtin_nontemporal_store(o, (u32x4*)(WT + (pitch < 0 ? tiled_off((size_t)row, k0 + 16 * c, pitch == -1 ? (K >> 7) : -pitch) : (size_t)row * (pitch ? pitch : K) + k0 + 16 * c))); }
;     LDS_WAIT(); asm volatile("" ::: "memory");
; __device__ __forceinline__ void ph0(LAS unsigned char* lds, int tid, int lane, int wave, int G, int bid) {
;     ...
;             if (r < I_S) { transpose_item_f8<0>(AIN(IWS), SW, D, (unsigned char*)(ws + WS_WFT), scr, r, lane, -(SW + FW) / 128); continue; } r -= I_S;
.LBB0_135:
	s_andn2_b64 vcc, exec, s[10:11]
	s_cbranch_vccnz .LBB0_137
	v_mov_b32_e32 v2, s74
	ds_read_b32 v2, v2
	v_mov_b32_e32 v9, s75
	ds_read_b32 v9, v9
	s_bfe_u32 s0, s93, 0x30005
	s_lshl_b32 s60, s0, 6
	s_waitcnt lgkmcnt(0)
	v_readfirstlane_b32 s94, v2
	s_lshl_b32 s11, s93, 6
	v_or_b32_e32 v2, s60, v10
	v_readfirstlane_b32 s95, v9
	s_and_b32 s10, s11, 0x7c0
	v_lshlrev_b32_e32 v2, 13, v2
	v_lshl_add_u64 v[62:63], s[94:95], 0, v[2:3]
	s_lshl_b32 s0, s10, 2
	v_lshl_add_u64 v[62:63], v[62:63], 0, s[0:1]
	v_mov_b32_e32 v9, v3
	v_lshl_add_u64 v[122:123], v[62:63], 0, v[8:9]
	v_add_co_u32_e32 v66, vcc, s28, v122
	s_lshr_b32 s0, s93, 5
	s_nop 0
	v_addc_co_u32_e32 v67, vcc, 0, v123, vcc
	global_load_dwordx4 v[62:65], v[122:123], off nt
	s_nop 0
	global_load_dwordx4 v[66:69], v[66:67], off nt
	v_add_co_u32_e32 v70, vcc, s29, v122
	s_bfe_u32 s11, s11, 0x30008
	s_nop 0
	v_addc_co_u32_e32 v71, vcc, 0, v123, vcc
	v_add_co_u32_e32 v74, vcc, s30, v122
	s_bfe_u32 s0, s0, 0x20001
	s_nop 0
	v_addc_co_u32_e32 v75, vcc, 0, v123, vcc
	global_load_dwordx4 v[70:73], v[70:71], off nt
	s_nop 0
	global_load_dwordx4 v[74:77], v[74:75], off nt
	v_add_co_u32_e32 v78, vcc, s31, v122
	v_and_or_b32 v2, s60, 64, v13
	s_nop 0
	v_addc_co_u32_e32 v79, vcc, 0, v123, vcc
	v_add_co_u32_e32 v82, vcc, s40, v122
	s_nop 1
	v_addc_co_u32_e32 v83, vcc, 0, v123, vcc
	global_load_dwordx4 v[78:81], v[78:79], off nt
	s_nop 0
	global_load_dwordx4 v[82:85], v[82:83], off nt
	v_add_co_u32_e32 v86, vcc, s41, v122
	s_nop 1
	v_addc_co_u32_e32 v87, vcc, 0, v123, vcc
	v_add_co_u32_e32 v90, vcc, s42, v122
	s_nop 1
	v_addc_co_u32_e32 v91, vcc, 0, v123, vcc
	global_load_dwordx4 v[86:89], v[86:87], off nt
	s_nop 0
	global_load_dwordx4 v[90:93], v[90:91], off nt
	v_add_co_u32_e32 v94, vcc, s43, v122
	s_nop 1
	v_addc_co_u32_e32 v95, vcc, 0, v123, vcc
	v_add_co_u32_e32 v98, vcc, s44, v122
	s_nop 1
	v_addc_co_u32_e32 v99, vcc, 0, v123, vcc
	global_load_dwordx4 v[94:97], v[94:95], off nt
	s_nop 0
	global_load_dwordx4 v[98:101], v[98:99], off nt
	v_add_co_u32_e32 v102, vcc, s45, v122
	s_nop 1
	v_addc_co_u32_e32 v103, vcc, 0, v123, vcc
	v_add_co_u32_e32 v106, vcc, s46, v122
	s_nop 1
	v_addc_co_u32_e32 v107, vcc, 0, v123, vcc
	global_load_dwordx4 v[102:105], v[102:103], off nt
	s_nop 0
	global_load_dwordx4 v[106:109], v[106:107], off nt
	v_add_co_u32_e32 v110, vcc, s47, v122
	s_nop 1
	v_addc_co_u32_e32 v111, vcc, 0, v123, vcc
	global_load_dwordx4 v[110:113], v[110:111], off nt
	v_add_co_u32_e32 v114, vcc, s48, v122
	s_nop 1
	v_addc_co_u32_e32 v115, vcc, 0, v123, vcc
	global_load_dwordx4 v[114:117], v[114:115], off nt
	v_add_co_u32_e32 v118, vcc, s49, v122
	s_nop 1
	v_addc_co_u32_e32 v119, vcc, 0, v123, vcc
	global_load_dwordx4 v[118:121], v[118:119], off nt
	v_add_co_u32_e32 v122, vcc, s50, v122
	s_nop 1
	v_addc_co_u32_e32 v123, vcc, 0, v123, vcc
	global_load_dwordx4 v[122:125], v[122:123], off nt
	s_waitcnt vmcnt(15)
	v_pk_mul_f32 v[62:63], v[62:63], s[8:9] op_sel_hi:[1,0]
	ds_write2_b32 v11, v62, v63 offset1:1
	v_pk_mul_f32 v[62:63], v[64:65], s[8:9] op_sel_hi:[1,0]
	ds_write2_b32 v11, v62, v63 offset0:2 offset1:3
	s_waitcnt vmcnt(14)
	v_pk_mul_f32 v[62:63], v[66:67], s[8:9] op_sel_hi:[1,0]
	ds_write2_b32 v27, v62, v63 offset1:1
	v_pk_mul_f32 v[62:63], v[68:69], s[8:9] op_sel_hi:[1,0]
	ds_write2_b32 v28, v62, v63 offset1:1
	s_waitcnt vmcnt(13)
	v_pk_mul_f32 v[62:63], v[70:71], s[8:9] op_sel_hi:[1,0]
	ds_write2_b32 v29, v62, v63 offset1:1
	v_pk_mul_f32 v[62:63], v[72:73], s[8:9] op_sel_hi:[1,0]
	ds_write2_b32 v30, v62, v63 offset1:1
	s_waitcnt vmcnt(12)
	v_pk_mul_f32 v[62:63], v[74:75], s[8:9] op_sel_hi:[1,0]
	ds_write2_b32 v31, v62, v63 offset1:1
	v_pk_mul_f32 v[62:63], v[76:77], s[8:9] op_sel_hi:[1,0]
	ds_write2_b32 v32, v62, v63 offset1:1
	s_waitcnt vmcnt(0) lgkmcnt(0)
	v_pk_mul_f32 v[62:63], v[78:79], s[8:9] op_sel_hi:[1,0]
	ds_write2_b32 v33, v62, v63 offset1:1
	v_pk_mul_f32 v[62:63], v[80:81], s[8:9] op_sel_hi:[1,0]
	ds_write2_b32 v34, v62, v63 offset1:1
	v_pk_mul_f32 v[62:63], v[82:83], s[8:9] op_sel_hi:[1,0]
	ds_write2_b32 v35, v62, v63 offset1:1
	v_pk_mul_f32 v[62:63], v[84:85], s[8:9] op_sel_hi:[1,0]
	ds_write2_b32 v36, v62, v63 offset1:1
	v_pk_mul_f32 v[62:63], v[86:87], s[8:9] op_sel_hi:[1,0]
	ds_write2_b32 v37, v62, v63 offset1:1
	v_pk_mul_f32 v[62:63], v[88:89], s[8:9] op_sel_hi:[1,0]
	ds_write2_b32 v38, v62, v63 offset1:1
	v_pk_mul_f32 v[62:63], v[90:91], s[8:9] op_sel_hi:[1,0]
	ds_write2_b32 v39, v62, v63 offset1:1
	v_pk_mul_f32 v[62:63], v[92:93], s[8:9] op_sel_hi:[1,0]
	ds_write2_b32 v40, v62, v63 offset1:1
	v_pk_mul_f32 v[62:63], v[94:95], s[8:9] op_sel_hi:[1,0]
	ds_write2_b32 v41, v62, v63 offset1:1
	v_pk_mul_f32 v[62:63], v[96:97], s[8:9] op_sel_hi:[1,0]
	ds_write2_b32 v42, v62, v63 offset1:1
	v_pk_mul_f32 v[62:63], v[98:99], s[8:9] op_sel_hi:[1,0]
	ds_write2_b32 v43, v62, v63 offset1:1
	v_pk_mul_f32 v[62:63], v[100:101], s[8:9] op_sel_hi:[1,0]
	ds_write2_b32 v44, v62, v63 offset1:1
	v_pk_mul_f32 v[62:63], v[102:103], s[8:9] op_sel_hi:[1,0]
	ds_write2_b32 v45, v62, v63 offset1:1
	v_pk_mul_f32 v[62:63], v[104:105], s[8:9] op_sel_hi:[1,0]
	ds_write2_b32 v46, v62, v63 offset1:1
	v_pk_mul_f32 v[62:63], v[106:107], s[8:9] op_sel_hi:[1,0]
	ds_write2_b32 v47, v62, v63 offset1:1
	v_pk_mul_f32 v[62:63], v[108:109], s[8:9] op_sel_hi:[1,0]
	ds_write2_b32 v48, v62, v63 offset1:1
	v_pk_mul_f32 v[62:63], v[110:111], s[8:9] op_sel_hi:[1,0]
	ds_write2_b32 v49, v62, v63 offset1:1
	v_pk_mul_f32 v[62:63], v[112:113], s[8:9] op_sel_hi:[1,0]
	ds_write2_b32 v50, v62, v63 offset1:1
	v_pk_mul_f32 v[62:63], v[114:115], s[8:9] op_sel_hi:[1,0]
	ds_write2_b32 v51, v62, v63 offset1:1
	v_pk_mul_f32 v[62:63], v[116:117], s[8:9] op_sel_hi:[1,0]
	ds_write2_b32 v52, v62, v63 offset1:1
	v_pk_mul_f32 v[62:63], v[118:119], s[8:9] op_sel_hi:[1,0]
	ds_write2_b32 v53, v62, v63 offset1:1
	v_pk_mul_f32 v[62:63], v[120:121], s[8:9] op_sel_hi:[1,0]
	ds_write2_b32 v54, v62, v63 offset1:1
	v_pk_mul_f32 v[62:63], v[122:123], s[8:9] op_sel_hi:[1,0]
	ds_write2_b32 v55, v62, v63 offset1:1
	v_pk_mul_f32 v[62:63], v[124:125], s[8:9] op_sel_hi:[1,0]
	ds_write2_b32 v56, v62, v63 offset1:1
	s_waitcnt lgkmcnt(0)
; #define LAS __attribute__((address_space(3)))
; __device__ __forceinline__ unsigned pk4_fp8(float a, float b, float c, float d) { int w = 0; w = __builtin_amdgcn_cvt_pk_fp8_f32(clamp8(a), clamp8(b), w, false); w = __builtin_amdgcn_cvt_pk_fp8_f32(clamp8(c), clamp8(d), w, true); return (unsigned)w; }
; #define LDS_WAIT() asm volatile("s_waitcnt lgkmcnt(0)" ::: "memory")
; __host__ __device__ __forceinline__ size_t tiled_off(size_t r, int kb, int ktiles) { return (((r >> 8) * ktiles + (kb >> 7)) << 15) + ((r & 255) << 7) + (kb & 127); }
;     ...
;     for (int i = 0; i < 16; ++i) { LAS float* d = scr + (4 * i + kr) * 65 + nc; d[0] = v[i].x * W8_SCALE; d[1] = v[i].y * W8_SCALE; d[2] = v[i].z * W8_SCALE; d[3] = v[i].w * W8_SCALE; }
;     LDS_WAIT(); asm volatile("" ::: "memory");
;     const int c = lane & 3;
; #pragma unroll
;     for (int j = 0; j < 4; ++j) { const int n = (lane >> 2) + 16 * j; const LAS float* s = scr + (16 * c) * 65 + n;
;         u32x4 o; o.x = pk4_fp8(s[0 * 65], s[1 * 65], s[2 * 65], s[3 * 65]); o.y = pk4_fp8(s[4 * 65], s[5 * 65], s[6 * 65], s[7 * 65]);
;         o.z = pk4_fp8(s[8 * 65], s[9 * 65], s[10 * 65], s[11 * 65]); o.w = pk4_fp8(s[12 * 65], s[13 * 65], s[14 * 65], s[15 * 65]);
;         const int nn = n0 + n; const int row = MAP == 0 ? nn : ((nn >> 7) * 256 + (nn & 127) + (MAP == 2 ? 128 : 0));
;         __builtin_nontemporal_store(o, (u32x4*)(WT + (pitch < 0 ? tiled_off((size_t)row, k0 + 16 * c, pitch == -1 ? (K >> 7) : -pitch) : (size_t)row * (pitch ? pitch : K) + k0 + 16 * c))); }
;     LDS_WAIT(); asm volatile("" ::: "memory");
	ds_read_b32 v9, v14
	ds_read_b32 v62, v14 offset:260
	ds_read_b32 v63, v14 offset:520
	ds_read_b32 v64, v14 offset:780
	ds_read_b32 v65, v14 offset:1040
	ds_read_b32 v66, v14 offset:1300
	ds_read_b32 v67, v14 offset:1560
	ds_read_b32 v68, v14 offset:1820
	s_waitcnt lgkmcnt(7)
	v_med3_f32 v9, v9, s51, v57
	s_waitcnt lgkmcnt(6)
	v_med3_f32 v69, v62, s51, v57
	v_mov_b32_e32 v62, v3
	v_cvt_pk_fp8_f32 v62, v9, v69
	s_waitcnt lgkmcnt(5)
	v_med3_f32 v9, v63, s51, v57
	s_waitcnt lgkmcnt(3)
	v_med3_f32 v65, v65, s51, v57
	s_waitcnt lgkmcnt(2)
	v_med3_f32 v66, v66, s51, v57
	v_mov_b32_e32 v63, v3
	v_cvt_pk_fp8_f32 v63, v65, v66
	v_med3_f32 v64, v64, s51, v57
	v_cvt_pk_fp8_f32 v62, v9, v64 op_sel:[0,0,1]
	s_waitcnt lgkmcnt(1)
	v_med3_f32 v9, v67, s51, v57
	s_waitcnt lgkmcnt(0)
	v_med3_f32 v64, v68, s51, v57
	v_cvt_pk_fp8_f32 v63, v9, v64 op_sel:[0,0,1]
	ds_read_b32 v9, v14 offset:2080
	ds_read_b32 v64, v14 offset:2340
	ds_read_b32 v65, v14 offset:2600
	ds_read_b32 v66, v14 offset:2860
	ds_read_b32 v67, v14 offset:3120
	ds_read_b32 v68, v14 offset:3380
	ds_read_b32 v69, v14 offset:3640
	ds_read_b32 v70, v14 offset:3900
	s_waitcnt lgkmcnt(7)
	v_med3_f32 v9, v9, s51, v57
	s_waitcnt lgkmcnt(6)
	v_med3_f32 v71, v64, s51, v57
	v_mov_b32_e32 v64, v3
	v_cvt_pk_fp8_f32 v64, v9, v71
	s_waitcnt lgkmcnt(5)
	v_med3_f32 v9, v65, s51, v57
	s_waitcnt lgkmcnt(3)
	v_med3_f32 v67, v67, s51, v57
	s_waitcnt lgkmcnt(2)
	v_med3_f32 v68, v68, s51, v57
	v_mov_b32_e32 v65, v3
	v_cvt_pk_fp8_f32 v65, v67, v68
	v_med3_f32 v66, v66, s51, v57
	v_cvt_pk_fp8_f32 v64, v9, v66 op_sel:[0,0,1]
	s_waitcnt lgkmcnt(1)
	v_med3_f32 v9, v69, s51, v57
	s_waitcnt lgkmcnt(0)
	v_med3_f32 v66, v70, s51, v57
	v_cvt_pk_fp8_f32 v65, v9, v66 op_sel:[0,0,1]
	v_or_b32_e32 v9, s10, v12
	v_lshlrev_b32_e32 v9, 7, v9
	v_and_b32_e32 v66, 0x6780, v9
	v_mul_u32_u24_e64 v9, s11, 12
	v_or_b32_e32 v9, s0, v9
	v_lshlrev_b32_e32 v68, 15, v9
	v_mov_b32_e32 v69, v3
	v_mov_b32_e32 v67, v3
	v_lshl_add_u64 v[68:69], s[4:5], 0, v[68:69]
	v_lshl_add_u64 v[66:67], v[68:69], 0, v[66:67]
	v_lshl_add_u64 v[66:67], v[66:67], 0, v[2:3]
	global_store_dwordx4 v[66:67], v[62:65], off nt
	ds_read_b32 v9, v14 offset:64
	ds_read_b32 v62, v14 offset:324
	ds_read_b32 v63, v14 offset:584
	ds_read_b32 v64, v14 offset:844
	ds_read_b32 v65, v14 offset:1104
	ds_read_b32 v66, v14 offset:1364
	ds_read_b32 v67, v14 offset:1624
	ds_read_b32 v70, v14 offset:1884
	s_waitcnt lgkmcnt(0)
	v_med3_f32 v9, v9, s51, v57
	v_med3_f32 v71, v62, s51, v57
	v_mov_b32_e32 v62, v3
	v_cvt_pk_fp8_f32 v62, v9, v71
	v_med3_f32 v9, v63, s51, v57
	v_med3_f32 v65, v65, s51, v57
	v_med3_f32 v66, v66, s51, v57
	v_mov_b32_e32 v63, v3
	v_cvt_pk_fp8_f32 v63, v65, v66
	v_med3_f32 v64, v64, s51, v57
	v_cvt_pk_fp8_f32 v62, v9, v64 op_sel:[0,0,1]
	v_med3_f32 v9, v67, s51, v57
	v_med3_f32 v64, v70, s51, v57
	v_cvt_pk_fp8_f32 v63, v9, v64 op_sel:[0,0,1]
	ds_read_b32 v9, v14 offset:2144
	ds_read_b32 v64, v14 offset:2404
	ds_read_b32 v65, v14 offset:2664
	ds_read_b32 v66, v14 offset:2924
	ds_read_b32 v67, v14 offset:3184
	ds_read_b32 v70, v14 offset:3444
	ds_read_b32 v71, v14 offset:3704
	ds_read_b32 v72, v14 offset:3964
	s_waitcnt lgkmcnt(0)
	v_med3_f32 v9, v9, s51, v57
	v_med3_f32 v73, v64, s51, v57
	v_mov_b32_e32 v64, v3
	v_cvt_pk_fp8_f32 v64, v9, v73
	v_med3_f32 v9, v65, s51, v57
	v_med3_f32 v67, v67, s51, v57
	v_med3_f32 v70, v70, s51, v57
	v_mov_b32_e32 v65, v3
	v_cvt_pk_fp8_f32 v65, v67, v70
	v_med3_f32 v66, v66, s51, v57
	v_cvt_pk_fp8_f32 v64, v9, v66 op_sel:[0,0,1]
	v_med3_f32 v9, v71, s51, v57
	v_med3_f32 v66, v72, s51, v57
	v_cvt_pk_fp8_f32 v65, v9, v66 op_sel:[0,0,1]
	v_or_b32_e32 v9, s10, v15
	v_lshlrev_b32_e32 v9, 7, v9
	v_and_b32_e32 v66, 0x6f80, v9
	v_mov_b32_e32 v67, v3
	v_lshl_add_u64 v[66:67], v[68:69], 0, v[66:67]
	v_lshl_add_u64 v[66:67], v[66:67], 0, v[2:3]
	global_store_dwordx4 v[66:67], v[62:65], off nt
	ds_read_b32 v9, v14 offset:128
	ds_read_b32 v62, v14 offset:388
	ds_read_b32 v63, v14 offset:648
	ds_read_b32 v64, v14 offset:908
	ds_read_b32 v65, v14 offset:1168
	ds_read_b32 v66, v14 offset:1428
	ds_read_b32 v67, v14 offset:1688
	ds_read_b32 v70, v14 offset:1948
	s_waitcnt lgkmcnt(0)
; #define LAS __attribute__((address_space(3)))
; __device__ __forceinline__ unsigned pk4_fp8(float a, float b, float c, float d) { int w = 0; w = __builtin_amdgcn_cvt_pk_fp8_f32(clamp8(a), clamp8(b), w, false); w = __builtin_amdgcn_cvt_pk_fp8_f32(clamp8(c), clamp8(d), w, true); return (unsigned)w; }
; #define LDS_WAIT() asm volatile("s_waitcnt lgkmcnt(0)" ::: "memory")
; __host__ __device__ __forceinline__ size_t tiled_off(size_t r, int kb, int ktiles) { return (((r >> 8) * ktiles + (kb >> 7)) << 15) + ((r & 255) << 7) + (kb & 127); }
;     ...
;     const int c = lane & 3;
; #pragma unroll
;     for (int j = 0; j < 4; ++j) { const int n = (lane >> 2) + 16 * j; const LAS float* s = scr + (16 * c) * 65 + n;
;         u32x4 o; o.x = pk4_fp8(s[0 * 65], s[1 * 65], s[2 * 65], s[3 * 65]); o.y = pk4_fp8(s[4 * 65], s[5 * 65], s[6 * 65], s[7 * 65]);
;         o.z = pk4_fp8(s[8 * 65], s[9 * 65], s[10 * 65], s[11 * 65]); o.w = pk4_fp8(s[12 * 65], s[13 * 65], s[14 * 65], s[15 * 65]);
;         const int nn = n0 + n; const int row = MAP == 0 ? nn : ((nn >> 7) * 256 + (nn & 127) + (MAP == 2 ? 128 : 0));
;         __builtin_nontemporal_store(o, (u32x4*)(WT + (pitch < 0 ? tiled_off((size_t)row, k0 + 16 * c, pitch == -1 ? (K >> 7) : -pitch) : (size_t)row * (pitch ? pitch : K) + k0 + 16 * c))); }
;     LDS_WAIT(); asm volatile("" ::: "memory");
	v_med3_f32 v9, v9, s51, v57
	v_med3_f32 v71, v62, s51, v57
	v_mov_b32_e32 v62, v3
	v_cvt_pk_fp8_f32 v62, v9, v71
	v_med3_f32 v9, v63, s51, v57
	v_med3_f32 v65, v65, s51, v57
	v_med3_f32 v66, v66, s51, v57
	v_mov_b32_e32 v63, v3
	v_cvt_pk_fp8_f32 v63, v65, v66
	v_med3_f32 v64, v64, s51, v57
	v_cvt_pk_fp8_f32 v62, v9, v64 op_sel:[0,0,1]
	v_med3_f32 v9, v67, s51, v57
	v_med3_f32 v64, v70, s51, v57
	v_cvt_pk_fp8_f32 v63, v9, v64 op_sel:[0,0,1]
	ds_read_b32 v9, v14 offset:2208
	ds_read_b32 v64, v14 offset:2468
	ds_read_b32 v65, v14 offset:2728
	ds_read_b32 v66, v14 offset:2988
	ds_read_b32 v67, v14 offset:3248
	ds_read_b32 v70, v14 offset:3508
	ds_read_b32 v71, v14 offset:3768
	ds_read_b32 v72, v14 offset:4028
	s_waitcnt lgkmcnt(0)
	v_med3_f32 v9, v9, s51, v57
	v_med3_f32 v73, v64, s51, v57
	v_mov_b32_e32 v64, v3
	v_cvt_pk_fp8_f32 v64, v9, v73
	v_med3_f32 v9, v65, s51, v57
	v_med3_f32 v67, v67, s51, v57
	v_med3_f32 v70, v70, s51, v57
	v_mov_b32_e32 v65, v3
	v_cvt_pk_fp8_f32 v65, v67, v70
	v_med3_f32 v66, v66, s51, v57
	v_cvt_pk_fp8_f32 v64, v9, v66 op_sel:[0,0,1]
	v_med3_f32 v9, v71, s51, v57
	v_med3_f32 v66, v72, s51, v57
	v_cvt_pk_fp8_f32 v65, v9, v66 op_sel:[0,0,1]
	v_or_b32_e32 v9, s10, v16
	v_lshlrev_b32_e32 v9, 7, v9
	v_and_b32_e32 v66, 0x7780, v9
	v_mov_b32_e32 v67, v3
	v_lshl_add_u64 v[66:67], v[68:69], 0, v[66:67]
	v_lshl_add_u64 v[66:67], v[66:67], 0, v[2:3]
	global_store_dwordx4 v[66:67], v[62:65], off nt
	ds_read_b32 v9, v14 offset:192
	ds_read_b32 v62, v14 offset:452
	ds_read_b32 v63, v14 offset:712
	ds_read_b32 v64, v14 offset:972
	ds_read_b32 v65, v14 offset:1232
	ds_read_b32 v66, v14 offset:1492
	ds_read_b32 v67, v14 offset:1752
	ds_read_b32 v70, v14 offset:2012
	s_waitcnt lgkmcnt(0)
	v_med3_f32 v9, v9, s51, v57
	v_med3_f32 v71, v62, s51, v57
	v_mov_b32_e32 v62, v3
	v_cvt_pk_fp8_f32 v62, v9, v71
	v_med3_f32 v9, v63, s51, v57
	v_med3_f32 v65, v65, s51, v57
	v_med3_f32 v66, v66, s51, v57
	v_mov_b32_e32 v63, v3
	v_cvt_pk_fp8_f32 v63, v65, v66
	v_med3_f32 v64, v64, s51, v57
	v_cvt_pk_fp8_f32 v62, v9, v64 op_sel:[0,0,1]
	v_med3_f32 v9, v67, s51, v57
	v_med3_f32 v64, v70, s51, v57
	v_cvt_pk_fp8_f32 v63, v9, v64 op_sel:[0,0,1]
	ds_read_b32 v9, v14 offset:2272
	ds_read_b32 v64, v14 offset:2532
	ds_read_b32 v65, v14 offset:2792
	ds_read_b32 v66, v14 offset:3052
	ds_read_b32 v67, v14 offset:3312
	ds_read_b32 v70, v14 offset:3572
	ds_read_b32 v71, v14 offset:3832
	ds_read_b32 v72, v14 offset:4092
	s_waitcnt lgkmcnt(0)
	v_med3_f32 v9, v9, s51, v57
	v_med3_f32 v73, v64, s51, v57
	v_mov_b32_e32 v64, v3
	v_cvt_pk_fp8_f32 v64, v9, v73
	v_med3_f32 v9, v65, s51, v57
	v_med3_f32 v67, v67, s51, v57
	v_med3_f32 v70, v70, s51, v57
	v_mov_b32_e32 v65, v3
	v_cvt_pk_fp8_f32 v65, v67, v70
	v_med3_f32 v66, v66, s51, v57
	v_cvt_pk_fp8_f32 v64, v9, v66 op_sel:[0,0,1]
	v_med3_f32 v9, v71, s51, v57
	v_med3_f32 v66, v72, s51, v57
	v_cvt_pk_fp8_f32 v65, v9, v66 op_sel:[0,0,1]
	v_or_b32_e32 v9, s10, v17
	v_lshlrev_b32_e32 v9, 7, v9
	v_and_b32_e32 v66, 0x7f80, v9
	v_mov_b32_e32 v67, v3
	v_lshl_add_u64 v[66:67], v[68:69], 0, v[66:67]
	v_lshl_add_u64 v[66:67], v[66:67], 0, v[2:3]
	global_store_dwordx4 v[66:67], v[62:65], off nt
	s_waitcnt lgkmcnt(0)

; #define LAS __attribute__((address_space(3)))
; __device__ __forceinline__ unsigned pk4_fp8(float a, float b, float c, float d) { int w = 0; w = __builtin_amdgcn_cvt_pk_fp8_f32(clamp8(a), clamp8(b), w, false); w = __builtin_amdgcn_cvt_pk_fp8_f32(clamp8(c), clamp8(d), w, true); return (unsigned)w; }
; #define LDS_WAIT() asm volatile("s_waitcnt lgkmcnt(0)" ::: "memory")
; __host__ __device__ __forceinline__ size_t tiled_off(size_t r, int kb, int ktiles) { return (((r >> 8) * ktiles + (kb >> 7)) << 15) + ((r & 255) << 7) + (kb & 127); }
; #define AIN(i) ((const float*)ldp(lds, (i)))
;     const int nblk = N / 64, kb = item / nblk, nb = item % nblk, k0 = 64 * kb, n0 = 64 * nb;
;     const int kr = lane >> 4, nc = (lane & 15) * 4;
;     const float* src = W + (size_t)(k0 + kr) * N + n0 + nc;
;     f32x4 v[16];
; #pragma unroll
;     for (int i = 0; i < 16; ++i) v[i] = __builtin_nontemporal_load((const f32x4*)(src + (size_t)(4 * i) * N));
; #pragma unroll
;     for (int i = 0; i < 16; ++i) { LAS float* d = scr + (4 * i + kr) * 65 + nc; d[0] = v[i].x * W8_SCALE; d[1] = v[i].y * W8_SCALE; d[2] = v[i].z * W8_SCALE; d[3] = v[i].w * W8_SCALE; }
;     LDS_WAIT(); asm volatile("" ::: "memory");
;     const int c = lane & 3;
; #pragma unroll
;     for (int j = 0; j < 4; ++j) { const int n = (lane >> 2) + 16 * j; const LAS float* s = scr + (16 * c) * 65 + n;
;         u32x4 o; o.x = pk4_fp8(s[0 * 65], s[1 * 65], s[2 * 65], s[3 * 65]); o.y = pk4_fp8(s[4 * 65], s[5 * 65], s[6 * 65], s[7 * 65]);
;         o.z = pk4_fp8(s[8 * 65], s[9 * 65], s[10 * 65], s[11 * 65]); o.w = pk4_fp8(s[12 * 65], s[13 * 65], s[14 * 65], s[15 * 65]);
;         const int nn = n0 + n; const int row = MAP == 0 ? nn : ((nn >> 7) * 256 + (nn & 127) + (MAP == 2 ? 128 : 0));
;         __builtin_nontemporal_store(o, (u32x4*)(WT + (pitch < 0 ? tiled_off((size_t)row, k0 + 16 * c, pitch == -1 ? (K >> 7) : -pitch) : (size_t)row * (pitch ? pitch : K) + k0 + 16 * c))); }
;     LDS_WAIT(); asm volatile("" ::: "memory");
; __device__ __forceinline__ void ph0(LAS unsigned char* lds, int tid, int lane, int wave, int G, int bid) {
;     ...
;             if (r < I_F) { transpose_item_f8<0>(AIN(IWF), FW, D, (unsigned char*)(ws + WS_WFT) + ((size_t)(SW / 128) << 15), scr, r, lane, -(SW + FW) / 128); continue; } r -= I_F;
.LBB0_138:
	s_andn2_b64 vcc, exec, s[10:11]
	s_cbranch_vccnz .LBB0_140
	v_mov_b32_e32 v2, s76
	ds_read_b32 v2, v2
	v_mov_b32_e32 v9, s77
	ds_read_b32 v9, v9
	s_bfe_u32 s0, s92, 0xb0005
	s_lshl_b32 s60, s0, 6
	s_waitcnt lgkmcnt(0)
	v_readfirstlane_b32 s94, v2
	s_lshl_b32 s11, s92, 6
	v_or_b32_e32 v2, s60, v10
	v_readfirstlane_b32 s95, v9
	s_and_b32 s10, s11, 0x7c0
	v_lshlrev_b32_e32 v2, 13, v2
	v_lshl_add_u64 v[62:63], s[94:95], 0, v[2:3]
	s_lshl_b32 s0, s10, 2
	v_lshl_add_u64 v[62:63], v[62:63], 0, s[0:1]
	v_mov_b32_e32 v9, v3
	v_lshl_add_u64 v[122:123], v[62:63], 0, v[8:9]
	v_add_co_u32_e32 v66, vcc, s28, v122
	s_lshr_b32 s0, s92, 5
	s_nop 0
	v_addc_co_u32_e32 v67, vcc, 0, v123, vcc
	global_load_dwordx4 v[62:65], v[122:123], off nt
	s_nop 0
	global_load_dwordx4 v[66:69], v[66:67], off nt
	v_add_co_u32_e32 v70, vcc, s29, v122
	s_bfe_u32 s11, s11, 0x30008
	s_nop 0
	v_addc_co_u32_e32 v71, vcc, 0, v123, vcc
	v_add_co_u32_e32 v74, vcc, s30, v122
	s_bfe_u32 s0, s0, 0xa0001
	s_nop 0
	v_addc_co_u32_e32 v75, vcc, 0, v123, vcc
	global_load_dwordx4 v[70:73], v[70:71], off nt
	s_nop 0
	global_load_dwordx4 v[74:77], v[74:75], off nt
	v_add_co_u32_e32 v78, vcc, s31, v122
	v_and_or_b32 v2, s60, 64, v13
	s_nop 0
	v_addc_co_u32_e32 v79, vcc, 0, v123, vcc
	v_add_co_u32_e32 v82, vcc, s40, v122
	s_nop 1
	v_addc_co_u32_e32 v83, vcc, 0, v123, vcc
	global_load_dwordx4 v[78:81], v[78:79], off nt
	s_nop 0
	global_load_dwordx4 v[82:85], v[82:83], off nt
	v_add_co_u32_e32 v86, vcc, s41, v122
	s_nop 1
	v_addc_co_u32_e32 v87, vcc, 0, v123, vcc
	v_add_co_u32_e32 v90, vcc, s42, v122
	s_nop 1
	v_addc_co_u32_e32 v91, vcc, 0, v123, vcc
	global_load_dwordx4 v[86:89], v[86:87], off nt
	s_nop 0
	global_load_dwordx4 v[90:93], v[90:91], off nt
	v_add_co_u32_e32 v94, vcc, s43, v122
	s_nop 1
	v_addc_co_u32_e32 v95, vcc, 0, v123, vcc
	v_add_co_u32_e32 v98, vcc, s44, v122
	s_nop 1
	v_addc_co_u32_e32 v99, vcc, 0, v123, vcc
	global_load_dwordx4 v[94:97], v[94:95], off nt
	s_nop 0
	global_load_dwordx4 v[98:101], v[98:99], off nt
	v_add_co_u32_e32 v102, vcc, s45, v122
	s_nop 1
	v_addc_co_u32_e32 v103, vcc, 0, v123, vcc
	v_add_co_u32_e32 v106, vcc, s46, v122
	s_nop 1
	v_addc_co_u32_e32 v107, vcc, 0, v123, vcc
	global_load_dwordx4 v[102:105], v[102:103], off nt
	s_nop 0
	global_load_dwordx4 v[106:109], v[106:107], off nt
	v_add_co_u32_e32 v110, vcc, s47, v122
	s_nop 1
	v_addc_co_u32_e32 v111, vcc, 0, v123, vcc
	global_load_dwordx4 v[110:113], v[110:111], off nt
	v_add_co_u32_e32 v114, vcc, s48, v122
	s_nop 1
	v_addc_co_u32_e32 v115, vcc, 0, v123, vcc
	global_load_dwordx4 v[114:117], v[114:115], off nt
	v_add_co_u32_e32 v118, vcc, s49, v122
	s_nop 1
	v_addc_co_u32_e32 v119, vcc, 0, v123, vcc
	global_load_dwordx4 v[118:121], v[118:119], off nt
	v_add_co_u32_e32 v122, vcc, s50, v122
	s_nop 1
	v_addc_co_u32_e32 v123, vcc, 0, v123, vcc
	global_load_dwordx4 v[122:125], v[122:123], off nt
	s_waitcnt vmcnt(15)
	v_pk_mul_f32 v[62:63], v[62:63], s[8:9] op_sel_hi:[1,0]
	ds_write2_b32 v11, v62, v63 offset1:1
	v_pk_mul_f32 v[62:63], v[64:65], s[8:9] op_sel_hi:[1,0]
	ds_write2_b32 v11, v62, v63 offset0:2 offset1:3
	s_waitcnt vmcnt(14)
	v_pk_mul_f32 v[62:63], v[66:67], s[8:9] op_sel_hi:[1,0]
	ds_write2_b32 v27, v62, v63 offset1:1
	v_pk_mul_f32 v[62:63], v[68:69], s[8:9] op_sel_hi:[1,0]
	ds_write2_b32 v28, v62, v63 offset1:1
	s_waitcnt vmcnt(13)
	v_pk_mul_f32 v[62:63], v[70:71], s[8:9] op_sel_hi:[1,0]
	ds_write2_b32 v29, v62, v63 offset1:1
	v_pk_mul_f32 v[62:63], v[72:73], s[8:9] op_sel_hi:[1,0]
	ds_write2_b32 v30, v62, v63 offset1:1
	s_waitcnt vmcnt(12)
	v_pk_mul_f32 v[62:63], v[74:75], s[8:9] op_sel_hi:[1,0]
	ds_write2_b32 v31, v62, v63 offset1:1
	v_pk_mul_f32 v[62:63], v[76:77], s[8:9] op_sel_hi:[1,0]
	ds_write2_b32 v32, v62, v63 offset1:1
	s_waitcnt vmcnt(0) lgkmcnt(0)
	v_pk_mul_f32 v[62:63], v[78:79], s[8:9] op_sel_hi:[1,0]
	ds_write2_b32 v33, v62, v63 offset1:1
	v_pk_mul_f32 v[62:63], v[80:81], s[8:9] op_sel_hi:[1,0]
	ds_write2_b32 v34, v62, v63 offset1:1
	v_pk_mul_f32 v[62:63], v[82:83], s[8:9] op_sel_hi:[1,0]
	ds_write2_b32 v35, v62, v63 offset1:1
	v_pk_mul_f32 v[62:63], v[84:85], s[8:9] op_sel_hi:[1,0]
	ds_write2_b32 v36, v62, v63 offset1:1
	v_pk_mul_f32 v[62:63], v[86:87], s[8:9] op_sel_hi:[1,0]
	ds_write2_b32 v37, v62, v63 offset1:1
	v_pk_mul_f32 v[62:63], v[88:89], s[8:9] op_sel_hi:[1,0]
	ds_write2_b32 v38, v62, v63 offset1:1
	v_pk_mul_f32 v[62:63], v[90:91], s[8:9] op_sel_hi:[1,0]
	ds_write2_b32 v39, v62, v63 offset1:1
	v_pk_mul_f32 v[62:63], v[92:93], s[8:9] op_sel_hi:[1,0]
	ds_write2_b32 v40, v62, v63 offset1:1
	v_pk_mul_f32 v[62:63], v[94:95], s[8:9] op_sel_hi:[1,0]
	ds_write2_b32 v41, v62, v63 offset1:1
	v_pk_mul_f32 v[62:63], v[96:97], s[8:9] op_sel_hi:[1,0]
	ds_write2_b32 v42, v62, v63 offset1:1
	v_pk_mul_f32 v[62:63], v[98:99], s[8:9] op_sel_hi:[1,0]
	ds_write2_b32 v43, v62, v63 offset1:1
	v_pk_mul_f32 v[62:63], v[100:101], s[8:9] op_sel_hi:[1,0]
	ds_write2_b32 v44, v62, v63 offset1:1
	v_pk_mul_f32 v[62:63], v[102:103], s[8:9] op_sel_hi:[1,0]
	ds_write2_b32 v45, v62, v63 offset1:1
	v_pk_mul_f32 v[62:63], v[104:105], s[8:9] op_sel_hi:[1,0]
	ds_write2_b32 v46, v62, v63 offset1:1
	v_pk_mul_f32 v[62:63], v[106:107], s[8:9] op_sel_hi:[1,0]
	ds_write2_b32 v47, v62, v63 offset1:1
	v_pk_mul_f32 v[62:63], v[108:109], s[8:9] op_sel_hi:[1,0]
	ds_write2_b32 v48, v62, v63 offset1:1
	v_pk_mul_f32 v[62:63], v[110:111], s[8:9] op_sel_hi:[1,0]
	ds_write2_b32 v49, v62, v63 offset1:1
	v_pk_mul_f32 v[62:63], v[112:113], s[8:9] op_sel_hi:[1,0]
	ds_write2_b32 v50, v62, v63 offset1:1
	v_pk_mul_f32 v[62:63], v[114:115], s[8:9] op_sel_hi:[1,0]
	ds_write2_b32 v51, v62, v63 offset1:1
	v_pk_mul_f32 v[62:63], v[116:117], s[8:9] op_sel_hi:[1,0]
	ds_write2_b32 v52, v62, v63 offset1:1
	v_pk_mul_f32 v[62:63], v[118:119], s[8:9] op_sel_hi:[1,0]
	ds_write2_b32 v53, v62, v63 offset1:1
	v_pk_mul_f32 v[62:63], v[120:121], s[8:9] op_sel_hi:[1,0]
	ds_write2_b32 v54, v62, v63 offset1:1
	v_pk_mul_f32 v[62:63], v[122:123], s[8:9] op_sel_hi:[1,0]
	ds_write2_b32 v55, v62, v63 offset1:1
	v_pk_mul_f32 v[62:63], v[124:125], s[8:9] op_sel_hi:[1,0]
	ds_write2_b32 v56, v62, v63 offset1:1
	s_waitcnt lgkmcnt(0)
; #define LAS __attribute__((address_space(3)))
; __device__ __forceinline__ unsigned pk4_fp8(float a, float b, float c, float d) { int w = 0; w = __builtin_amdgcn_cvt_pk_fp8_f32(clamp8(a), clamp8(b), w, false); w = __builtin_amdgcn_cvt_pk_fp8_f32(clamp8(c), clamp8(d), w, true); return (unsigned)w; }
; #define LDS_WAIT() asm volatile("s_waitcnt lgkmcnt(0)" ::: "memory")
; __host__ __device__ __forceinline__ size_t tiled_off(size_t r, int kb, int ktiles) { return (((r >> 8) * ktiles + (kb >> 7)) << 15) + ((r & 255) << 7) + (kb & 127); }
;     ...
;     for (int i = 0; i < 16; ++i) { LAS float* d = scr + (4 * i + kr) * 65 + nc; d[0] = v[i].x * W8_SCALE; d[1] = v[i].y * W8_SCALE; d[2] = v[i].z * W8_SCALE; d[3] = v[i].w * W8_SCALE; }
;     LDS_WAIT(); asm volatile("" ::: "memory");
;     const int c = lane & 3;
; #pragma unroll
;     for (int j = 0; j < 4; ++j) { const int n = (lane >> 2) + 16 * j; const LAS float* s = scr + (16 * c) * 65 + n;
;         u32x4 o; o.x = pk4_fp8(s[0 * 65], s[1 * 65], s[2 * 65], s[3 * 65]); o.y = pk4_fp8(s[4 * 65], s[5 * 65], s[6 * 65], s[7 * 65]);
;         o.z = pk4_fp8(s[8 * 65], s[9 * 65], s[10 * 65], s[11 * 65]); o.w = pk4_fp8(s[12 * 65], s[13 * 65], s[14 * 65], s[15 * 65]);
;         const int nn = n0 + n; const int row = MAP == 0 ? nn : ((nn >> 7) * 256 + (nn & 127) + (MAP == 2 ? 128 : 0));
;         __builtin_nontemporal_store(o, (u32x4*)(WT + (pitch < 0 ? tiled_off((size_t)row, k0 + 16 * c, pitch == -1 ? (K >> 7) : -pitch) : (size_t)row * (pitch ? pitch : K) + k0 + 16 * c))); }
;     LDS_WAIT(); asm volatile("" ::: "memory");
	ds_read_b32 v9, v14
	ds_read_b32 v62, v14 offset:260
	ds_read_b32 v63, v14 offset:520
	ds_read_b32 v64, v14 offset:780
	ds_read_b32 v65, v14 offset:1040
	ds_read_b32 v66, v14 offset:1300
	ds_read_b32 v67, v14 offset:1560
	ds_read_b32 v68, v14 offset:1820
	s_waitcnt lgkmcnt(7)
	v_med3_f32 v9, v9, s51, v57
	s_waitcnt lgkmcnt(6)
	v_med3_f32 v69, v62, s51, v57
	v_mov_b32_e32 v62, v3
	v_cvt_pk_fp8_f32 v62, v9, v69
	s_waitcnt lgkmcnt(5)
	v_med3_f32 v9, v63, s51, v57
	s_waitcnt lgkmcnt(3)
	v_med3_f32 v65, v65, s51, v57
	s_waitcnt lgkmcnt(2)
	v_med3_f32 v66, v66, s51, v57
	v_mov_b32_e32 v63, v3
	v_cvt_pk_fp8_f32 v63, v65, v66
	v_med3_f32 v64, v64, s51, v57
	v_cvt_pk_fp8_f32 v62, v9, v64 op_sel:[0,0,1]
	s_waitcnt lgkmcnt(1)
	v_med3_f32 v9, v67, s51, v57
	s_waitcnt lgkmcnt(0)
	v_med3_f32 v64, v68, s51, v57
	v_cvt_pk_fp8_f32 v63, v9, v64 op_sel:[0,0,1]
	ds_read_b32 v9, v14 offset:2080
	ds_read_b32 v64, v14 offset:2340
	ds_read_b32 v65, v14 offset:2600
	ds_read_b32 v66, v14 offset:2860
	ds_read_b32 v67, v14 offset:3120
	ds_read_b32 v68, v14 offset:3380
	ds_read_b32 v69, v14 offset:3640
	ds_read_b32 v70, v14 offset:3900
	s_waitcnt lgkmcnt(7)
	v_med3_f32 v9, v9, s51, v57
	s_waitcnt lgkmcnt(6)
	v_med3_f32 v71, v64, s51, v57
	v_mov_b32_e32 v64, v3
	v_cvt_pk_fp8_f32 v64, v9, v71
	s_waitcnt lgkmcnt(5)
	v_med3_f32 v9, v65, s51, v57
	s_waitcnt lgkmcnt(3)
	v_med3_f32 v67, v67, s51, v57
	s_waitcnt lgkmcnt(2)
	v_med3_f32 v68, v68, s51, v57
	v_mov_b32_e32 v65, v3
	v_cvt_pk_fp8_f32 v65, v67, v68
	v_med3_f32 v66, v66, s51, v57
	v_cvt_pk_fp8_f32 v64, v9, v66 op_sel:[0,0,1]
	s_waitcnt lgkmcnt(1)
	v_med3_f32 v9, v69, s51, v57
	s_waitcnt lgkmcnt(0)
	v_med3_f32 v66, v70, s51, v57
	v_cvt_pk_fp8_f32 v65, v9, v66 op_sel:[0,0,1]
	v_or_b32_e32 v9, s10, v12
	v_lshlrev_b32_e32 v9, 7, v9
	v_and_b32_e32 v66, 0x6780, v9
	v_mul_u32_u24_e64 v9, s11, 12
	v_add_u32_e32 v9, s0, v9
	v_lshlrev_b32_e32 v68, 15, v9
	v_mov_b32_e32 v69, v3
	v_mov_b32_e32 v67, v3
	v_lshl_add_u64 v[68:69], s[6:7], 0, v[68:69]
	v_lshl_add_u64 v[66:67], v[68:69], 0, v[66:67]
	v_lshl_add_u64 v[66:67], v[66:67], 0, v[2:3]
	global_store_dwordx4 v[66:67], v[62:65], off nt
	ds_read_b32 v9, v14 offset:64
	ds_read_b32 v62, v14 offset:324
	ds_read_b32 v63, v14 offset:584
	ds_read_b32 v64, v14 offset:844
	ds_read_b32 v65, v14 offset:1104
	ds_read_b32 v66, v14 offset:1364
	ds_read_b32 v67, v14 offset:1624
	ds_read_b32 v70, v14 offset:1884
	s_waitcnt lgkmcnt(0)
	v_med3_f32 v9, v9, s51, v57
	v_med3_f32 v71, v62, s51, v57
	v_mov_b32_e32 v62, v3
	v_cvt_pk_fp8_f32 v62, v9, v71
	v_med3_f32 v9, v63, s51, v57
	v_med3_f32 v65, v65, s51, v57
	v_med3_f32 v66, v66, s51, v57
	v_mov_b32_e32 v63, v3
	v_cvt_pk_fp8_f32 v63, v65, v66
	v_med3_f32 v64, v64, s51, v57
	v_cvt_pk_fp8_f32 v62, v9, v64 op_sel:[0,0,1]
	v_med3_f32 v9, v67, s51, v57
	v_med3_f32 v64, v70, s51, v57
	v_cvt_pk_fp8_f32 v63, v9, v64 op_sel:[0,0,1]
	ds_read_b32 v9, v14 offset:2144
	ds_read_b32 v64, v14 offset:2404
	ds_read_b32 v65, v14 offset:2664
	ds_read_b32 v66, v14 offset:2924
	ds_read_b32 v67, v14 offset:3184
	ds_read_b32 v70, v14 offset:3444
	ds_read_b32 v71, v14 offset:3704
	ds_read_b32 v72, v14 offset:3964
	s_waitcnt lgkmcnt(0)
	v_med3_f32 v9, v9, s51, v57
	v_med3_f32 v73, v64, s51, v57
	v_mov_b32_e32 v64, v3
	v_cvt_pk_fp8_f32 v64, v9, v73
	v_med3_f32 v9, v65, s51, v57
	v_med3_f32 v67, v67, s51, v57
	v_med3_f32 v70, v70, s51, v57
	v_mov_b32_e32 v65, v3
	v_cvt_pk_fp8_f32 v65, v67, v70
	v_med3_f32 v66, v66, s51, v57
	v_cvt_pk_fp8_f32 v64, v9, v66 op_sel:[0,0,1]
	v_med3_f32 v9, v71, s51, v57
	v_med3_f32 v66, v72, s51, v57
	v_cvt_pk_fp8_f32 v65, v9, v66 op_sel:[0,0,1]
	v_or_b32_e32 v9, s10, v15
	v_lshlrev_b32_e32 v9, 7, v9
	v_and_b32_e32 v66, 0x6f80, v9
	v_mov_b32_e32 v67, v3
	v_lshl_add_u64 v[66:67], v[68:69], 0, v[66:67]
	v_lshl_add_u64 v[66:67], v[66:67], 0, v[2:3]
	global_store_dwordx4 v[66:67], v[62:65], off nt
	ds_read_b32 v9, v14 offset:128
	ds_read_b32 v62, v14 offset:388
	ds_read_b32 v63, v14 offset:648
	ds_read_b32 v64, v14 offset:908
	ds_read_b32 v65, v14 offset:1168
	ds_read_b32 v66, v14 offset:1428
	ds_read_b32 v67, v14 offset:1688
	ds_read_b32 v70, v14 offset:1948
	s_waitcnt lgkmcnt(0)
; #define LAS __attribute__((address_space(3)))
; __device__ __forceinline__ unsigned pk4_fp8(float a, float b, float c, float d) { int w = 0; w = __builtin_amdgcn_cvt_pk_fp8_f32(clamp8(a), clamp8(b), w, false); w = __builtin_amdgcn_cvt_pk_fp8_f32(clamp8(c), clamp8(d), w, true); return (unsigned)w; }
; #define LDS_WAIT() asm volatile("s_waitcnt lgkmcnt(0)" ::: "memory")
; __host__ __device__ __forceinline__ size_t tiled_off(size_t r, int kb, int ktiles) { return (((r >> 8) * ktiles + (kb >> 7)) << 15) + ((r & 255) << 7) + (kb & 127); }
;     ...
;     const int c = lane & 3;
; #pragma unroll
;     for (int j = 0; j < 4; ++j) { const int n = (lane >> 2) + 16 * j; const LAS float* s = scr + (16 * c) * 65 + n;
;         u32x4 o; o.x = pk4_fp8(s[0 * 65], s[1 * 65], s[2 * 65], s[3 * 65]); o.y = pk4_fp8(s[4 * 65], s[5 * 65], s[6 * 65], s[7 * 65]);
;         o.z = pk4_fp8(s[8 * 65], s[9 * 65], s[10 * 65], s[11 * 65]); o.w = pk4_fp8(s[12 * 65], s[13 * 65], s[14 * 65], s[15 * 65]);
;         const int nn = n0 + n; const int row = MAP == 0 ? nn : ((nn >> 7) * 256 + (nn & 127) + (MAP == 2 ? 128 : 0));
;         __builtin_nontemporal_store(o, (u32x4*)(WT + (pitch < 0 ? tiled_off((size_t)row, k0 + 16 * c, pitch == -1 ? (K >> 7) : -pitch) : (size_t)row * (pitch ? pitch : K) + k0 + 16 * c))); }
;     LDS_WAIT(); asm volatile("" ::: "memory");
	v_med3_f32 v9, v9, s51, v57
	v_med3_f32 v71, v62, s51, v57
	v_mov_b32_e32 v62, v3
	v_cvt_pk_fp8_f32 v62, v9, v71
	v_med3_f32 v9, v63, s51, v57
	v_med3_f32 v65, v65, s51, v57
	v_med3_f32 v66, v66, s51, v57
	v_mov_b32_e32 v63, v3
	v_cvt_pk_fp8_f32 v63, v65, v66
	v_med3_f32 v64, v64, s51, v57
	v_cvt_pk_fp8_f32 v62, v9, v64 op_sel:[0,0,1]
	v_med3_f32 v9, v67, s51, v57
	v_med3_f32 v64, v70, s51, v57
	v_cvt_pk_fp8_f32 v63, v9, v64 op_sel:[0,0,1]
	ds_read_b32 v9, v14 offset:2208
	ds_read_b32 v64, v14 offset:2468
	ds_read_b32 v65, v14 offset:2728
	ds_read_b32 v66, v14 offset:2988
	ds_read_b32 v67, v14 offset:3248
	ds_read_b32 v70, v14 offset:3508
	ds_read_b32 v71, v14 offset:3768
	ds_read_b32 v72, v14 offset:4028
	s_waitcnt lgkmcnt(0)
	v_med3_f32 v9, v9, s51, v57
	v_med3_f32 v73, v64, s51, v57
	v_mov_b32_e32 v64, v3
	v_cvt_pk_fp8_f32 v64, v9, v73
	v_med3_f32 v9, v65, s51, v57
	v_med3_f32 v67, v67, s51, v57
	v_med3_f32 v70, v70, s51, v57
	v_mov_b32_e32 v65, v3
	v_cvt_pk_fp8_f32 v65, v67, v70
	v_med3_f32 v66, v66, s51, v57
	v_cvt_pk_fp8_f32 v64, v9, v66 op_sel:[0,0,1]
	v_med3_f32 v9, v71, s51, v57
	v_med3_f32 v66, v72, s51, v57
	v_cvt_pk_fp8_f32 v65, v9, v66 op_sel:[0,0,1]
	v_or_b32_e32 v9, s10, v16
	v_lshlrev_b32_e32 v9, 7, v9
	v_and_b32_e32 v66, 0x7780, v9
	v_mov_b32_e32 v67, v3
	v_lshl_add_u64 v[66:67], v[68:69], 0, v[66:67]
	v_lshl_add_u64 v[66:67], v[66:67], 0, v[2:3]
	global_store_dwordx4 v[66:67], v[62:65], off nt
	ds_read_b32 v9, v14 offset:192
	ds_read_b32 v62, v14 offset:452
	ds_read_b32 v63, v14 offset:712
	ds_read_b32 v64, v14 offset:972
	ds_read_b32 v65, v14 offset:1232
	ds_read_b32 v66, v14 offset:1492
	ds_read_b32 v67, v14 offset:1752
	ds_read_b32 v70, v14 offset:2012
	s_waitcnt lgkmcnt(0)
	v_med3_f32 v9, v9, s51, v57
	v_med3_f32 v71, v62, s51, v57
	v_mov_b32_e32 v62, v3
	v_cvt_pk_fp8_f32 v62, v9, v71
	v_med3_f32 v9, v63, s51, v57
	v_med3_f32 v65, v65, s51, v57
	v_med3_f32 v66, v66, s51, v57
	v_mov_b32_e32 v63, v3
	v_cvt_pk_fp8_f32 v63, v65, v66
	v_med3_f32 v64, v64, s51, v57
	v_cvt_pk_fp8_f32 v62, v9, v64 op_sel:[0,0,1]
	v_med3_f32 v9, v67, s51, v57
	v_med3_f32 v64, v70, s51, v57
	v_cvt_pk_fp8_f32 v63, v9, v64 op_sel:[0,0,1]
	ds_read_b32 v9, v14 offset:2272
	ds_read_b32 v64, v14 offset:2532
	ds_read_b32 v65, v14 offset:2792
	ds_read_b32 v66, v14 offset:3052
	ds_read_b32 v67, v14 offset:3312
	ds_read_b32 v70, v14 offset:3572
	ds_read_b32 v71, v14 offset:3832
	ds_read_b32 v72, v14 offset:4092
	s_waitcnt lgkmcnt(0)
	v_med3_f32 v9, v9, s51, v57
	v_med3_f32 v73, v64, s51, v57
	v_mov_b32_e32 v64, v3
	v_cvt_pk_fp8_f32 v64, v9, v73
	v_med3_f32 v9, v65, s51, v57
	v_med3_f32 v67, v67, s51, v57
	v_med3_f32 v70, v70, s51, v57
	v_mov_b32_e32 v65, v3
	v_cvt_pk_fp8_f32 v65, v67, v70
	v_med3_f32 v66, v66, s51, v57
	v_cvt_pk_fp8_f32 v64, v9, v66 op_sel:[0,0,1]
	v_med3_f32 v9, v71, s51, v57
	v_med3_f32 v66, v72, s51, v57
	v_cvt_pk_fp8_f32 v65, v9, v66 op_sel:[0,0,1]
	v_or_b32_e32 v9, s10, v17
	v_lshlrev_b32_e32 v9, 7, v9
	v_and_b32_e32 v66, 0x7f80, v9
	v_mov_b32_e32 v67, v3
	v_lshl_add_u64 v[66:67], v[68:69], 0, v[66:67]
	v_lshl_add_u64 v[66:67], v[66:67], 0, v[2:3]
	global_store_dwordx4 v[66:67], v[62:65], off nt
	s_waitcnt lgkmcnt(0)

; #define LAS __attribute__((address_space(3)))
; #define LDS_WAIT() asm volatile("s_waitcnt lgkmcnt(0)" ::: "memory")
; #define AIN(i) ((const float*)ldp(lds, (i)))
; template <int MAP>
; __device__ __forceinline__ void transpose_item(const float* W, int K, int N, bf16* WT, LAS float* scr, int item, int lane) {
;     const int nblk = N / 64, kb = item / nblk, nb = item % nblk, k0 = 64 * kb, n0 = 64 * nb;
;     const int kr = lane >> 4, nc = (lane & 15) * 4;
;     const float* src = W + (size_t)(k0 + kr) * N + n0 + nc;
;     f32x4 v[16];
; #pragma unroll
;     for (int i = 0; i < 16; ++i) v[i] = __builtin_nontemporal_load((const f32x4*)(src + (size_t)(4 * i) * N));
; #pragma unroll
;     for (int i = 0; i < 16; ++i) { LAS float* d = scr + (4 * i + kr) * 65 + nc; d[0] = v[i].x; d[1] = v[i].y; d[2] = v[i].z; d[3] = v[i].w; }
;     LDS_WAIT(); asm volatile("" ::: "memory");
; __device__ __forceinline__ void ph0(LAS unsigned char* lds, int tid, int lane, int wave, int G, int bid) {
;     ...
;             if (r < I_IN2) { transpose_item<0>(AIN(IWIN), D, INW, (bf16*)(ws + WS_WINT), scr, (r >> 3) * 88 + 16 + (r & 7), lane); continue; } r -= I_IN2;
.LBB0_141:
	s_andn2_b64 vcc, exec, s[10:11]
	s_cbranch_vccnz .LBB0_143
	s_lshr_b32 s0, s23, 3
	s_mulk_i32 s0, 0x58
	s_and_b32 s60, s23, 7
	s_or_b32 s0, s0, s60
	v_mov_b32_e32 v2, s78
	s_add_i32 s0, s0, 16
	ds_read_b32 v2, v2
	s_and_b32 s60, s0, 0xffff
	v_mov_b32_e32 v9, s79
	s_mul_i32 s60, s60, 0xba2f
	ds_read_b32 v9, v9
	s_lshr_b32 s61, s60, 16
	s_lshr_b32 s60, s60, 22
	s_mulk_i32 s60, 0x58
	s_sub_i32 s0, s0, s60
	s_and_b32 s60, s61, 0xffc0
	s_waitcnt lgkmcnt(0)
	v_readfirstlane_b32 s10, v2
	v_or_b32_e32 v2, s60, v10
	v_mul_u32_u24_e32 v2, 0x1600, v2
	v_readfirstlane_b32 s11, v9
	s_lshl_b32 s0, s0, 6
	v_lshlrev_b32_e32 v2, 2, v2
	v_lshl_add_u64 v[62:63], s[10:11], 0, v[2:3]
	s_and_b32 s10, s0, 0xffc0
	s_lshl_b32 s0, s10, 2
	v_lshl_add_u64 v[62:63], v[62:63], 0, s[0:1]
	v_mov_b32_e32 v9, v3
	v_lshl_add_u64 v[122:123], v[62:63], 0, v[8:9]
	v_add_co_u32_e32 v66, vcc, s71, v122
	s_lshl_b32 s0, s60, 1
	s_nop 0
	v_addc_co_u32_e32 v67, vcc, 0, v123, vcc
	v_add_co_u32_e32 v70, vcc, s64, v122
	global_load_dwordx4 v[62:65], v[122:123], off nt
	s_nop 0
	global_load_dwordx4 v[66:69], v[66:67], off nt
	v_addc_co_u32_e32 v71, vcc, 0, v123, vcc
	v_add_co_u32_e32 v74, vcc, s80, v122
	s_nop 1
	v_addc_co_u32_e32 v75, vcc, 0, v123, vcc
	v_add_co_u32_e32 v78, vcc, s46, v122
	global_load_dwordx4 v[70:73], v[70:71], off nt
	s_nop 0
	global_load_dwordx4 v[74:77], v[74:75], off nt
	v_addc_co_u32_e32 v79, vcc, 0, v123, vcc
	v_add_co_u32_e32 v82, vcc, s81, v122
	s_nop 1
	v_addc_co_u32_e32 v83, vcc, 0, v123, vcc
	v_add_co_u32_e32 v86, vcc, s82, v122
	global_load_dwordx4 v[78:81], v[78:79], off nt
	s_nop 0
	global_load_dwordx4 v[82:85], v[82:83], off nt
	v_addc_co_u32_e32 v87, vcc, 0, v123, vcc
	v_add_co_u32_e32 v90, vcc, s83, v122
	s_nop 1
	v_addc_co_u32_e32 v91, vcc, 0, v123, vcc
	v_add_co_u32_e32 v94, vcc, s84, v122
	global_load_dwordx4 v[86:89], v[86:87], off nt
	s_nop 0
	global_load_dwordx4 v[90:93], v[90:91], off nt
	v_addc_co_u32_e32 v95, vcc, 0, v123, vcc
	v_add_co_u32_e32 v98, vcc, s85, v122
	s_nop 1
	v_addc_co_u32_e32 v99, vcc, 0, v123, vcc
	v_add_co_u32_e32 v102, vcc, s86, v122
	global_load_dwordx4 v[94:97], v[94:95], off nt
	s_nop 0
	global_load_dwordx4 v[98:101], v[98:99], off nt
	v_addc_co_u32_e32 v103, vcc, 0, v123, vcc
	v_add_co_u32_e32 v106, vcc, s87, v122
	s_nop 1
	v_addc_co_u32_e32 v107, vcc, 0, v123, vcc
	v_add_co_u32_e32 v110, vcc, s88, v122
	global_load_dwordx4 v[102:105], v[102:103], off nt
	s_nop 0
	global_load_dwordx4 v[106:109], v[106:107], off nt
	v_addc_co_u32_e32 v111, vcc, 0, v123, vcc
	v_add_co_u32_e32 v114, vcc, s89, v122
	s_nop 1
	v_addc_co_u32_e32 v115, vcc, 0, v123, vcc
	global_load_dwordx4 v[110:113], v[110:111], off nt
	s_nop 0
	global_load_dwordx4 v[114:117], v[114:115], off nt
	v_add_co_u32_e32 v118, vcc, s90, v122
	s_nop 1
	v_addc_co_u32_e32 v119, vcc, 0, v123, vcc
	global_load_dwordx4 v[118:121], v[118:119], off nt
	v_add_co_u32_e32 v122, vcc, s91, v122
	s_nop 1
	v_addc_co_u32_e32 v123, vcc, 0, v123, vcc
	global_load_dwordx4 v[122:125], v[122:123], off nt
	s_waitcnt vmcnt(0) lgkmcnt(0)
	ds_write2_b32 v11, v62, v63 offset1:1
	ds_write2_b32 v11, v64, v65 offset0:2 offset1:3
	ds_write2_b32 v27, v66, v67 offset1:1
	ds_write2_b32 v28, v68, v69 offset1:1
	ds_write2_b32 v29, v70, v71 offset1:1
	ds_write2_b32 v30, v72, v73 offset1:1
	ds_write2_b32 v31, v74, v75 offset1:1
	ds_write2_b32 v32, v76, v77 offset1:1
	ds_write2_b32 v33, v78, v79 offset1:1
	ds_write2_b32 v34, v80, v81 offset1:1
	ds_write2_b32 v35, v82, v83 offset1:1
	ds_write2_b32 v36, v84, v85 offset1:1
	ds_write2_b32 v37, v86, v87 offset1:1
	ds_write2_b32 v38, v88, v89 offset1:1
	ds_write2_b32 v39, v90, v91 offset1:1
	ds_write2_b32 v40, v92, v93 offset1:1
	ds_write2_b32 v41, v94, v95 offset1:1
	ds_write2_b32 v42, v96, v97 offset1:1
	ds_write2_b32 v43, v98, v99 offset1:1
	ds_write2_b32 v44, v100, v101 offset1:1
	ds_write2_b32 v45, v102, v103 offset1:1
	ds_write2_b32 v46, v104, v105 offset1:1
	ds_write2_b32 v47, v106, v107 offset1:1
	ds_write2_b32 v48, v108, v109 offset1:1
	ds_write2_b32 v49, v110, v111 offset1:1
	ds_write2_b32 v50, v112, v113 offset1:1
	ds_write2_b32 v51, v114, v115 offset1:1
	ds_write2_b32 v52, v116, v117 offset1:1
	ds_write2_b32 v53, v118, v119 offset1:1
	ds_write2_b32 v54, v120, v121 offset1:1
	ds_write2_b32 v55, v122, v123 offset1:1
	ds_write2_b32 v56, v124, v125 offset1:1
	s_waitcnt lgkmcnt(0)
	ds_read_b32 v2, v19
	ds_read_b32 v9, v19 offset:260
	ds_read_b32 v63, v19 offset:520
	ds_read_b32 v64, v19 offset:780
	ds_read_b32 v65, v19 offset:1040
	ds_read_b32 v68, v19 offset:1300
	ds_read_b32 v69, v19 offset:1560
	ds_read_b32 v70, v19 offset:1820
	s_waitcnt lgkmcnt(6)
; #define LAS __attribute__((address_space(3)))
; __device__ __forceinline__ unsigned pk_bf16(float lo, float hi) { const bf16x2_t r = __builtin_convertvector((f32x2){lo, hi}, bf16x2_t); return __builtin_bit_cast(unsigned, r); }
; #define LDS_WAIT() asm volatile("s_waitcnt lgkmcnt(0)" ::: "memory")
; template <int MAP>
; __device__ __forceinline__ void transpose_item(const float* W, int K, int N, bf16* WT, LAS float* scr, int item, int lane) {
;     ...
;     const int c = lane & 7;
; #pragma unroll
;     for (int j = 0; j < 8; ++j) { const int n = (lane >> 3) + 8 * j; const LAS float* s = scr + (8 * c) * 65 + n;
;         u32x4 o; o.x = pk_bf16(s[0 * 65], s[1 * 65]); o.y = pk_bf16(s[2 * 65], s[3 * 65]); o.z = pk_bf16(s[4 * 65], s[5 * 65]); o.w = pk_bf16(s[6 * 65], s[7 * 65]);
;         const int nn = n0 + n; const int row = MAP == 0 ? nn : ((nn >> 7) * 256 + (nn & 127) + (MAP == 2 ? 128 : 0));
;         __builtin_nontemporal_store(o, (u32x4*)(WT + (size_t)row * K + k0 + 8 * c)); }
;     LDS_WAIT(); asm volatile("" ::: "memory");
	v_cvt_pk_bf16_f32 v62, v2, v9
	v_or_b32_e32 v2, s10, v18
	v_lshl_add_u64 v[66:67], v[6:7], 0, s[0:1]
	v_lshlrev_b32_e32 v2, 12, v2
	s_waitcnt lgkmcnt(4)
	v_cvt_pk_bf16_f32 v63, v63, v64
	s_waitcnt lgkmcnt(2)
	v_cvt_pk_bf16_f32 v64, v65, v68
	s_waitcnt lgkmcnt(0)
	v_cvt_pk_bf16_f32 v65, v69, v70
	v_lshl_add_u64 v[68:69], v[66:67], 0, v[2:3]
	global_store_dwordx4 v[68:69], v[62:65], off nt
	ds_read_b32 v2, v19 offset:32
	ds_read_b32 v9, v19 offset:292
	ds_read_b32 v63, v19 offset:552
	ds_read_b32 v64, v19 offset:812
	ds_read_b32 v65, v19 offset:1072
	ds_read_b32 v68, v19 offset:1332
	ds_read_b32 v69, v19 offset:1592
	ds_read_b32 v70, v19 offset:1852
	s_waitcnt lgkmcnt(0)
	v_cvt_pk_bf16_f32 v62, v2, v9
	v_or_b32_e32 v2, s10, v20
	v_lshlrev_b32_e32 v2, 12, v2
	v_cvt_pk_bf16_f32 v63, v63, v64
	v_cvt_pk_bf16_f32 v64, v65, v68
	v_cvt_pk_bf16_f32 v65, v69, v70
	v_lshl_add_u64 v[68:69], v[66:67], 0, v[2:3]
	global_store_dwordx4 v[68:69], v[62:65], off nt
	ds_read_b32 v2, v19 offset:64
	ds_read_b32 v9, v19 offset:324
	ds_read_b32 v63, v19 offset:584
	ds_read_b32 v64, v19 offset:844
	ds_read_b32 v65, v19 offset:1104
	ds_read_b32 v68, v19 offset:1364
	ds_read_b32 v69, v19 offset:1624
	ds_read_b32 v70, v19 offset:1884
	s_waitcnt lgkmcnt(0)
	v_cvt_pk_bf16_f32 v62, v2, v9
	v_or_b32_e32 v2, s10, v21
	v_lshlrev_b32_e32 v2, 12, v2
	v_cvt_pk_bf16_f32 v63, v63, v64
	v_cvt_pk_bf16_f32 v64, v65, v68
	v_cvt_pk_bf16_f32 v65, v69, v70
	v_lshl_add_u64 v[68:69], v[66:67], 0, v[2:3]
	global_store_dwordx4 v[68:69], v[62:65], off nt
	ds_read_b32 v2, v19 offset:96
	ds_read_b32 v9, v19 offset:356
	ds_read_b32 v63, v19 offset:616
	ds_read_b32 v64, v19 offset:876
	ds_read_b32 v65, v19 offset:1136
	ds_read_b32 v68, v19 offset:1396
	ds_read_b32 v69, v19 offset:1656
	ds_read_b32 v70, v19 offset:1916
	s_waitcnt lgkmcnt(0)
	v_cvt_pk_bf16_f32 v62, v2, v9
	v_or_b32_e32 v2, s10, v22
	v_lshlrev_b32_e32 v2, 12, v2
	v_cvt_pk_bf16_f32 v63, v63, v64
	v_cvt_pk_bf16_f32 v64, v65, v68
	v_cvt_pk_bf16_f32 v65, v69, v70
	v_lshl_add_u64 v[68:69], v[66:67], 0, v[2:3]
	global_store_dwordx4 v[68:69], v[62:65], off nt
	ds_read_b32 v2, v19 offset:128
	ds_read_b32 v9, v19 offset:388
	ds_read_b32 v63, v19 offset:648
	ds_read_b32 v64, v19 offset:908
	ds_read_b32 v65, v19 offset:1168
	ds_read_b32 v68, v19 offset:1428
	ds_read_b32 v69, v19 offset:1688
	ds_read_b32 v70, v19 offset:1948
	s_waitcnt lgkmcnt(0)
	v_cvt_pk_bf16_f32 v62, v2, v9
	v_or_b32_e32 v2, s10, v23
	v_lshlrev_b32_e32 v2, 12, v2
	v_cvt_pk_bf16_f32 v63, v63, v64
	v_cvt_pk_bf16_f32 v64, v65, v68
	v_cvt_pk_bf16_f32 v65, v69, v70
	v_lshl_add_u64 v[68:69], v[66:67], 0, v[2:3]
	global_store_dwordx4 v[68:69], v[62:65], off nt
	ds_read_b32 v2, v19 offset:160
	ds_read_b32 v9, v19 offset:420
	ds_read_b32 v63, v19 offset:680
	ds_read_b32 v64, v19 offset:940
	ds_read_b32 v65, v19 offset:1200
	ds_read_b32 v68, v19 offset:1460
	ds_read_b32 v69, v19 offset:1720
	ds_read_b32 v70, v19 offset:1980
	s_waitcnt lgkmcnt(0)
	v_cvt_pk_bf16_f32 v62, v2, v9
	v_or_b32_e32 v2, s10, v24
	v_lshlrev_b32_e32 v2, 12, v2
	v_cvt_pk_bf16_f32 v63, v63, v64
	v_cvt_pk_bf16_f32 v64, v65, v68
	v_cvt_pk_bf16_f32 v65, v69, v70
	v_lshl_add_u64 v[68:69], v[66:67], 0, v[2:3]
	global_store_dwordx4 v[68:69], v[62:65], off nt
	ds_read_b32 v2, v19 offset:192
	ds_read_b32 v9, v19 offset:452
	ds_read_b32 v63, v19 offset:712
	ds_read_b32 v64, v19 offset:972
	ds_read_b32 v65, v19 offset:1232
	ds_read_b32 v68, v19 offset:1492
	ds_read_b32 v69, v19 offset:1752
	ds_read_b32 v70, v19 offset:2012
	s_waitcnt lgkmcnt(0)
	v_cvt_pk_bf16_f32 v62, v2, v9
	v_or_b32_e32 v2, s10, v25
	v_lshlrev_b32_e32 v2, 12, v2
	v_cvt_pk_bf16_f32 v63, v63, v64
	v_cvt_pk_bf16_f32 v64, v65, v68
	v_cvt_pk_bf16_f32 v65, v69, v70
	v_lshl_add_u64 v[68:69], v[66:67], 0, v[2:3]
	global_store_dwordx4 v[68:69], v[62:65], off nt
	ds_read_b32 v2, v19 offset:224
	ds_read_b32 v9, v19 offset:484
	ds_read_b32 v63, v19 offset:744
	ds_read_b32 v64, v19 offset:1004
	ds_read_b32 v65, v19 offset:1264
	ds_read_b32 v68, v19 offset:1524
	ds_read_b32 v69, v19 offset:1784
	ds_read_b32 v70, v19 offset:2044
	s_waitcnt lgkmcnt(0)
	v_cvt_pk_bf16_f32 v62, v2, v9
	v_or_b32_e32 v2, s10, v26
	v_lshlrev_b32_e32 v2, 12, v2
	v_cvt_pk_bf16_f32 v63, v63, v64
	v_cvt_pk_bf16_f32 v64, v65, v68
	v_cvt_pk_bf16_f32 v65, v69, v70
	v_lshl_add_u64 v[66:67], v[66:67], 0, v[2:3]
	global_store_dwordx4 v[66:67], v[62:65], off nt
	s_waitcnt lgkmcnt(0)

; #define LAS __attribute__((address_space(3)))
; #define LDS_WAIT() asm volatile("s_waitcnt lgkmcnt(0)" ::: "memory")
; #define AIN(i) ((const float*)ldp(lds, (i)))
;     const int nblk = N / 64, kb = item / nblk, nb = item % nblk, k0 = 64 * kb, n0 = 64 * nb;
;     const int kr = lane >> 4, nc = (lane & 15) * 4;
;     const float* src = W + (size_t)(k0 + kr) * N + n0 + nc;
;     f32x4 v[16];
; #pragma unroll
;     for (int i = 0; i < 16; ++i) v[i] = __builtin_nontemporal_load((const f32x4*)(src + (size_t)(4 * i) * N));
; #pragma unroll
;     for (int i = 0; i < 16; ++i) { LAS float* d = scr + (4 * i + kr) * 65 + nc; d[0] = v[i].x * W8_SCALE; d[1] = v[i].y * W8_SCALE; d[2] = v[i].z * W8_SCALE; d[3] = v[i].w * W8_SCALE; }
;     LDS_WAIT(); asm volatile("" ::: "memory");
; __device__ __forceinline__ void ph0(LAS unsigned char* lds, int tid, int lane, int wave, int G, int bid) {
;     ...
;             if (r < I_IN) { transpose_item_f8<0>(AIN(IWIN), D, INW, (unsigned char*)(ws + WS_WG8), scr, r, lane, -1); continue; } r -= I_IN;
.LBB0_144:
	s_andn2_b64 vcc, exec, s[10:11]
	s_cbranch_vccnz .LBB0_113
	v_mov_b32_e32 v2, s78
	ds_read_b32 v2, v2
	s_sub_i32 s0, 0xd33f, s9
	v_mov_b32_e32 v9, s79
	s_and_b32 s11, s0, 0xffff
	ds_read_b32 v9, v9
	s_mul_i32 s11, s11, 0xba2f
	s_lshr_b32 s60, s11, 22
	s_lshl_b32 s63, s60, 6
	s_waitcnt lgkmcnt(0)
	v_readfirstlane_b32 s92, v2
	s_mul_i32 s10, s60, 0x58
	v_or_b32_e32 v2, s63, v10
	s_sub_i32 s10, s0, s10
	v_mul_u32_u24_e32 v2, 0x1600, v2
	v_readfirstlane_b32 s93, v9
	s_lshl_b32 s0, s10, 6
	v_lshlrev_b32_e32 v2, 2, v2
	v_lshl_add_u64 v[62:63], s[92:93], 0, v[2:3]
	s_and_b32 s92, s0, 0xffc0
	s_lshl_b32 s0, s92, 2
	v_lshl_add_u64 v[62:63], v[62:63], 0, s[0:1]
	v_mov_b32_e32 v9, v3
	v_lshl_add_u64 v[122:123], v[62:63], 0, v[8:9]
	v_add_co_u32_e32 v66, vcc, s71, v122
	global_load_dwordx4 v[62:65], v[122:123], off nt
	s_nop 0
	v_addc_co_u32_e32 v67, vcc, 0, v123, vcc
	v_add_co_u32_e32 v70, vcc, s64, v122
	global_load_dwordx4 v[66:69], v[66:67], off nt
	s_nop 0
	v_addc_co_u32_e32 v71, vcc, 0, v123, vcc
	v_add_co_u32_e32 v74, vcc, s80, v122
	global_load_dwordx4 v[70:73], v[70:71], off nt
	s_nop 0
	v_addc_co_u32_e32 v75, vcc, 0, v123, vcc
	v_add_co_u32_e32 v78, vcc, s46, v122
	s_lshl_b32 s10, s10, 2
	s_nop 0
	v_addc_co_u32_e32 v79, vcc, 0, v123, vcc
	v_add_co_u32_e32 v82, vcc, s81, v122
	global_load_dwordx4 v[74:77], v[74:75], off nt
	s_nop 0
	global_load_dwordx4 v[78:81], v[78:79], off nt
	v_addc_co_u32_e32 v83, vcc, 0, v123, vcc
	v_add_co_u32_e32 v86, vcc, s82, v122
	global_load_dwordx4 v[82:85], v[82:83], off nt
	s_nop 0
	v_addc_co_u32_e32 v87, vcc, 0, v123, vcc
	v_add_co_u32_e32 v90, vcc, s83, v122
	global_load_dwordx4 v[86:89], v[86:87], off nt
	s_nop 0
	v_addc_co_u32_e32 v91, vcc, 0, v123, vcc
	v_add_co_u32_e32 v94, vcc, s84, v122
	s_lshr_b32 s0, s11, 23
	s_nop 0
	v_addc_co_u32_e32 v95, vcc, 0, v123, vcc
	v_add_co_u32_e32 v98, vcc, s85, v122
	global_load_dwordx4 v[90:93], v[90:91], off nt
	s_nop 0
	global_load_dwordx4 v[94:97], v[94:95], off nt
	v_addc_co_u32_e32 v99, vcc, 0, v123, vcc
	v_add_co_u32_e32 v102, vcc, s86, v122
	global_load_dwordx4 v[98:101], v[98:99], off nt
	s_nop 0
	v_addc_co_u32_e32 v103, vcc, 0, v123, vcc
	v_add_co_u32_e32 v106, vcc, s87, v122
	global_load_dwordx4 v[102:105], v[102:103], off nt
	s_nop 0
	v_addc_co_u32_e32 v107, vcc, 0, v123, vcc
	v_add_co_u32_e32 v110, vcc, s88, v122
	s_and_b32 s10, s10, 0x7f0
	s_nop 0
	v_addc_co_u32_e32 v111, vcc, 0, v123, vcc
	global_load_dwordx4 v[106:109], v[106:107], off nt
	s_nop 0
	global_load_dwordx4 v[110:113], v[110:111], off nt
	v_add_co_u32_e32 v114, vcc, s89, v122
	s_add_i32 s10, s10, s0
	s_nop 0
	v_addc_co_u32_e32 v115, vcc, 0, v123, vcc
	global_load_dwordx4 v[114:117], v[114:115], off nt
	v_add_co_u32_e32 v118, vcc, s90, v122
	s_lshl_b32 s0, s10, 15
	s_nop 0
	v_addc_co_u32_e32 v119, vcc, 0, v123, vcc
	global_load_dwordx4 v[118:121], v[118:119], off nt
	v_add_co_u32_e32 v122, vcc, s91, v122
	s_add_u32 s10, s14, s0
	s_nop 0
	v_addc_co_u32_e32 v123, vcc, 0, v123, vcc
	global_load_dwordx4 v[122:125], v[122:123], off nt
	s_addc_u32 s11, s15, 0
	v_and_or_b32 v2, s63, 64, v13
	s_waitcnt vmcnt(0) lgkmcnt(0)
	v_pk_mul_f32 v[62:63], v[62:63], s[8:9] op_sel_hi:[1,0]
	ds_write2_b32 v11, v62, v63 offset1:1
	v_pk_mul_f32 v[62:63], v[64:65], s[8:9] op_sel_hi:[1,0]
	ds_write2_b32 v11, v62, v63 offset0:2 offset1:3
	v_pk_mul_f32 v[62:63], v[66:67], s[8:9] op_sel_hi:[1,0]
	ds_write2_b32 v27, v62, v63 offset1:1
	v_pk_mul_f32 v[62:63], v[68:69], s[8:9] op_sel_hi:[1,0]
	ds_write2_b32 v28, v62, v63 offset1:1
	v_pk_mul_f32 v[62:63], v[70:71], s[8:9] op_sel_hi:[1,0]
	ds_write2_b32 v29, v62, v63 offset1:1
	v_pk_mul_f32 v[62:63], v[72:73], s[8:9] op_sel_hi:[1,0]
	ds_write2_b32 v30, v62, v63 offset1:1
	v_pk_mul_f32 v[62:63], v[74:75], s[8:9] op_sel_hi:[1,0]
	ds_write2_b32 v31, v62, v63 offset1:1
	v_pk_mul_f32 v[62:63], v[76:77], s[8:9] op_sel_hi:[1,0]
	ds_write2_b32 v32, v62, v63 offset1:1
	v_pk_mul_f32 v[62:63], v[78:79], s[8:9] op_sel_hi:[1,0]
	ds_write2_b32 v33, v62, v63 offset1:1
	v_pk_mul_f32 v[62:63], v[80:81], s[8:9] op_sel_hi:[1,0]
	ds_write2_b32 v34, v62, v63 offset1:1
	v_pk_mul_f32 v[62:63], v[82:83], s[8:9] op_sel_hi:[1,0]
	ds_write2_b32 v35, v62, v63 offset1:1
	v_pk_mul_f32 v[62:63], v[84:85], s[8:9] op_sel_hi:[1,0]
	ds_write2_b32 v36, v62, v63 offset1:1
	v_pk_mul_f32 v[62:63], v[86:87], s[8:9] op_sel_hi:[1,0]
	ds_write2_b32 v37, v62, v63 offset1:1
	v_pk_mul_f32 v[62:63], v[88:89], s[8:9] op_sel_hi:[1,0]
	ds_write2_b32 v38, v62, v63 offset1:1
	v_pk_mul_f32 v[62:63], v[90:91], s[8:9] op_sel_hi:[1,0]
	ds_write2_b32 v39, v62, v63 offset1:1
	v_pk_mul_f32 v[62:63], v[92:93], s[8:9] op_sel_hi:[1,0]
	ds_write2_b32 v40, v62, v63 offset1:1
	v_pk_mul_f32 v[62:63], v[94:95], s[8:9] op_sel_hi:[1,0]
	ds_write2_b32 v41, v62, v63 offset1:1
	v_pk_mul_f32 v[62:63], v[96:97], s[8:9] op_sel_hi:[1,0]
	ds_write2_b32 v42, v62, v63 offset1:1
	v_pk_mul_f32 v[62:63], v[98:99], s[8:9] op_sel_hi:[1,0]
	ds_write2_b32 v43, v62, v63 offset1:1
	v_pk_mul_f32 v[62:63], v[100:101], s[8:9] op_sel_hi:[1,0]
	ds_write2_b32 v44, v62, v63 offset1:1
	v_pk_mul_f32 v[62:63], v[102:103], s[8:9] op_sel_hi:[1,0]
	ds_write2_b32 v45, v62, v63 offset1:1
	v_pk_mul_f32 v[62:63], v[104:105], s[8:9] op_sel_hi:[1,0]
	ds_write2_b32 v46, v62, v63 offset1:1
	v_pk_mul_f32 v[62:63], v[106:107], s[8:9] op_sel_hi:[1,0]
	ds_write2_b32 v47, v62, v63 offset1:1
	v_pk_mul_f32 v[62:63], v[108:109], s[8:9] op_sel_hi:[1,0]
	ds_write2_b32 v48, v62, v63 offset1:1
	v_pk_mul_f32 v[62:63], v[110:111], s[8:9] op_sel_hi:[1,0]
	ds_write2_b32 v49, v62, v63 offset1:1
	v_pk_mul_f32 v[62:63], v[112:113], s[8:9] op_sel_hi:[1,0]
	ds_write2_b32 v50, v62, v63 offset1:1
	v_pk_mul_f32 v[62:63], v[114:115], s[8:9] op_sel_hi:[1,0]
	ds_write2_b32 v51, v62, v63 offset1:1
	v_pk_mul_f32 v[62:63], v[116:117], s[8:9] op_sel_hi:[1,0]
	ds_write2_b32 v52, v62, v63 offset1:1
	v_pk_mul_f32 v[62:63], v[118:119], s[8:9] op_sel_hi:[1,0]
	ds_write2_b32 v53, v62, v63 offset1:1
	v_pk_mul_f32 v[62:63], v[120:121], s[8:9] op_sel_hi:[1,0]
	ds_write2_b32 v54, v62, v63 offset1:1
	v_pk_mul_f32 v[62:63], v[122:123], s[8:9] op_sel_hi:[1,0]
	ds_write2_b32 v55, v62, v63 offset1:1
	v_pk_mul_f32 v[62:63], v[124:125], s[8:9] op_sel_hi:[1,0]
	ds_write2_b32 v56, v62, v63 offset1:1
	s_waitcnt lgkmcnt(0)
; #define LAS __attribute__((address_space(3)))
; __device__ __forceinline__ unsigned pk4_fp8(float a, float b, float c, float d) { int w = 0; w = __builtin_amdgcn_cvt_pk_fp8_f32(clamp8(a), clamp8(b), w, false); w = __builtin_amdgcn_cvt_pk_fp8_f32(clamp8(c), clamp8(d), w, true); return (unsigned)w; }
; #define LDS_WAIT() asm volatile("s_waitcnt lgkmcnt(0)" ::: "memory")
; __host__ __device__ __forceinline__ size_t tiled_off(size_t r, int kb, int ktiles) { return (((r >> 8) * ktiles + (kb >> 7)) << 15) + ((r & 255) << 7) + (kb & 127); }
;     ...
;     const int c = lane & 3;
; #pragma unroll
;     for (int j = 0; j < 4; ++j) { const int n = (lane >> 2) + 16 * j; const LAS float* s = scr + (16 * c) * 65 + n;
;         u32x4 o; o.x = pk4_fp8(s[0 * 65], s[1 * 65], s[2 * 65], s[3 * 65]); o.y = pk4_fp8(s[4 * 65], s[5 * 65], s[6 * 65], s[7 * 65]);
;         o.z = pk4_fp8(s[8 * 65], s[9 * 65], s[10 * 65], s[11 * 65]); o.w = pk4_fp8(s[12 * 65], s[13 * 65], s[14 * 65], s[15 * 65]);
;         const int nn = n0 + n; const int row = MAP == 0 ? nn : ((nn >> 7) * 256 + (nn & 127) + (MAP == 2 ? 128 : 0));
;         __builtin_nontemporal_store(o, (u32x4*)(WT + (pitch < 0 ? tiled_off((size_t)row, k0 + 16 * c, pitch == -1 ? (K >> 7) : -pitch) : (size_t)row * (pitch ? pitch : K) + k0 + 16 * c))); }
;     LDS_WAIT(); asm volatile("" ::: "memory");
	ds_read_b32 v9, v14
	ds_read_b32 v62, v14 offset:260
	ds_read_b32 v63, v14 offset:520
	ds_read_b32 v64, v14 offset:780
	ds_read_b32 v65, v14 offset:1040
	ds_read_b32 v66, v14 offset:1300
	ds_read_b32 v67, v14 offset:1560
	ds_read_b32 v68, v14 offset:1820
	s_waitcnt lgkmcnt(7)
	v_med3_f32 v9, v9, s51, v57
	s_waitcnt lgkmcnt(6)
	v_med3_f32 v69, v62, s51, v57
	v_mov_b32_e32 v62, v3
	v_cvt_pk_fp8_f32 v62, v9, v69
	s_waitcnt lgkmcnt(5)
	v_med3_f32 v9, v63, s51, v57
	s_waitcnt lgkmcnt(3)
	v_med3_f32 v65, v65, s51, v57
	s_waitcnt lgkmcnt(2)
	v_med3_f32 v66, v66, s51, v57
	v_mov_b32_e32 v63, v3
	v_cvt_pk_fp8_f32 v63, v65, v66
	v_med3_f32 v64, v64, s51, v57
	v_cvt_pk_fp8_f32 v62, v9, v64 op_sel:[0,0,1]
	s_waitcnt lgkmcnt(1)
	v_med3_f32 v9, v67, s51, v57
	s_waitcnt lgkmcnt(0)
	v_med3_f32 v64, v68, s51, v57
	v_cvt_pk_fp8_f32 v63, v9, v64 op_sel:[0,0,1]
	ds_read_b32 v9, v14 offset:2080
	ds_read_b32 v64, v14 offset:2340
	ds_read_b32 v65, v14 offset:2600
	ds_read_b32 v66, v14 offset:2860
	ds_read_b32 v67, v14 offset:3120
	ds_read_b32 v68, v14 offset:3380
	ds_read_b32 v69, v14 offset:3640
	ds_read_b32 v70, v14 offset:3900
	s_waitcnt lgkmcnt(7)
	v_med3_f32 v9, v9, s51, v57
	s_waitcnt lgkmcnt(6)
	v_med3_f32 v71, v64, s51, v57
	v_mov_b32_e32 v64, v3
	v_cvt_pk_fp8_f32 v64, v9, v71
	s_waitcnt lgkmcnt(5)
	v_med3_f32 v9, v65, s51, v57
	s_waitcnt lgkmcnt(3)
	v_med3_f32 v67, v67, s51, v57
	s_waitcnt lgkmcnt(2)
	v_med3_f32 v68, v68, s51, v57
	v_mov_b32_e32 v65, v3
	v_cvt_pk_fp8_f32 v65, v67, v68
	v_med3_f32 v66, v66, s51, v57
	v_cvt_pk_fp8_f32 v64, v9, v66 op_sel:[0,0,1]
	s_waitcnt lgkmcnt(1)
	v_med3_f32 v9, v69, s51, v57
	s_waitcnt lgkmcnt(0)
	v_med3_f32 v66, v70, s51, v57
	v_cvt_pk_fp8_f32 v65, v9, v66 op_sel:[0,0,1]
	v_or_b32_e32 v9, s92, v12
	v_lshlrev_b32_e32 v9, 7, v9
	v_and_b32_e32 v66, 0x6780, v9
	v_mov_b32_e32 v67, v3
	v_lshl_add_u64 v[66:67], s[10:11], 0, v[66:67]
	v_lshl_add_u64 v[66:67], v[66:67], 0, v[2:3]
	global_store_dwordx4 v[66:67], v[62:65], off nt
	ds_read_b32 v9, v14 offset:64
	ds_read_b32 v62, v14 offset:324
	ds_read_b32 v63, v14 offset:584
	ds_read_b32 v64, v14 offset:844
	ds_read_b32 v65, v14 offset:1104
	ds_read_b32 v66, v14 offset:1364
	ds_read_b32 v67, v14 offset:1624
	ds_read_b32 v68, v14 offset:1884
	s_waitcnt lgkmcnt(0)
	v_med3_f32 v9, v9, s51, v57
	v_med3_f32 v69, v62, s51, v57
	v_mov_b32_e32 v62, v3
	v_cvt_pk_fp8_f32 v62, v9, v69
	v_med3_f32 v9, v63, s51, v57
	v_med3_f32 v65, v65, s51, v57
	v_med3_f32 v66, v66, s51, v57
	v_mov_b32_e32 v63, v3
	v_cvt_pk_fp8_f32 v63, v65, v66
	v_med3_f32 v64, v64, s51, v57
	v_cvt_pk_fp8_f32 v62, v9, v64 op_sel:[0,0,1]
	v_med3_f32 v9, v67, s51, v57
	v_med3_f32 v64, v68, s51, v57
	v_cvt_pk_fp8_f32 v63, v9, v64 op_sel:[0,0,1]
	ds_read_b32 v9, v14 offset:2144
	ds_read_b32 v64, v14 offset:2404
	ds_read_b32 v65, v14 offset:2664
	ds_read_b32 v66, v14 offset:2924
	ds_read_b32 v67, v14 offset:3184
	ds_read_b32 v68, v14 offset:3444
	ds_read_b32 v69, v14 offset:3704
	ds_read_b32 v70, v14 offset:3964
	s_waitcnt lgkmcnt(0)
	v_med3_f32 v9, v9, s51, v57
	v_med3_f32 v71, v64, s51, v57
	v_mov_b32_e32 v64, v3
	v_cvt_pk_fp8_f32 v64, v9, v71
	v_med3_f32 v9, v65, s51, v57
	v_med3_f32 v67, v67, s51, v57
	v_med3_f32 v68, v68, s51, v57
	v_mov_b32_e32 v65, v3
	v_cvt_pk_fp8_f32 v65, v67, v68
	v_med3_f32 v66, v66, s51, v57
	v_cvt_pk_fp8_f32 v64, v9, v66 op_sel:[0,0,1]
	v_med3_f32 v9, v69, s51, v57
	v_med3_f32 v66, v70, s51, v57
	v_cvt_pk_fp8_f32 v65, v9, v66 op_sel:[0,0,1]
	v_or_b32_e32 v9, s92, v15
	v_lshlrev_b32_e32 v9, 7, v9
	v_and_b32_e32 v66, 0x6f80, v9
	v_mov_b32_e32 v67, v3
	v_lshl_add_u64 v[66:67], s[10:11], 0, v[66:67]
	v_lshl_add_u64 v[66:67], v[66:67], 0, v[2:3]
	global_store_dwordx4 v[66:67], v[62:65], off nt
	ds_read_b32 v9, v14 offset:128
	ds_read_b32 v62, v14 offset:388
	ds_read_b32 v63, v14 offset:648
	ds_read_b32 v64, v14 offset:908
	ds_read_b32 v65, v14 offset:1168
	ds_read_b32 v66, v14 offset:1428
	ds_read_b32 v67, v14 offset:1688
	ds_read_b32 v68, v14 offset:1948
	s_waitcnt lgkmcnt(0)
; #define LAS __attribute__((address_space(3)))
; __device__ __forceinline__ unsigned pk4_fp8(float a, float b, float c, float d) { int w = 0; w = __builtin_amdgcn_cvt_pk_fp8_f32(clamp8(a), clamp8(b), w, false); w = __builtin_amdgcn_cvt_pk_fp8_f32(clamp8(c), clamp8(d), w, true); return (unsigned)w; }
; #define LDS_WAIT() asm volatile("s_waitcnt lgkmcnt(0)" ::: "memory")
; __host__ __device__ __forceinline__ size_t tiled_off(size_t r, int kb, int ktiles) { return (((r >> 8) * ktiles + (kb >> 7)) << 15) + ((r & 255) << 7) + (kb & 127); }
;     ...
;     const int c = lane & 3;
; #pragma unroll
;     for (int j = 0; j < 4; ++j) { const int n = (lane >> 2) + 16 * j; const LAS float* s = scr + (16 * c) * 65 + n;
;         u32x4 o; o.x = pk4_fp8(s[0 * 65], s[1 * 65], s[2 * 65], s[3 * 65]); o.y = pk4_fp8(s[4 * 65], s[5 * 65], s[6 * 65], s[7 * 65]);
;         o.z = pk4_fp8(s[8 * 65], s[9 * 65], s[10 * 65], s[11 * 65]); o.w = pk4_fp8(s[12 * 65], s[13 * 65], s[14 * 65], s[15 * 65]);
;         const int nn = n0 + n; const int row = MAP == 0 ? nn : ((nn >> 7) * 256 + (nn & 127) + (MAP == 2 ? 128 : 0));
;         __builtin_nontemporal_store(o, (u32x4*)(WT + (pitch < 0 ? tiled_off((size_t)row, k0 + 16 * c, pitch == -1 ? (K >> 7) : -pitch) : (size_t)row * (pitch ? pitch : K) + k0 + 16 * c))); }
;     LDS_WAIT(); asm volatile("" ::: "memory");
; __device__ __forceinline__ void ph0(LAS unsigned char* lds, int tid, int lane, int wave, int G, int bid) {
;     ...
;         for (int it = gw; it < NITEMS; it += NGW) {
;             int r = NITEMS - 1 - it;
	v_med3_f32 v9, v9, s51, v57
	v_med3_f32 v69, v62, s51, v57
	v_mov_b32_e32 v62, v3
	v_cvt_pk_fp8_f32 v62, v9, v69
	v_med3_f32 v9, v63, s51, v57
	v_med3_f32 v65, v65, s51, v57
	v_med3_f32 v66, v66, s51, v57
	v_mov_b32_e32 v63, v3
	v_cvt_pk_fp8_f32 v63, v65, v66
	v_med3_f32 v64, v64, s51, v57
	v_cvt_pk_fp8_f32 v62, v9, v64 op_sel:[0,0,1]
	v_med3_f32 v9, v67, s51, v57
	v_med3_f32 v64, v68, s51, v57
	v_cvt_pk_fp8_f32 v63, v9, v64 op_sel:[0,0,1]
	ds_read_b32 v9, v14 offset:2208
	ds_read_b32 v64, v14 offset:2468
	ds_read_b32 v65, v14 offset:2728
	ds_read_b32 v66, v14 offset:2988
	ds_read_b32 v67, v14 offset:3248
	ds_read_b32 v68, v14 offset:3508
	ds_read_b32 v69, v14 offset:3768
	ds_read_b32 v70, v14 offset:4028
	s_waitcnt lgkmcnt(0)
	v_med3_f32 v9, v9, s51, v57
	v_med3_f32 v71, v64, s51, v57
	v_mov_b32_e32 v64, v3
	v_cvt_pk_fp8_f32 v64, v9, v71
	v_med3_f32 v9, v65, s51, v57
	v_med3_f32 v67, v67, s51, v57
	v_med3_f32 v68, v68, s51, v57
	v_mov_b32_e32 v65, v3
	v_cvt_pk_fp8_f32 v65, v67, v68
	v_med3_f32 v66, v66, s51, v57
	v_cvt_pk_fp8_f32 v64, v9, v66 op_sel:[0,0,1]
	v_med3_f32 v9, v69, s51, v57
	v_med3_f32 v66, v70, s51, v57
	v_cvt_pk_fp8_f32 v65, v9, v66 op_sel:[0,0,1]
	v_or_b32_e32 v9, s92, v16
	v_lshlrev_b32_e32 v9, 7, v9
	v_and_b32_e32 v66, 0x7780, v9
	v_mov_b32_e32 v67, v3
	v_lshl_add_u64 v[66:67], s[10:11], 0, v[66:67]
	v_lshl_add_u64 v[66:67], v[66:67], 0, v[2:3]
	global_store_dwordx4 v[66:67], v[62:65], off nt
	ds_read_b32 v9, v14 offset:192
	ds_read_b32 v62, v14 offset:452
	ds_read_b32 v63, v14 offset:712
	ds_read_b32 v64, v14 offset:972
	ds_read_b32 v65, v14 offset:1232
	ds_read_b32 v66, v14 offset:1492
	ds_read_b32 v67, v14 offset:1752
	ds_read_b32 v68, v14 offset:2012
	s_waitcnt lgkmcnt(0)
	v_med3_f32 v9, v9, s51, v57
	v_med3_f32 v69, v62, s51, v57
	v_mov_b32_e32 v62, v3
	v_cvt_pk_fp8_f32 v62, v9, v69
	v_med3_f32 v9, v63, s51, v57
	v_med3_f32 v65, v65, s51, v57
	v_med3_f32 v66, v66, s51, v57
	v_mov_b32_e32 v63, v3
	v_cvt_pk_fp8_f32 v63, v65, v66
	v_med3_f32 v64, v64, s51, v57
	v_cvt_pk_fp8_f32 v62, v9, v64 op_sel:[0,0,1]
	v_med3_f32 v9, v67, s51, v57
	v_med3_f32 v64, v68, s51, v57
	v_cvt_pk_fp8_f32 v63, v9, v64 op_sel:[0,0,1]
	ds_read_b32 v9, v14 offset:2272
	ds_read_b32 v64, v14 offset:2532
	ds_read_b32 v65, v14 offset:2792
	ds_read_b32 v66, v14 offset:3052
	ds_read_b32 v67, v14 offset:3312
	ds_read_b32 v68, v14 offset:3572
	ds_read_b32 v69, v14 offset:3832
	ds_read_b32 v70, v14 offset:4092
	s_waitcnt lgkmcnt(0)
	v_med3_f32 v9, v9, s51, v57
	v_med3_f32 v71, v64, s51, v57
	v_mov_b32_e32 v64, v3
	v_cvt_pk_fp8_f32 v64, v9, v71
	v_med3_f32 v9, v65, s51, v57
	v_med3_f32 v67, v67, s51, v57
	v_med3_f32 v68, v68, s51, v57
	v_mov_b32_e32 v65, v3
	v_cvt_pk_fp8_f32 v65, v67, v68
	v_med3_f32 v66, v66, s51, v57
	v_cvt_pk_fp8_f32 v64, v9, v66 op_sel:[0,0,1]
	v_med3_f32 v9, v69, s51, v57
	v_med3_f32 v66, v70, s51, v57
	v_cvt_pk_fp8_f32 v65, v9, v66 op_sel:[0,0,1]
	v_or_b32_e32 v9, s92, v17
	v_lshlrev_b32_e32 v9, 7, v9
	v_and_b32_e32 v66, 0x7f80, v9
	v_mov_b32_e32 v67, v3
	v_lshl_add_u64 v[66:67], s[10:11], 0, v[66:67]
	v_lshl_add_u64 v[66:67], v[66:67], 0, v[2:3]
	global_store_dwordx4 v[66:67], v[62:65], off nt
	s_waitcnt lgkmcnt(0)
	s_branch .LBB0_113
